# v14 + GEMM K-loops: first trip peeled with SrcC=0 (no accumulator zero-init) in the 8 non-gather GEMM instances
# speedup vs baseline: 1.0165x; 1.0063x over previous
.Lpeel_0:
	s_add_u32 s31, s26, 0xfffc0080
	s_addc_u32 s33, s27, -1
	s_add_i32 s34, 0, 0x10000
	v_add_u32_e32 v0, s34, v138
	ds_read_b128 v[140:143], v0
	ds_read_b128 v[144:147], v0 offset:1024
	ds_read_b128 v[148:151], v0 offset:2048
	ds_read_b128 v[152:155], v0 offset:3072
	s_cmp_eq_u32 s30, 12
	s_cselect_b32 s49, s3, s33
	s_cselect_b32 s48, s5, s31
	s_cselect_b32 s47, s20, s25
	s_cselect_b32 s46, s21, s22
	v_mov_b32_e32 v0, v136
	ds_read_b128 v[156:159], v139
	ds_read_b128 v[160:163], v139 offset:1024
	ds_read_b128 v[172:175], v139 offset:2048
	ds_read_b128 v[176:179], v139 offset:3072
	ds_read_b128 v[180:183], v139 offset:4096
	ds_read_b128 v[184:187], v139 offset:5120
	ds_read_b128 v[188:191], v139 offset:6144
	ds_read_b128 v[192:195], v139 offset:7168
	s_nop 0
	v_mov_b32_e32 v0, v137
	s_nop 0
	s_waitcnt lgkmcnt(8)
	s_barrier
	s_waitcnt lgkmcnt(0)
	s_setprio 1
	v_mov_b64_e32 v[50:51], v[164:165]
	s_waitcnt lgkmcnt(0)
	v_mfma_scale_f32_16x16x128_f8f6f4 v[98:101], v[156:163], v[148:155], 0, v202, v202 op_sel_hi:[0,0,0]
	v_mov_b64_e32 v[52:53], v[166:167]
	v_mfma_scale_f32_16x16x128_f8f6f4 v[164:167], v[172:179], v[140:147], 0, v202, v202 op_sel_hi:[0,0,0]
	s_add_i32 m0, s1, 0xc000
	v_mfma_scale_f32_16x16x128_f8f6f4 v[90:93], v[180:187], v[148:155], 0, v202, v202 op_sel_hi:[0,0,0]
	global_load_lds_dwordx4 v136, s[26:27]
	v_mfma_scale_f32_16x16x128_f8f6f4 v[130:133], v[156:163], v[140:147], 0, v202, v202 op_sel_hi:[0,0,0]
	v_mfma_scale_f32_16x16x128_f8f6f4 v[168:171], v[172:179], v[148:155], 0, v202, v202 op_sel_hi:[0,0,0]
	s_add_i32 m0, s1, 0xe000
	v_mfma_scale_f32_16x16x128_f8f6f4 v[196:199], v[180:187], v[140:147], 0, v202, v202 op_sel_hi:[0,0,0]
	global_load_lds_dwordx4 v137, s[26:27]
	v_mfma_scale_f32_16x16x128_f8f6f4 v[206:209], v[188:195], v[140:147], 0, v202, v202 op_sel_hi:[0,0,0]
	v_mfma_scale_f32_16x16x128_f8f6f4 v[210:213], v[188:195], v[148:155], 0, v202, v202 op_sel_hi:[0,0,0]
	s_setprio 0
	s_barrier
	s_add_i32 s31, 0, 0x14000
	v_add_u32_e32 v0, s31, v138
	s_nop 2
	ds_read_b128 v[82:85], v0
	ds_read_b128 v[86:89], v0 offset:1024
	ds_read_b128 v[114:117], v0 offset:2048
	ds_read_b128 v[118:121], v0 offset:3072
	v_mov_b32_e32 v0, v136
	s_add_i32 s33, s34, s73
	s_nop 0
	v_mov_b32_e32 v0, v137
	s_nop 0
	s_barrier
	s_waitcnt lgkmcnt(0)
	s_setprio 1
	s_waitcnt lgkmcnt(0)
	v_mfma_scale_f32_16x16x128_f8f6f4 v[66:69], v[156:163], v[82:89], 0, v202, v202 op_sel_hi:[0,0,0]
	v_mfma_scale_f32_16x16x128_f8f6f4 v[38:41], v[156:163], v[114:121], 0, v202, v202 op_sel_hi:[0,0,0]
	s_mov_b32 m0, s33
	v_mfma_scale_f32_16x16x128_f8f6f4 v[58:61], v[180:187], v[82:89], 0, v202, v202 op_sel_hi:[0,0,0]
	global_load_lds_dwordx4 v136, s[46:47]
	v_mfma_scale_f32_16x16x128_f8f6f4 v[214:217], v[172:179], v[82:89], 0, v202, v202 op_sel_hi:[0,0,0]
	v_mfma_scale_f32_16x16x128_f8f6f4 v[172:175], v[172:179], v[114:121], 0, v202, v202 op_sel_hi:[0,0,0]
	s_add_i32 m0, s33, 0x2000
	v_mfma_scale_f32_16x16x128_f8f6f4 v[176:179], v[180:187], v[114:121], 0, v202, v202 op_sel_hi:[0,0,0]
	global_load_lds_dwordx4 v137, s[46:47]
	v_mfma_scale_f32_16x16x128_f8f6f4 v[180:183], v[188:195], v[82:89], 0, v202, v202 op_sel_hi:[0,0,0]
	v_mfma_scale_f32_16x16x128_f8f6f4 v[184:187], v[188:195], v[114:121], 0, v202, v202 op_sel_hi:[0,0,0]
	s_setprio 0
	v_mov_b32_e32 v0, v136
	s_barrier
	s_nop 1
	ds_read_b128 v[18:21], v139 offset:16384
	ds_read_b128 v[22:25], v139 offset:17408
	ds_read_b128 v[50:53], v139 offset:18432
	ds_read_b128 v[54:57], v139 offset:19456
	ds_read_b128 v[122:125], v139 offset:20480
	ds_read_b128 v[126:129], v139 offset:21504
	ds_read_b128 v[156:159], v139 offset:22528
	ds_read_b128 v[160:163], v139 offset:23552
	s_nop 0
	v_mov_b32_e32 v0, v137
	s_nop 0
	s_barrier
	s_waitcnt lgkmcnt(0)
	s_setprio 1
	s_waitcnt lgkmcnt(0)
	v_mfma_scale_f32_16x16x128_f8f6f4 v[110:113], v[18:25], v[140:147], 0, v202, v202 op_sel_hi:[0,0,0]
	v_mfma_scale_f32_16x16x128_f8f6f4 v[78:81], v[18:25], v[148:155], 0, v202, v202 op_sel_hi:[0,0,0]
	s_mov_b32 m0, s1
	v_mfma_scale_f32_16x16x128_f8f6f4 v[102:105], v[50:57], v[140:147], 0, v202, v202 op_sel_hi:[0,0,0]
	global_load_lds_dwordx4 v136, s[48:49]
	v_mfma_scale_f32_16x16x128_f8f6f4 v[106:109], v[122:129], v[140:147], 0, v202, v202 op_sel_hi:[0,0,0]
	v_mfma_scale_f32_16x16x128_f8f6f4 v[94:97], v[156:163], v[140:147], 0, v202, v202 op_sel_hi:[0,0,0]
	s_mov_b32 m0, s13
	v_mfma_scale_f32_16x16x128_f8f6f4 v[62:65], v[156:163], v[148:155], 0, v202, v202 op_sel_hi:[0,0,0]
	global_load_lds_dwordx4 v137, s[48:49]
	v_mfma_scale_f32_16x16x128_f8f6f4 v[218:221], v[50:57], v[148:155], 0, v202, v202 op_sel_hi:[0,0,0]
	v_mfma_scale_f32_16x16x128_f8f6f4 v[222:225], v[122:129], v[148:155], 0, v202, v202 op_sel_hi:[0,0,0]
	s_setprio 0
	s_barrier
	s_add_u32 s34, s46, 0x40000
	s_addc_u32 s35, s47, 0
	v_mov_b32_e32 v0, v136
	s_add_i32 s31, s31, s73
	s_mov_b32 s100, s31
	s_nop 0
	v_mov_b32_e32 v0, v137
	s_add_i32 s101, s31, 0x2000
	s_nop 0
	s_waitcnt vmcnt(4)
	s_barrier
	s_setprio 1
	v_mfma_scale_f32_16x16x128_f8f6f4 v[34:37], v[50:57], v[82:89], 0, v202, v202 op_sel_hi:[0,0,0]
	v_mfma_scale_f32_16x16x128_f8f6f4 v[226:229], v[18:25], v[82:89], 0, v202, v202 op_sel_hi:[0,0,0]
	s_mov_b32 m0, s100
	v_mfma_scale_f32_16x16x128_f8f6f4 v[230:233], v[18:25], v[114:121], 0, v202, v202 op_sel_hi:[0,0,0]
	global_load_lds_dwordx4 v136, s[34:35]
	v_mfma_scale_f32_16x16x128_f8f6f4 v[234:237], v[50:57], v[114:121], 0, v202, v202 op_sel_hi:[0,0,0]
	v_mfma_scale_f32_16x16x128_f8f6f4 v[238:241], v[122:129], v[82:89], 0, v202, v202 op_sel_hi:[0,0,0]
	s_mov_b32 m0, s101
	v_mfma_scale_f32_16x16x128_f8f6f4 v[242:245], v[122:129], v[114:121], 0, v202, v202 op_sel_hi:[0,0,0]
	global_load_lds_dwordx4 v137, s[34:35]
	v_mfma_scale_f32_16x16x128_f8f6f4 v[246:249], v[156:163], v[82:89], 0, v202, v202 op_sel_hi:[0,0,0]
	v_mfma_scale_f32_16x16x128_f8f6f4 v[50:53], v[156:163], v[114:121], 0, v202, v202 op_sel_hi:[0,0,0]
	s_setprio 0
	s_add_i32 s31, 0, 0x18000
	v_add_u32_e32 v0, s31, v138
	s_barrier
	s_nop 2
	ds_read_b128 v[2:5], v0
	ds_read_b128 v[6:9], v0 offset:1024
	ds_read_b128 v[10:13], v0 offset:2048
	ds_read_b128 v[14:17], v0 offset:3072
	s_add_u32 s34, s48, 0x40000
	v_mov_b32_e32 v0, v136
	ds_read_b128 v[18:21], v139 offset:32768
	ds_read_b128 v[22:25], v139 offset:33792
	ds_read_b128 v[26:29], v139 offset:34816
	ds_read_b128 v[30:33], v139 offset:35840
	ds_read_b128 v[42:45], v139 offset:36864
	ds_read_b128 v[46:49], v139 offset:37888
	ds_read_b128 v[70:73], v139 offset:38912
	ds_read_b128 v[74:77], v139 offset:39936
	s_addc_u32 s35, s49, 0
	s_nop 0
	v_mov_b32_e32 v0, v137
	s_nop 0
	s_waitcnt lgkmcnt(8)
	s_barrier
	s_waitcnt lgkmcnt(0)
	s_setprio 1
	s_waitcnt lgkmcnt(0)
	v_mfma_scale_f32_16x16x128_f8f6f4 v[126:129], v[18:25], v[2:9], v[130:133], v202, v202 op_sel_hi:[0,0,0]
	v_mfma_scale_f32_16x16x128_f8f6f4 v[98:101], v[18:25], v[10:17], v[98:101], v202, v202 op_sel_hi:[0,0,0]
	s_mov_b32 m0, s14
	v_mfma_scale_f32_16x16x128_f8f6f4 v[118:121], v[26:33], v[2:9], v[164:167], v202, v202 op_sel_hi:[0,0,0]
	global_load_lds_dwordx4 v136, s[34:35]
	v_mfma_scale_f32_16x16x128_f8f6f4 v[86:89], v[26:33], v[10:17], v[168:171], v202, v202 op_sel_hi:[0,0,0]
	v_mfma_scale_f32_16x16x128_f8f6f4 v[122:125], v[42:49], v[2:9], v[196:199], v202, v202 op_sel_hi:[0,0,0]
	s_mov_b32 m0, s15
	v_mfma_scale_f32_16x16x128_f8f6f4 v[90:93], v[42:49], v[10:17], v[90:93], v202, v202 op_sel_hi:[0,0,0]
	global_load_lds_dwordx4 v137, s[34:35]
	v_mfma_scale_f32_16x16x128_f8f6f4 v[114:117], v[70:77], v[2:9], v[206:209], v202, v202 op_sel_hi:[0,0,0]
	v_mfma_scale_f32_16x16x128_f8f6f4 v[82:85], v[70:77], v[10:17], v[210:213], v202, v202 op_sel_hi:[0,0,0]
	s_setprio 0
	s_barrier
	s_add_i32 s33, 0, 0x1c000
	v_add_u32_e32 v0, s33, v138
	ds_read_b128 v[140:143], v0
	ds_read_b128 v[144:147], v0 offset:1024
	ds_read_b128 v[148:151], v0 offset:2048
	ds_read_b128 v[152:155], v0 offset:3072
	v_mov_b32_e32 v0, v136
	s_add_i32 s31, s31, s73
	v_lshl_add_u64 v[54:55], s[46:47], 0, v[0:1]
	v_lshl_add_u64 v[54:55], v[54:55], 0, s[66:67]
	v_mov_b32_e32 v0, v137
	v_lshl_add_u64 v[54:55], s[46:47], 0, v[0:1]
	v_lshl_add_u64 v[54:55], v[54:55], 0, s[66:67]
	s_barrier
	s_waitcnt lgkmcnt(0)
	s_setprio 1
	s_waitcnt lgkmcnt(0)
	v_mfma_scale_f32_16x16x128_f8f6f4 v[66:69], v[18:25], v[140:147], v[66:69], v202, v202 op_sel_hi:[0,0,0]
	v_mfma_scale_f32_16x16x128_f8f6f4 v[38:41], v[18:25], v[148:155], v[38:41], v202, v202 op_sel_hi:[0,0,0]
	s_add_u32 s98, s46, s66
	s_addc_u32 s99, s47, s67
	s_mov_b32 m0, s31
	v_mfma_scale_f32_16x16x128_f8f6f4 v[54:57], v[26:33], v[140:147], v[214:217], v202, v202 op_sel_hi:[0,0,0]
	global_load_lds_dwordx4 v136, s[98:99]
	v_mfma_scale_f32_16x16x128_f8f6f4 v[22:25], v[26:33], v[148:155], v[172:175], v202, v202 op_sel_hi:[0,0,0]
	v_mfma_scale_f32_16x16x128_f8f6f4 v[58:61], v[42:49], v[140:147], v[58:61], v202, v202 op_sel_hi:[0,0,0]
	s_add_i32 m0, s31, 0x2000
	v_mfma_scale_f32_16x16x128_f8f6f4 v[30:33], v[42:49], v[148:155], v[176:179], v202, v202 op_sel_hi:[0,0,0]
	global_load_lds_dwordx4 v137, s[98:99]
	v_mfma_scale_f32_16x16x128_f8f6f4 v[18:21], v[70:77], v[140:147], v[180:183], v202, v202 op_sel_hi:[0,0,0]
	v_mfma_scale_f32_16x16x128_f8f6f4 v[164:167], v[70:77], v[148:155], v[184:187], v202, v202 op_sel_hi:[0,0,0]
	s_setprio 0
	v_mov_b32_e32 v0, v136
	s_barrier
	ds_read_b128 v[156:159], v139 offset:49152
	ds_read_b128 v[160:163], v139 offset:50176
	ds_read_b128 v[172:175], v139 offset:51200
	ds_read_b128 v[176:179], v139 offset:52224
	ds_read_b128 v[180:183], v139 offset:53248
	ds_read_b128 v[184:187], v139 offset:54272
	ds_read_b128 v[188:191], v139 offset:55296
	ds_read_b128 v[192:195], v139 offset:56320
	v_lshl_add_u64 v[26:27], s[48:49], 0, v[0:1]
	v_lshl_add_u64 v[26:27], v[26:27], 0, s[66:67]
	v_mov_b32_e32 v0, v137
	v_lshl_add_u64 v[26:27], s[48:49], 0, v[0:1]
	v_lshl_add_u64 v[26:27], v[26:27], 0, s[66:67]
	s_barrier
	s_waitcnt lgkmcnt(0)
	s_setprio 1
	s_waitcnt lgkmcnt(0)
	v_mfma_scale_f32_16x16x128_f8f6f4 v[110:113], v[156:163], v[2:9], v[110:113], v202, v202 op_sel_hi:[0,0,0]
	v_mfma_scale_f32_16x16x128_f8f6f4 v[78:81], v[156:163], v[10:17], v[78:81], v202, v202 op_sel_hi:[0,0,0]
	s_add_u32 s98, s48, s66
	s_addc_u32 s99, s49, s67
	s_mov_b32 m0, s17
	v_mfma_scale_f32_16x16x128_f8f6f4 v[102:105], v[172:179], v[2:9], v[102:105], v202, v202 op_sel_hi:[0,0,0]
	global_load_lds_dwordx4 v136, s[98:99]
	v_mfma_scale_f32_16x16x128_f8f6f4 v[70:73], v[172:179], v[10:17], v[218:221], v202, v202 op_sel_hi:[0,0,0]
	v_mfma_scale_f32_16x16x128_f8f6f4 v[106:109], v[180:187], v[2:9], v[106:109], v202, v202 op_sel_hi:[0,0,0]
	s_mov_b32 m0, s18
	v_mfma_scale_f32_16x16x128_f8f6f4 v[74:77], v[180:187], v[10:17], v[222:225], v202, v202 op_sel_hi:[0,0,0]
	global_load_lds_dwordx4 v137, s[98:99]
	v_mfma_scale_f32_16x16x128_f8f6f4 v[94:97], v[188:195], v[2:9], v[94:97], v202, v202 op_sel_hi:[0,0,0]
	v_mfma_scale_f32_16x16x128_f8f6f4 v[62:65], v[188:195], v[10:17], v[62:65], v202, v202 op_sel_hi:[0,0,0]
	s_setprio 0
	s_barrier
	s_add_u32 s34, s46, 0x40080
	s_addc_u32 s35, s47, 0
	v_mov_b32_e32 v0, v136
	s_add_i32 s31, s33, s73
	s_nop 0
	v_mov_b32_e32 v0, v137
	s_nop 0
	s_waitcnt vmcnt(4)
	s_barrier
	s_setprio 1
	v_mfma_scale_f32_16x16x128_f8f6f4 v[46:49], v[156:163], v[140:147], v[226:229], v202, v202 op_sel_hi:[0,0,0]
	v_mfma_scale_f32_16x16x128_f8f6f4 v[14:17], v[156:163], v[148:155], v[230:233], v202, v202 op_sel_hi:[0,0,0]
	s_mov_b32 m0, s31
	v_mfma_scale_f32_16x16x128_f8f6f4 v[34:37], v[172:179], v[140:147], v[34:37], v202, v202 op_sel_hi:[0,0,0]
	global_load_lds_dwordx4 v136, s[34:35]
	v_mfma_scale_f32_16x16x128_f8f6f4 v[6:9], v[172:179], v[148:155], v[234:237], v202, v202 op_sel_hi:[0,0,0]
	v_mfma_scale_f32_16x16x128_f8f6f4 v[42:45], v[180:187], v[140:147], v[238:241], v202, v202 op_sel_hi:[0,0,0]
	s_add_i32 m0, s31, 0x2000
	v_mfma_scale_f32_16x16x128_f8f6f4 v[10:13], v[180:187], v[148:155], v[242:245], v202, v202 op_sel_hi:[0,0,0]
	global_load_lds_dwordx4 v137, s[34:35]
	v_mfma_scale_f32_16x16x128_f8f6f4 v[26:29], v[188:195], v[140:147], v[246:249], v202, v202 op_sel_hi:[0,0,0]
	v_mfma_scale_f32_16x16x128_f8f6f4 v[2:5], v[188:195], v[148:155], v[50:53], v202, v202 op_sel_hi:[0,0,0]
	s_setprio 0
	s_add_i32 s30, s30, 2
	s_add_u32 s26, s26, 0x100
	s_addc_u32 s27, s27, 0
	s_add_u32 s22, s22, 0x100
	s_addc_u32 s25, s25, 0
	s_cmp_gt_u32 s30, 13
	s_barrier
	s_cbranch_scc0 .LBB0_249
	s_branch .Lpeel_exit_0

.Lpeel_exit_0:
	s_mul_hi_i32 s3, s24, 0x2aaaaaab
	s_lshr_b32 s5, s3, 31
	s_lshr_b32 s3, s3, 1
	s_add_i32 s3, s3, s5
	s_lshl_b32 s5, s24, 1
	s_and_b32 s5, s5, 6
	s_and_b32 s20, s12, -16
	s_lshl_b32 s3, s3, 3
	s_or_b32 s5, s5, s20
	s_add_i32 s24, s5, s3
	v_readlane_b32 s3, v252, 41
	v_mbcnt_lo_u32_b32 v0, -1, 0
	v_mbcnt_hi_u32_b32 v0, -1, v0
	s_ashr_i32 s25, s24, 31
	s_lshl_b64 s[20:21], s[24:25], 19
	v_and_or_b32 v51, v0, 15, s3
	s_lshl_b32 s3, s12, 8
	s_and_b32 s22, s3, 0xf00
	v_ashrrev_i32_e32 v50, 4, v0
	s_add_u32 s20, s87, s20
	v_readlane_b32 s3, v252, 59
	v_lshlrev_b32_e32 v0, 5, v50
	v_lshlrev_b32_e32 v50, 3, v50
	v_lshlrev_b32_e32 v132, 12, v51
	v_mov_b32_e32 v133, v1
	s_addc_u32 s21, s3, s21
	v_and_b32_e32 v130, -16, v50
	v_lshl_add_u64 v[50:51], s[20:21], 0, v[132:133]
	v_lshl_add_u64 v[50:51], v[50:51], 0, s[22:23]
	v_and_b32_e32 v0, 32, v0
	v_lshl_add_u64 v[50:51], v[50:51], 0, s[28:29]
	v_pk_mul_f32 v[52:53], v[126:127], s[68:69] op_sel_hi:[1,0]
	v_mov_b32_e32 v126, v1
	v_ashrrev_i32_e32 v131, 31, v130
	v_lshl_add_u64 v[50:51], v[50:51], 0, v[0:1]
	v_cvt_pk_fp8_f32 v126, v52, v53
	v_pk_mul_f32 v[52:53], v[122:123], s[68:69] op_sel_hi:[1,0]
	v_mov_b32_e32 v127, v1
	v_lshl_add_u64 v[134:135], v[50:51], 0, v[130:131]
	v_pk_mul_f32 v[50:51], v[128:129], s[68:69] op_sel_hi:[1,0]
	v_cvt_pk_fp8_f32 v127, v52, v53
	v_pk_mul_f32 v[52:53], v[118:119], s[68:69] op_sel_hi:[1,0]
	v_mov_b32_e32 v128, v1
	v_cvt_pk_fp8_f32 v128, v52, v53
	v_pk_mul_f32 v[52:53], v[114:115], s[68:69] op_sel_hi:[1,0]
	v_mov_b32_e32 v129, v1
	v_cvt_pk_fp8_f32 v129, v52, v53
	v_cvt_pk_fp8_f32 v126, v50, v51 op_sel:[0,0,1]
	v_pk_mul_f32 v[50:51], v[124:125], s[68:69] op_sel_hi:[1,0]
	v_pk_mul_f32 v[52:53], v[110:111], s[68:69] op_sel_hi:[1,0]
	v_cvt_pk_fp8_f32 v127, v50, v51 op_sel:[0,0,1]
	v_pk_mul_f32 v[50:51], v[120:121], s[68:69] op_sel_hi:[1,0]
	v_mov_b32_e32 v110, v1
	v_cvt_pk_fp8_f32 v128, v50, v51 op_sel:[0,0,1]
	v_pk_mul_f32 v[50:51], v[116:117], s[68:69] op_sel_hi:[1,0]
	v_cvt_pk_fp8_f32 v110, v52, v53
	v_pk_mul_f32 v[52:53], v[106:107], s[68:69] op_sel_hi:[1,0]
	v_mov_b32_e32 v111, v1
	v_cvt_pk_fp8_f32 v129, v50, v51 op_sel:[0,0,1]
	v_pk_mul_f32 v[50:51], v[112:113], s[68:69] op_sel_hi:[1,0]
	v_cvt_pk_fp8_f32 v111, v52, v53
	v_pk_mul_f32 v[52:53], v[102:103], s[68:69] op_sel_hi:[1,0]
	v_mov_b32_e32 v112, v1
	v_cvt_pk_fp8_f32 v112, v52, v53
	v_cvt_pk_fp8_f32 v110, v50, v51 op_sel:[0,0,1]
	v_pk_mul_f32 v[50:51], v[108:109], s[68:69] op_sel_hi:[1,0]
	v_pk_mul_f32 v[52:53], v[94:95], s[68:69] op_sel_hi:[1,0]
	v_cvt_pk_fp8_f32 v111, v50, v51 op_sel:[0,0,1]
	v_pk_mul_f32 v[50:51], v[104:105], s[68:69] op_sel_hi:[1,0]
	v_mov_b32_e32 v94, v1
	v_cvt_pk_fp8_f32 v112, v50, v51 op_sel:[0,0,1]
	v_pk_mul_f32 v[50:51], v[96:97], s[68:69] op_sel_hi:[1,0]
	v_pk_mul_f32 v[96:97], v[98:99], s[68:69] op_sel_hi:[1,0]
	v_pk_mul_f32 v[90:91], v[90:91], s[68:69] op_sel_hi:[1,0]
	v_cvt_pk_fp8_f32 v94, v96, v97
	v_mov_b32_e32 v95, v1
	v_cvt_pk_fp8_f32 v95, v90, v91
	v_pk_mul_f32 v[86:87], v[86:87], s[68:69] op_sel_hi:[1,0]
	v_mov_b32_e32 v96, v1
	v_mov_b32_e32 v113, v1
	v_cvt_pk_fp8_f32 v96, v86, v87
	v_pk_mul_f32 v[82:83], v[82:83], s[68:69] op_sel_hi:[1,0]
	v_mov_b32_e32 v97, v1
	v_cvt_pk_fp8_f32 v113, v52, v53
	v_pk_mul_f32 v[52:53], v[100:101], s[68:69] op_sel_hi:[1,0]
	v_cvt_pk_fp8_f32 v97, v82, v83
	v_cvt_pk_fp8_f32 v94, v52, v53 op_sel:[0,0,1]
	v_pk_mul_f32 v[52:53], v[92:93], s[68:69] op_sel_hi:[1,0]
	s_mov_b32 s5, 0x10000
	v_cvt_pk_fp8_f32 v95, v52, v53 op_sel:[0,0,1]
	v_pk_mul_f32 v[52:53], v[88:89], s[68:69] op_sel_hi:[1,0]
	v_pk_mul_f32 v[74:75], v[74:75], s[68:69] op_sel_hi:[1,0]
	v_cvt_pk_fp8_f32 v96, v52, v53 op_sel:[0,0,1]
	v_pk_mul_f32 v[52:53], v[84:85], s[68:69] op_sel_hi:[1,0]
	v_permlane32_swap_b32_e32 v94, v95
	v_cvt_pk_fp8_f32 v97, v52, v53 op_sel:[0,0,1]
	v_add_co_u32_e32 v52, vcc, s5, v134
	v_pk_mul_f32 v[70:71], v[70:71], s[68:69] op_sel_hi:[1,0]
	v_permlane32_swap_b32_e32 v96, v97
	v_addc_co_u32_e32 v53, vcc, 0, v135, vcc
	global_store_dwordx4 v[52:53], v[94:97], off
	v_pk_mul_f32 v[52:53], v[80:81], s[68:69] op_sel_hi:[1,0]
	v_pk_mul_f32 v[80:81], v[78:79], s[68:69] op_sel_hi:[1,0]
	v_mov_b32_e32 v78, v1
	v_cvt_pk_fp8_f32 v78, v80, v81
	v_mov_b32_e32 v79, v1
	v_cvt_pk_fp8_f32 v79, v74, v75
	v_mov_b32_e32 v80, v1
	v_cvt_pk_fp8_f32 v80, v70, v71
	v_pk_mul_f32 v[62:63], v[62:63], s[68:69] op_sel_hi:[1,0]
	v_mov_b32_e32 v81, v1
	v_cvt_pk_fp8_f32 v81, v62, v63
	v_cvt_pk_fp8_f32 v78, v52, v53 op_sel:[0,0,1]
	v_pk_mul_f32 v[52:53], v[76:77], s[68:69] op_sel_hi:[1,0]
	v_pk_mul_f32 v[18:19], v[18:19], s[68:69] op_sel_hi:[1,0]
	v_cvt_pk_fp8_f32 v79, v52, v53 op_sel:[0,0,1]
	v_pk_mul_f32 v[52:53], v[72:73], s[68:69] op_sel_hi:[1,0]
	v_pk_mul_f32 v[20:21], v[20:21], s[68:69] op_sel_hi:[1,0]
	v_cvt_pk_fp8_f32 v80, v52, v53 op_sel:[0,0,1]
	v_pk_mul_f32 v[52:53], v[64:65], s[68:69] op_sel_hi:[1,0]
	s_or_b32 s20, s24, 1
	v_cvt_pk_fp8_f32 v81, v52, v53 op_sel:[0,0,1]
	v_pk_mul_f32 v[52:53], v[66:67], s[68:69] op_sel_hi:[1,0]
	v_mov_b32_e32 v67, v1
	v_cvt_pk_fp8_f32 v67, v18, v19
	v_pk_mul_f32 v[18:19], v[48:49], s[68:69] op_sel_hi:[1,0]
	v_mov_b32_e32 v48, v1
	s_ashr_i32 s21, s20, 31
	v_cvt_pk_fp8_f32 v67, v20, v21 op_sel:[0,0,1]
	v_pk_mul_f32 v[20:21], v[46:47], s[68:69] op_sel_hi:[1,0]
	v_mov_b32_e32 v46, v1
	v_cvt_pk_fp8_f32 v46, v20, v21
	v_pk_mul_f32 v[20:21], v[42:43], s[68:69] op_sel_hi:[1,0]
	v_mov_b32_e32 v47, v1
	v_cvt_pk_fp8_f32 v47, v20, v21
	v_pk_mul_f32 v[20:21], v[34:35], s[68:69] op_sel_hi:[1,0]
	v_cvt_pk_fp8_f32 v46, v18, v19 op_sel:[0,0,1]
	v_cvt_pk_fp8_f32 v48, v20, v21
	v_pk_mul_f32 v[18:19], v[44:45], s[68:69] op_sel_hi:[1,0]
	v_pk_mul_f32 v[20:21], v[26:27], s[68:69] op_sel_hi:[1,0]
	v_cvt_pk_fp8_f32 v47, v18, v19 op_sel:[0,0,1]
	v_pk_mul_f32 v[18:19], v[36:37], s[68:69] op_sel_hi:[1,0]
	v_mov_b32_e32 v26, v1
	v_cvt_pk_fp8_f32 v48, v18, v19 op_sel:[0,0,1]
	v_pk_mul_f32 v[18:19], v[28:29], s[68:69] op_sel_hi:[1,0]
	v_pk_mul_f32 v[28:29], v[38:39], s[68:69] op_sel_hi:[1,0]
	v_mov_b32_e32 v27, v1
	v_cvt_pk_fp8_f32 v26, v28, v29
	v_pk_mul_f32 v[28:29], v[30:31], s[68:69] op_sel_hi:[1,0]
	v_pk_mul_f32 v[22:23], v[22:23], s[68:69] op_sel_hi:[1,0]
	v_cvt_pk_fp8_f32 v27, v28, v29
	v_mov_b32_e32 v28, v1
	s_lshl_b64 s[20:21], s[20:21], 19
	v_mov_b32_e32 v49, v1
	v_cvt_pk_fp8_f32 v28, v22, v23
	v_pk_mul_f32 v[22:23], v[164:165], s[68:69] op_sel_hi:[1,0]
	v_mov_b32_e32 v29, v1
	s_mov_b64 s[26:27], 0x10000
	s_add_u32 s20, s87, s20
	v_cvt_pk_fp8_f32 v49, v20, v21
	v_pk_mul_f32 v[20:21], v[40:41], s[68:69] op_sel_hi:[1,0]
	v_cvt_pk_fp8_f32 v29, v22, v23
	v_cvt_pk_fp8_f32 v113, v50, v51 op_sel:[0,0,1]
	v_lshl_add_u64 v[50:51], v[134:135], 0, s[26:27]
	v_permlane32_swap_b32_e32 v78, v79
	v_permlane32_swap_b32_e32 v80, v81
	s_addc_u32 s21, s3, s21
	v_cvt_pk_fp8_f32 v26, v20, v21 op_sel:[0,0,1]
	v_pk_mul_f32 v[20:21], v[32:33], s[68:69] op_sel_hi:[1,0]
	global_store_dwordx4 v[50:51], v[78:81], off offset:128
	v_lshl_add_u64 v[50:51], s[20:21], 0, v[132:133]
	v_cvt_pk_fp8_f32 v27, v20, v21 op_sel:[0,0,1]
	v_pk_mul_f32 v[20:21], v[24:25], s[68:69] op_sel_hi:[1,0]
	v_lshl_add_u64 v[50:51], v[50:51], 0, s[22:23]
	v_cvt_pk_fp8_f32 v28, v20, v21 op_sel:[0,0,1]
	v_pk_mul_f32 v[20:21], v[166:167], s[68:69] op_sel_hi:[1,0]
	v_lshl_add_u64 v[50:51], v[50:51], 0, s[28:29]
	v_cvt_pk_fp8_f32 v29, v20, v21 op_sel:[0,0,1]
	v_lshl_add_u64 v[50:51], v[50:51], 0, v[0:1]
	v_lshl_add_u64 v[62:63], v[50:51], 0, v[130:131]
	v_add_co_u32_e32 v20, vcc, s5, v62
	v_permlane32_swap_b32_e32 v26, v27
	v_permlane32_swap_b32_e32 v28, v29
	v_addc_co_u32_e32 v21, vcc, 0, v63, vcc
	global_store_dwordx4 v[20:21], v[26:29], off
	v_pk_mul_f32 v[20:21], v[14:15], s[68:69] op_sel_hi:[1,0]
	v_mov_b32_e32 v14, v1
	v_cvt_pk_fp8_f32 v14, v20, v21
	v_mov_b32_e32 v64, v1
	v_cvt_pk_fp8_f32 v64, v52, v53
	v_pk_mul_f32 v[52:53], v[58:59], s[68:69] op_sel_hi:[1,0]
	v_mov_b32_e32 v65, v1
	v_pk_mul_f32 v[16:17], v[16:17], s[68:69] op_sel_hi:[1,0]
	v_cvt_pk_fp8_f32 v65, v52, v53
	v_pk_mul_f32 v[52:53], v[54:55], s[68:69] op_sel_hi:[1,0]
	v_mov_b32_e32 v66, v1
	v_cvt_pk_fp8_f32 v14, v16, v17 op_sel:[0,0,1]
	v_pk_mul_f32 v[10:11], v[10:11], s[68:69] op_sel_hi:[1,0]
	v_mov_b32_e32 v15, v1
	v_pk_mul_f32 v[6:7], v[6:7], s[68:69] op_sel_hi:[1,0]
	v_mov_b32_e32 v16, v1
	v_pk_mul_f32 v[2:3], v[2:3], s[68:69] op_sel_hi:[1,0]
	v_mov_b32_e32 v17, v1
	v_cvt_pk_fp8_f32 v66, v52, v53
	v_cvt_pk_fp8_f32 v15, v10, v11
	v_cvt_pk_fp8_f32 v16, v6, v7
	v_cvt_pk_fp8_f32 v17, v2, v3
	v_pk_mul_f32 v[50:51], v[68:69], s[68:69] op_sel_hi:[1,0]
	v_pk_mul_f32 v[12:13], v[12:13], s[68:69] op_sel_hi:[1,0]
	v_cvt_pk_fp8_f32 v64, v50, v51 op_sel:[0,0,1]
	v_pk_mul_f32 v[50:51], v[60:61], s[68:69] op_sel_hi:[1,0]
	v_pk_mul_f32 v[8:9], v[8:9], s[68:69] op_sel_hi:[1,0]
	v_cvt_pk_fp8_f32 v65, v50, v51 op_sel:[0,0,1]
	v_pk_mul_f32 v[50:51], v[56:57], s[68:69] op_sel_hi:[1,0]
	v_pk_mul_f32 v[4:5], v[4:5], s[68:69] op_sel_hi:[1,0]
	v_cvt_pk_fp8_f32 v66, v50, v51 op_sel:[0,0,1]
	v_cvt_pk_fp8_f32 v49, v18, v19 op_sel:[0,0,1]
	v_cvt_pk_fp8_f32 v15, v12, v13 op_sel:[0,0,1]
	v_cvt_pk_fp8_f32 v16, v8, v9 op_sel:[0,0,1]
	v_cvt_pk_fp8_f32 v17, v4, v5 op_sel:[0,0,1]
	v_permlane32_swap_b32_e32 v126, v127
	v_permlane32_swap_b32_e32 v128, v129
	v_permlane32_swap_b32_e32 v110, v111
	v_permlane32_swap_b32_e32 v112, v113
	v_permlane32_swap_b32_e32 v64, v65
	v_permlane32_swap_b32_e32 v66, v67
	v_permlane32_swap_b32_e32 v46, v47
	v_permlane32_swap_b32_e32 v48, v49
	v_lshl_add_u64 v[18:19], v[62:63], 0, s[26:27]
	v_permlane32_swap_b32_e32 v14, v15
	v_permlane32_swap_b32_e32 v16, v17
	s_and_b64 vcc, exec, s[10:11]
	s_mov_b32 s12, s2
	s_mov_b32 s24, s4
	s_mov_b64 s[46:47], s[8:9]
	s_mov_b64 s[26:27], s[6:7]
	global_store_dwordx4 v[134:135], v[126:129], off
	global_store_dwordx4 v[134:135], v[110:113], off offset:128
	global_store_dwordx4 v[62:63], v[64:67], off
	global_store_dwordx4 v[62:63], v[46:49], off offset:128
	global_store_dwordx4 v[18:19], v[14:17], off offset:128
	s_cbranch_vccz .LBB0_241
	v_readlane_b32 s0, v252, 50
	s_waitcnt vmcnt(0)
	v_readlane_b32 s1, v252, 51
	s_andn2_b64 vcc, exec, s[0:1]
	s_cbranch_vccnz .LBB0_253
	s_barrier

.Lpeel_1:
	s_add_u32 s6, s4, 0xfffc0080
	s_addc_u32 s7, s5, -1
	s_add_i32 s25, 0, 0x10000
	v_add_u32_e32 v0, s25, v207
	ds_read_b128 v[52:55], v0
	ds_read_b128 v[56:59], v0 offset:1024
	ds_read_b128 v[68:71], v0 offset:2048
	ds_read_b128 v[72:75], v0 offset:3072
	s_cmp_eq_u32 s17, 12
	s_cselect_b32 s11, s3, s7
	s_cselect_b32 s10, s9, s6
	s_cselect_b32 s7, s12, s16
	s_cselect_b32 s6, s13, s15
	v_mov_b32_e32 v0, v205
	ds_read_b128 v[84:87], v208
	ds_read_b128 v[88:91], v208 offset:1024
	ds_read_b128 v[92:95], v208 offset:2048
	ds_read_b128 v[96:99], v208 offset:3072
	ds_read_b128 v[172:175], v208 offset:4096
	ds_read_b128 v[176:179], v208 offset:5120
	ds_read_b128 v[180:183], v208 offset:6144
	ds_read_b128 v[184:187], v208 offset:7168
	s_nop 0
	v_mov_b32_e32 v0, v206
	s_nop 0
	s_waitcnt lgkmcnt(8)
	s_barrier
	s_waitcnt lgkmcnt(0)
	s_setprio 1
	s_waitcnt lgkmcnt(0)
	v_mfma_scale_f32_16x16x128_f8f6f4 v[164:167], v[52:59], v[84:91], 0, v202, v202 op_sel_hi:[0,0,0]
	v_mfma_scale_f32_16x16x128_f8f6f4 v[160:163], v[68:75], v[84:91], 0, v202, v202 op_sel_hi:[0,0,0]
	s_add_i32 m0, s18, 0xc000
	v_mfma_scale_f32_16x16x128_f8f6f4 v[156:159], v[52:59], v[92:99], 0, v202, v202 op_sel_hi:[0,0,0]
	global_load_lds_dwordx4 v205, s[4:5]
	v_mfma_scale_f32_16x16x128_f8f6f4 v[152:155], v[68:75], v[92:99], 0, v202, v202 op_sel_hi:[0,0,0]
	v_mfma_scale_f32_16x16x128_f8f6f4 v[148:151], v[52:59], v[172:179], 0, v202, v202 op_sel_hi:[0,0,0]
	s_add_i32 m0, s18, 0xe000
	v_mfma_scale_f32_16x16x128_f8f6f4 v[188:191], v[68:75], v[172:179], 0, v202, v202 op_sel_hi:[0,0,0]
	global_load_lds_dwordx4 v206, s[4:5]
	v_mfma_scale_f32_16x16x128_f8f6f4 v[192:195], v[52:59], v[180:187], 0, v202, v202 op_sel_hi:[0,0,0]
	v_mfma_scale_f32_16x16x128_f8f6f4 v[196:199], v[68:75], v[180:187], 0, v202, v202 op_sel_hi:[0,0,0]
	s_setprio 0
	s_barrier
	s_add_i32 s30, 0, 0x14000
	v_add_u32_e32 v0, s30, v207
	s_nop 2
	ds_read_b128 v[132:135], v0
	ds_read_b128 v[136:139], v0 offset:1024
	ds_read_b128 v[140:143], v0 offset:2048
	ds_read_b128 v[144:147], v0 offset:3072
	v_mov_b32_e32 v0, v205
	s_add_i32 s25, s25, s73
	s_nop 0
	v_mov_b32_e32 v0, v206
	s_nop 0
	s_barrier
	s_waitcnt lgkmcnt(0)
	s_setprio 1
	s_waitcnt lgkmcnt(0)
	v_mfma_scale_f32_16x16x128_f8f6f4 v[128:131], v[132:139], v[84:91], 0, v202, v202 op_sel_hi:[0,0,0]
	v_mfma_scale_f32_16x16x128_f8f6f4 v[124:127], v[140:147], v[84:91], 0, v202, v202 op_sel_hi:[0,0,0]
	s_mov_b32 m0, s25
	v_mfma_scale_f32_16x16x128_f8f6f4 v[120:123], v[132:139], v[92:99], 0, v202, v202 op_sel_hi:[0,0,0]
	global_load_lds_dwordx4 v205, s[6:7]
	v_mfma_scale_f32_16x16x128_f8f6f4 v[116:119], v[140:147], v[92:99], 0, v202, v202 op_sel_hi:[0,0,0]
	v_mfma_scale_f32_16x16x128_f8f6f4 v[210:213], v[132:139], v[172:179], 0, v202, v202 op_sel_hi:[0,0,0]
	s_add_i32 m0, s25, 0x2000
	v_mfma_scale_f32_16x16x128_f8f6f4 v[172:175], v[140:147], v[172:179], 0, v202, v202 op_sel_hi:[0,0,0]
	global_load_lds_dwordx4 v206, s[6:7]
	v_mfma_scale_f32_16x16x128_f8f6f4 v[176:179], v[132:139], v[180:187], 0, v202, v202 op_sel_hi:[0,0,0]
	v_mfma_scale_f32_16x16x128_f8f6f4 v[180:183], v[140:147], v[180:187], 0, v202, v202 op_sel_hi:[0,0,0]
	s_setprio 0
	v_mov_b32_e32 v0, v205
	s_barrier
	ds_read_b128 v[84:87], v208 offset:16384
	ds_read_b128 v[88:91], v208 offset:17408
	ds_read_b128 v[92:95], v208 offset:18432
	ds_read_b128 v[96:99], v208 offset:19456
	ds_read_b128 v[100:103], v208 offset:20480
	ds_read_b128 v[104:107], v208 offset:21504
	ds_read_b128 v[108:111], v208 offset:22528
	ds_read_b128 v[112:115], v208 offset:23552
	s_nop 0
	v_mov_b32_e32 v0, v206
	s_nop 0
	s_barrier
	s_waitcnt lgkmcnt(0)
	s_setprio 1
	s_waitcnt lgkmcnt(0)
	v_mfma_scale_f32_16x16x128_f8f6f4 v[80:83], v[52:59], v[84:91], 0, v202, v202 op_sel_hi:[0,0,0]
	v_mfma_scale_f32_16x16x128_f8f6f4 v[76:79], v[68:75], v[84:91], 0, v202, v202 op_sel_hi:[0,0,0]
	s_mov_b32 m0, s18
	v_mfma_scale_f32_16x16x128_f8f6f4 v[64:67], v[52:59], v[92:99], 0, v202, v202 op_sel_hi:[0,0,0]
	global_load_lds_dwordx4 v205, s[10:11]
	v_mfma_scale_f32_16x16x128_f8f6f4 v[60:63], v[68:75], v[92:99], 0, v202, v202 op_sel_hi:[0,0,0]
	v_mfma_scale_f32_16x16x128_f8f6f4 v[184:187], v[52:59], v[100:107], 0, v202, v202 op_sel_hi:[0,0,0]
	s_mov_b32 m0, s19
	v_mfma_scale_f32_16x16x128_f8f6f4 v[214:217], v[68:75], v[100:107], 0, v202, v202 op_sel_hi:[0,0,0]
	global_load_lds_dwordx4 v206, s[10:11]
	v_mfma_scale_f32_16x16x128_f8f6f4 v[218:221], v[52:59], v[108:115], 0, v202, v202 op_sel_hi:[0,0,0]
	v_mfma_scale_f32_16x16x128_f8f6f4 v[222:225], v[68:75], v[108:115], 0, v202, v202 op_sel_hi:[0,0,0]
	s_setprio 0
	s_barrier
	s_add_u32 s26, s6, 0x40000
	s_addc_u32 s27, s7, 0
	v_mov_b32_e32 v0, v205
	s_add_i32 s25, s30, s73
	s_mov_b32 s100, s25
	s_nop 0
	v_mov_b32_e32 v0, v206
	s_add_i32 s101, s25, 0x2000
	s_nop 0
	s_waitcnt vmcnt(4)
	s_barrier
	s_setprio 1
	v_mfma_scale_f32_16x16x128_f8f6f4 v[226:229], v[132:139], v[84:91], 0, v202, v202 op_sel_hi:[0,0,0]
	v_mfma_scale_f32_16x16x128_f8f6f4 v[230:233], v[140:147], v[84:91], 0, v202, v202 op_sel_hi:[0,0,0]
	s_mov_b32 m0, s100
	v_mfma_scale_f32_16x16x128_f8f6f4 v[234:237], v[132:139], v[92:99], 0, v202, v202 op_sel_hi:[0,0,0]
	global_load_lds_dwordx4 v205, s[26:27]
	v_mfma_scale_f32_16x16x128_f8f6f4 v[238:241], v[140:147], v[92:99], 0, v202, v202 op_sel_hi:[0,0,0]
	v_mfma_scale_f32_16x16x128_f8f6f4 v[242:245], v[132:139], v[100:107], 0, v202, v202 op_sel_hi:[0,0,0]
	s_mov_b32 m0, s101
	v_mfma_scale_f32_16x16x128_f8f6f4 v[246:249], v[140:147], v[100:107], 0, v202, v202 op_sel_hi:[0,0,0]
	global_load_lds_dwordx4 v206, s[26:27]
	v_mfma_scale_f32_16x16x128_f8f6f4 v[168:171], v[132:139], v[108:115], 0, v202, v202 op_sel_hi:[0,0,0]
	v_mfma_scale_f32_16x16x128_f8f6f4 v[140:143], v[140:147], v[108:115], 0, v202, v202 op_sel_hi:[0,0,0]
	s_setprio 0
	s_add_i32 s25, 0, 0x18000
	v_add_u32_e32 v0, s25, v207
	s_barrier
	s_nop 2
	ds_read_b128 v[2:5], v0
	ds_read_b128 v[6:9], v0 offset:1024
	ds_read_b128 v[10:13], v0 offset:2048
	ds_read_b128 v[14:17], v0 offset:3072
	s_add_u32 s26, s10, 0x40000
	v_mov_b32_e32 v0, v205
	ds_read_b128 v[18:21], v208 offset:32768
	ds_read_b128 v[22:25], v208 offset:33792
	ds_read_b128 v[26:29], v208 offset:34816
	ds_read_b128 v[30:33], v208 offset:35840
	ds_read_b128 v[34:37], v208 offset:36864
	ds_read_b128 v[38:41], v208 offset:37888
	ds_read_b128 v[42:45], v208 offset:38912
	ds_read_b128 v[46:49], v208 offset:39936
	s_addc_u32 s27, s11, 0
	s_nop 0
	v_mov_b32_e32 v0, v206
	s_nop 0
	s_waitcnt lgkmcnt(8)
	s_barrier
	s_waitcnt lgkmcnt(0)
	s_setprio 1
	s_waitcnt lgkmcnt(0)
	v_mfma_scale_f32_16x16x128_f8f6f4 v[164:167], v[2:9], v[18:25], v[164:167], v202, v202 op_sel_hi:[0,0,0]
	v_mfma_scale_f32_16x16x128_f8f6f4 v[160:163], v[10:17], v[18:25], v[160:163], v202, v202 op_sel_hi:[0,0,0]
	s_mov_b32 m0, s20
	v_mfma_scale_f32_16x16x128_f8f6f4 v[156:159], v[2:9], v[26:33], v[156:159], v202, v202 op_sel_hi:[0,0,0]
	global_load_lds_dwordx4 v205, s[26:27]
	v_mfma_scale_f32_16x16x128_f8f6f4 v[152:155], v[10:17], v[26:33], v[152:155], v202, v202 op_sel_hi:[0,0,0]
	v_mfma_scale_f32_16x16x128_f8f6f4 v[148:151], v[2:9], v[34:41], v[148:151], v202, v202 op_sel_hi:[0,0,0]
	s_mov_b32 m0, s21
	v_mfma_scale_f32_16x16x128_f8f6f4 v[144:147], v[10:17], v[34:41], v[188:191], v202, v202 op_sel_hi:[0,0,0]
	global_load_lds_dwordx4 v206, s[26:27]
	v_mfma_scale_f32_16x16x128_f8f6f4 v[136:139], v[2:9], v[42:49], v[192:195], v202, v202 op_sel_hi:[0,0,0]
	v_mfma_scale_f32_16x16x128_f8f6f4 v[132:135], v[10:17], v[42:49], v[196:199], v202, v202 op_sel_hi:[0,0,0]
	s_setprio 0
	s_barrier
	s_add_i32 s26, 0, 0x1c000
	v_add_u32_e32 v0, s26, v207
	ds_read_b128 v[52:55], v0
	ds_read_b128 v[56:59], v0 offset:1024
	ds_read_b128 v[68:71], v0 offset:2048
	ds_read_b128 v[72:75], v0 offset:3072
	v_mov_b32_e32 v0, v205
	s_add_i32 s25, s25, s73
	v_lshl_add_u64 v[50:51], s[6:7], 0, v[0:1]
	v_lshl_add_u64 v[50:51], v[50:51], 0, s[66:67]
	v_mov_b32_e32 v0, v206
	v_lshl_add_u64 v[50:51], s[6:7], 0, v[0:1]
	v_lshl_add_u64 v[50:51], v[50:51], 0, s[66:67]
	s_barrier
	s_waitcnt lgkmcnt(0)
	s_setprio 1
	s_waitcnt lgkmcnt(0)
	v_mfma_scale_f32_16x16x128_f8f6f4 v[128:131], v[52:59], v[18:25], v[128:131], v202, v202 op_sel_hi:[0,0,0]
	v_mfma_scale_f32_16x16x128_f8f6f4 v[124:127], v[68:75], v[18:25], v[124:127], v202, v202 op_sel_hi:[0,0,0]
	s_add_u32 s98, s6, s66
	s_addc_u32 s99, s7, s67
	s_mov_b32 m0, s25
	v_mfma_scale_f32_16x16x128_f8f6f4 v[120:123], v[52:59], v[26:33], v[120:123], v202, v202 op_sel_hi:[0,0,0]
	global_load_lds_dwordx4 v205, s[98:99]
	v_mfma_scale_f32_16x16x128_f8f6f4 v[116:119], v[68:75], v[26:33], v[116:119], v202, v202 op_sel_hi:[0,0,0]
	v_mfma_scale_f32_16x16x128_f8f6f4 v[112:115], v[52:59], v[34:41], v[210:213], v202, v202 op_sel_hi:[0,0,0]
	s_add_i32 m0, s25, 0x2000
	v_mfma_scale_f32_16x16x128_f8f6f4 v[108:111], v[68:75], v[34:41], v[172:175], v202, v202 op_sel_hi:[0,0,0]
	global_load_lds_dwordx4 v206, s[98:99]
	v_mfma_scale_f32_16x16x128_f8f6f4 v[104:107], v[52:59], v[42:49], v[176:179], v202, v202 op_sel_hi:[0,0,0]
	v_mfma_scale_f32_16x16x128_f8f6f4 v[100:103], v[68:75], v[42:49], v[180:183], v202, v202 op_sel_hi:[0,0,0]
	s_setprio 0
	v_mov_b32_e32 v0, v205
	s_barrier
	ds_read_b128 v[18:21], v208 offset:49152
	ds_read_b128 v[22:25], v208 offset:50176
	ds_read_b128 v[84:87], v208 offset:51200
	ds_read_b128 v[88:91], v208 offset:52224
	ds_read_b128 v[92:95], v208 offset:53248
	ds_read_b128 v[96:99], v208 offset:54272
	ds_read_b128 v[172:175], v208 offset:55296
	ds_read_b128 v[176:179], v208 offset:56320
	v_lshl_add_u64 v[26:27], s[10:11], 0, v[0:1]
	v_lshl_add_u64 v[26:27], v[26:27], 0, s[66:67]
	v_mov_b32_e32 v0, v206
	v_lshl_add_u64 v[26:27], s[10:11], 0, v[0:1]
	v_lshl_add_u64 v[26:27], v[26:27], 0, s[66:67]
	s_barrier
	s_waitcnt lgkmcnt(0)
	s_setprio 1
	s_waitcnt lgkmcnt(0)
	v_mfma_scale_f32_16x16x128_f8f6f4 v[80:83], v[2:9], v[18:25], v[80:83], v202, v202 op_sel_hi:[0,0,0]
	v_mfma_scale_f32_16x16x128_f8f6f4 v[76:79], v[10:17], v[18:25], v[76:79], v202, v202 op_sel_hi:[0,0,0]
	s_add_u32 s98, s10, s66
	s_addc_u32 s99, s11, s67
	s_mov_b32 m0, s22
	v_mfma_scale_f32_16x16x128_f8f6f4 v[64:67], v[2:9], v[84:91], v[64:67], v202, v202 op_sel_hi:[0,0,0]
	global_load_lds_dwordx4 v205, s[98:99]
	v_mfma_scale_f32_16x16x128_f8f6f4 v[60:63], v[10:17], v[84:91], v[60:63], v202, v202 op_sel_hi:[0,0,0]
	v_mfma_scale_f32_16x16x128_f8f6f4 v[48:51], v[2:9], v[92:99], v[184:187], v202, v202 op_sel_hi:[0,0,0]
	s_mov_b32 m0, s34
	v_mfma_scale_f32_16x16x128_f8f6f4 v[44:47], v[10:17], v[92:99], v[214:217], v202, v202 op_sel_hi:[0,0,0]
	global_load_lds_dwordx4 v206, s[98:99]
	v_mfma_scale_f32_16x16x128_f8f6f4 v[40:43], v[2:9], v[172:179], v[218:221], v202, v202 op_sel_hi:[0,0,0]
	v_mfma_scale_f32_16x16x128_f8f6f4 v[36:39], v[10:17], v[172:179], v[222:225], v202, v202 op_sel_hi:[0,0,0]
	s_setprio 0
	s_barrier
	s_add_u32 s6, s6, 0x40080
	s_addc_u32 s7, s7, 0
	v_mov_b32_e32 v0, v205
	s_add_i32 s10, s26, s73
	s_nop 0
	v_mov_b32_e32 v0, v206
	s_nop 0
	s_waitcnt vmcnt(4)
	s_barrier
	s_setprio 1
	v_mfma_scale_f32_16x16x128_f8f6f4 v[32:35], v[52:59], v[18:25], v[226:229], v202, v202 op_sel_hi:[0,0,0]
	v_mfma_scale_f32_16x16x128_f8f6f4 v[28:31], v[68:75], v[18:25], v[230:233], v202, v202 op_sel_hi:[0,0,0]
	s_mov_b32 m0, s10
	v_mfma_scale_f32_16x16x128_f8f6f4 v[24:27], v[52:59], v[84:91], v[234:237], v202, v202 op_sel_hi:[0,0,0]
	global_load_lds_dwordx4 v205, s[6:7]
	v_mfma_scale_f32_16x16x128_f8f6f4 v[20:23], v[68:75], v[84:91], v[238:241], v202, v202 op_sel_hi:[0,0,0]
	v_mfma_scale_f32_16x16x128_f8f6f4 v[16:19], v[52:59], v[92:99], v[242:245], v202, v202 op_sel_hi:[0,0,0]
	s_add_i32 m0, s10, 0x2000
	v_mfma_scale_f32_16x16x128_f8f6f4 v[12:15], v[68:75], v[92:99], v[246:249], v202, v202 op_sel_hi:[0,0,0]
	global_load_lds_dwordx4 v206, s[6:7]
	v_mfma_scale_f32_16x16x128_f8f6f4 v[8:11], v[52:59], v[172:179], v[168:171], v202, v202 op_sel_hi:[0,0,0]
	v_mfma_scale_f32_16x16x128_f8f6f4 v[4:7], v[68:75], v[172:179], v[140:143], v202, v202 op_sel_hi:[0,0,0]
	s_setprio 0
	s_add_i32 s17, s17, 2
	s_add_u32 s4, s4, 0x100
	s_addc_u32 s5, s5, 0
	s_add_u32 s15, s15, 0x100
	s_addc_u32 s16, s16, 0
	s_cmp_gt_u32 s17, 13
	s_barrier
	s_cbranch_scc0 .LBB0_278
	s_branch .Lpeel_exit_1

.Lpeel_exit_1:
	s_ashr_i32 s3, s8, 2
	s_mul_hi_i32 s4, s3, 0x55555556
	s_lshr_b32 s5, s4, 31
	s_add_i32 s4, s4, s5
	s_mul_i32 s4, s4, 3
	s_sub_i32 s15, s3, s4
	s_add_i32 s3, s8, 11
	s_cmp_lt_u32 s3, 23
	s_cselect_b64 s[12:13], -1, 0
	s_cmp_lt_i32 s15, 2
	v_readlane_b32 s6, v252, 53
	s_cselect_b64 s[4:5], -1, 0
	v_readlane_b32 s7, v252, 54
	s_and_b64 s[4:5], s[6:7], s[4:5]
	v_mbcnt_lo_u32_b32 v211, -1, 0
	v_mbcnt_hi_u32_b32 v211, -1, v211
	s_and_b64 s[6:7], s[12:13], s[4:5]
	v_ashrrev_i32_e32 v210, 4, v211
	s_lshl_b32 s3, s74, 8
	v_lshlrev_b32_e32 v172, 2, v210
	v_mov_b32_e32 v140, 0
	v_cndmask_b32_e64 v0, 0, 1, s[6:7]
	v_and_b32_e32 v209, 15, v211
	s_add_i32 s46, s3, s28
	v_ashrrev_i32_e32 v173, 31, v172
	v_cmp_ne_u32_e64 s[10:11], 1, v0
	s_andn2_b64 vcc, exec, s[6:7]
	v_mov_b32_e32 v141, v140
	v_mov_b32_e32 v142, v140
	v_mov_b32_e32 v143, v140
	v_mov_b32_e32 v92, v140
	v_mov_b32_e32 v93, v140
	v_mov_b32_e32 v94, v140
	v_mov_b32_e32 v95, v140
	v_mov_b32_e32 v88, v140
	v_mov_b32_e32 v89, v140
	v_mov_b32_e32 v90, v140
	v_mov_b32_e32 v91, v140
	v_mov_b32_e32 v72, v140
	v_mov_b32_e32 v73, v140
	v_mov_b32_e32 v74, v140
	v_mov_b32_e32 v75, v140
	v_mov_b32_e32 v56, v140
	v_mov_b32_e32 v57, v140
	v_mov_b32_e32 v58, v140
	v_mov_b32_e32 v59, v140
	s_cbranch_vccnz .LBB0_281
	s_and_b32 s3, s46, 0xfc0
	v_readlane_b32 s4, v252, 31
	v_or_b32_e32 v0, s3, v209
	v_readlane_b32 s5, v252, 32
	v_lshlrev_b32_e32 v0, 7, v0
	s_movk_i32 s3, 0x1000
	v_lshl_add_u64 v[2:3], v[172:173], 2, s[4:5]
	v_lshl_add_u64 v[2:3], v[2:3], 0, v[0:1]
	global_load_dwordx4 v[92:95], v[2:3], off
	global_load_dwordx4 v[96:99], v[2:3], off offset:64
	v_add_co_u32_e32 v52, vcc, s3, v2
	s_nop 1
	v_addc_co_u32_e32 v53, vcc, 0, v3, vcc
	global_load_dwordx4 v[140:143], v[52:53], off offset:2048
	global_load_dwordx4 v[88:91], v[2:3], off offset:2048
	global_load_dwordx4 v[84:87], v[2:3], off offset:2112
	global_load_dwordx4 v[72:75], v[52:53], off
	global_load_dwordx4 v[68:71], v[52:53], off offset:64
	s_nop 0
	global_load_dwordx4 v[52:55], v[52:53], off offset:2112
	s_waitcnt vmcnt(0)
	v_mov_b32_e32 v56, v140
	v_mov_b32_e32 v57, v141
	v_mov_b32_e32 v58, v142
	v_mov_b32_e32 v59, v143

.Lpeel_2:
	s_add_u32 s24, s2, 0xfffc0080
	s_addc_u32 s25, s3, -1
	s_add_i32 s28, 0, 0x10000
	v_add_u32_e32 v128, s28, v150
	ds_read_b128 v[136:139], v128
	ds_read_b128 v[140:143], v128 offset:1024
	ds_read_b128 v[152:155], v128 offset:2048
	ds_read_b128 v[156:159], v128 offset:3072
	s_cmp_eq_u32 s22, 12
	s_cselect_b32 s41, s49, s25
	s_cselect_b32 s40, s48, s24
	s_cselect_b32 s39, s59, s20
	s_cselect_b32 s38, s58, s7
	v_mov_b32_e32 v128, v148
	ds_read_b128 v[160:163], v151
	ds_read_b128 v[164:167], v151 offset:1024
	ds_read_b128 v[168:171], v151 offset:2048
	ds_read_b128 v[172:175], v151 offset:3072
	ds_read_b128 v[176:179], v151 offset:4096
	ds_read_b128 v[180:183], v151 offset:5120
	ds_read_b128 v[184:187], v151 offset:6144
	ds_read_b128 v[188:191], v151 offset:7168
	s_nop 0
	v_mov_b32_e32 v128, v149
	s_nop 0
	s_waitcnt lgkmcnt(8)
	s_barrier
	s_waitcnt lgkmcnt(0)
	s_setprio 1
	s_waitcnt lgkmcnt(0)
	v_mfma_scale_f32_16x16x128_f8f6f4 v[124:127], v[136:143], v[160:167], 0, v146, v146 op_sel_hi:[0,0,0]
	v_mfma_scale_f32_16x16x128_f8f6f4 v[120:123], v[152:159], v[160:167], 0, v146, v146 op_sel_hi:[0,0,0]
	s_add_i32 m0, s0, 0xc000
	v_mfma_scale_f32_16x16x128_f8f6f4 v[116:119], v[136:143], v[168:175], 0, v146, v146 op_sel_hi:[0,0,0]
	global_load_lds_dwordx4 v148, s[2:3]
	v_mfma_scale_f32_16x16x128_f8f6f4 v[112:115], v[152:159], v[168:175], 0, v146, v146 op_sel_hi:[0,0,0]
	v_mfma_scale_f32_16x16x128_f8f6f4 v[128:131], v[136:143], v[176:183], 0, v146, v146 op_sel_hi:[0,0,0]
	s_add_i32 m0, s0, 0xe000
	v_mfma_scale_f32_16x16x128_f8f6f4 v[192:195], v[152:159], v[176:183], 0, v146, v146 op_sel_hi:[0,0,0]
	global_load_lds_dwordx4 v149, s[2:3]
	v_mfma_scale_f32_16x16x128_f8f6f4 v[196:199], v[136:143], v[184:191], 0, v146, v146 op_sel_hi:[0,0,0]
	v_mfma_scale_f32_16x16x128_f8f6f4 v[200:203], v[152:159], v[184:191], 0, v146, v146 op_sel_hi:[0,0,0]
	s_setprio 0
	s_barrier
	s_add_i32 s29, 0, 0x14000
	s_nop 0
	v_add_u32_e32 v108, s29, v150
	v_mov_b32_e32 v132, v148
	s_add_i32 s24, s28, s21
	ds_read_b128 v[96:99], v108
	ds_read_b128 v[100:103], v108 offset:1024
	ds_read_b128 v[104:107], v108 offset:2048
	ds_read_b128 v[108:111], v108 offset:3072
	s_nop 0
	v_mov_b32_e32 v132, v149
	s_nop 0
	s_barrier
	s_waitcnt lgkmcnt(0)
	s_setprio 1
	s_waitcnt lgkmcnt(0)
	v_mfma_scale_f32_16x16x128_f8f6f4 v[204:207], v[96:103], v[160:167], 0, v146, v146 op_sel_hi:[0,0,0]
	v_mfma_scale_f32_16x16x128_f8f6f4 v[160:163], v[104:111], v[160:167], 0, v146, v146 op_sel_hi:[0,0,0]
	s_mov_b32 m0, s24
	v_mfma_scale_f32_16x16x128_f8f6f4 v[164:167], v[96:103], v[168:175], 0, v146, v146 op_sel_hi:[0,0,0]
	global_load_lds_dwordx4 v148, s[38:39]
	v_mfma_scale_f32_16x16x128_f8f6f4 v[168:171], v[104:111], v[168:175], 0, v146, v146 op_sel_hi:[0,0,0]
	v_mfma_scale_f32_16x16x128_f8f6f4 v[172:175], v[96:103], v[176:183], 0, v146, v146 op_sel_hi:[0,0,0]
	s_add_i32 m0, s24, 0x2000
	v_mfma_scale_f32_16x16x128_f8f6f4 v[176:179], v[104:111], v[176:183], 0, v146, v146 op_sel_hi:[0,0,0]
	global_load_lds_dwordx4 v149, s[38:39]
	v_mfma_scale_f32_16x16x128_f8f6f4 v[180:183], v[96:103], v[184:191], 0, v146, v146 op_sel_hi:[0,0,0]
	v_mfma_scale_f32_16x16x128_f8f6f4 v[184:187], v[104:111], v[184:191], 0, v146, v146 op_sel_hi:[0,0,0]
	s_setprio 0
	v_mov_b32_e32 v132, v148
	s_barrier
	s_nop 2
	ds_read_b128 v[32:35], v151 offset:16384
	ds_read_b128 v[36:39], v151 offset:17408
	ds_read_b128 v[40:43], v151 offset:18432
	ds_read_b128 v[44:47], v151 offset:19456
	ds_read_b128 v[48:51], v151 offset:20480
	ds_read_b128 v[52:55], v151 offset:21504
	ds_read_b128 v[56:59], v151 offset:22528
	ds_read_b128 v[60:63], v151 offset:23552
	s_nop 0
	v_mov_b32_e32 v132, v149
	s_nop 0
	s_barrier
	s_waitcnt lgkmcnt(0)
	s_setprio 1
	s_waitcnt lgkmcnt(0)
	v_mfma_scale_f32_16x16x128_f8f6f4 v[92:95], v[136:143], v[32:39], 0, v146, v146 op_sel_hi:[0,0,0]
	v_mfma_scale_f32_16x16x128_f8f6f4 v[88:91], v[152:159], v[32:39], 0, v146, v146 op_sel_hi:[0,0,0]
	s_mov_b32 m0, s0
	v_mfma_scale_f32_16x16x128_f8f6f4 v[84:87], v[136:143], v[40:47], 0, v146, v146 op_sel_hi:[0,0,0]
	global_load_lds_dwordx4 v148, s[40:41]
	v_mfma_scale_f32_16x16x128_f8f6f4 v[80:83], v[152:159], v[40:47], 0, v146, v146 op_sel_hi:[0,0,0]
	v_mfma_scale_f32_16x16x128_f8f6f4 v[76:79], v[136:143], v[48:55], 0, v146, v146 op_sel_hi:[0,0,0]
	s_mov_b32 m0, s1
	v_mfma_scale_f32_16x16x128_f8f6f4 v[72:75], v[152:159], v[48:55], 0, v146, v146 op_sel_hi:[0,0,0]
	global_load_lds_dwordx4 v149, s[40:41]
	v_mfma_scale_f32_16x16x128_f8f6f4 v[188:191], v[136:143], v[56:63], 0, v146, v146 op_sel_hi:[0,0,0]
	v_mfma_scale_f32_16x16x128_f8f6f4 v[208:211], v[152:159], v[56:63], 0, v146, v146 op_sel_hi:[0,0,0]
	s_setprio 0
	s_barrier
	s_add_u32 s24, s38, 0x40000
	s_addc_u32 s25, s39, 0
	s_nop 2
	v_mov_b32_e32 v64, v148
	s_add_i32 s28, s29, s21
	s_mov_b32 s100, s28
	s_nop 0
	v_mov_b32_e32 v64, v149
	s_add_i32 s101, s28, 0x2000
	s_nop 0
	s_waitcnt vmcnt(4)
	s_barrier
	s_setprio 1
	v_mfma_scale_f32_16x16x128_f8f6f4 v[212:215], v[96:103], v[32:39], 0, v146, v146 op_sel_hi:[0,0,0]
	v_mfma_scale_f32_16x16x128_f8f6f4 v[216:219], v[104:111], v[32:39], 0, v146, v146 op_sel_hi:[0,0,0]
	s_mov_b32 m0, s100
	v_mfma_scale_f32_16x16x128_f8f6f4 v[220:223], v[96:103], v[40:47], 0, v146, v146 op_sel_hi:[0,0,0]
	global_load_lds_dwordx4 v148, s[24:25]
	v_mfma_scale_f32_16x16x128_f8f6f4 v[224:227], v[104:111], v[40:47], 0, v146, v146 op_sel_hi:[0,0,0]
	v_mfma_scale_f32_16x16x128_f8f6f4 v[228:231], v[96:103], v[48:55], 0, v146, v146 op_sel_hi:[0,0,0]
	s_mov_b32 m0, s101
	v_mfma_scale_f32_16x16x128_f8f6f4 v[232:235], v[104:111], v[48:55], 0, v146, v146 op_sel_hi:[0,0,0]
	global_load_lds_dwordx4 v149, s[24:25]
	v_mfma_scale_f32_16x16x128_f8f6f4 v[236:239], v[96:103], v[56:63], 0, v146, v146 op_sel_hi:[0,0,0]
	v_mfma_scale_f32_16x16x128_f8f6f4 v[240:243], v[104:111], v[56:63], 0, v146, v146 op_sel_hi:[0,0,0]
	s_setprio 0
	s_add_i32 s28, 0, 0x18000
	s_nop 1
	v_add_u32_e32 v12, s28, v150
	s_barrier
	s_nop 0
	ds_read_b128 v[0:3], v12
	ds_read_b128 v[4:7], v12 offset:1024
	ds_read_b128 v[8:11], v12 offset:2048
	ds_read_b128 v[12:15], v12 offset:3072
	s_add_u32 s24, s40, 0x40000
	v_mov_b32_e32 v40, v148
	ds_read_b128 v[16:19], v151 offset:32768
	ds_read_b128 v[20:23], v151 offset:33792
	ds_read_b128 v[24:27], v151 offset:34816
	ds_read_b128 v[28:31], v151 offset:35840
	ds_read_b128 v[32:35], v151 offset:36864
	ds_read_b128 v[36:39], v151 offset:37888
	ds_read_b128 v[64:67], v151 offset:38912
	ds_read_b128 v[68:71], v151 offset:39936
	s_addc_u32 s25, s41, 0
	s_nop 0
	v_mov_b32_e32 v40, v149
	s_nop 0
	s_waitcnt lgkmcnt(8)
	s_barrier
	s_waitcnt lgkmcnt(0)
	s_setprio 1
	s_waitcnt lgkmcnt(0)
	v_mfma_scale_f32_16x16x128_f8f6f4 v[124:127], v[0:7], v[16:23], v[124:127], v146, v146 op_sel_hi:[0,0,0]
	v_mfma_scale_f32_16x16x128_f8f6f4 v[120:123], v[8:15], v[16:23], v[120:123], v146, v146 op_sel_hi:[0,0,0]
	s_mov_b32 m0, s8
	v_mfma_scale_f32_16x16x128_f8f6f4 v[116:119], v[0:7], v[24:31], v[116:119], v146, v146 op_sel_hi:[0,0,0]
	global_load_lds_dwordx4 v148, s[24:25]
	v_mfma_scale_f32_16x16x128_f8f6f4 v[112:115], v[8:15], v[24:31], v[112:115], v146, v146 op_sel_hi:[0,0,0]
	v_mfma_scale_f32_16x16x128_f8f6f4 v[108:111], v[0:7], v[32:39], v[128:131], v146, v146 op_sel_hi:[0,0,0]
	s_mov_b32 m0, s9
	v_mfma_scale_f32_16x16x128_f8f6f4 v[104:107], v[8:15], v[32:39], v[192:195], v146, v146 op_sel_hi:[0,0,0]
	global_load_lds_dwordx4 v149, s[24:25]
	v_mfma_scale_f32_16x16x128_f8f6f4 v[100:103], v[0:7], v[64:71], v[196:199], v146, v146 op_sel_hi:[0,0,0]
	v_mfma_scale_f32_16x16x128_f8f6f4 v[96:99], v[8:15], v[64:71], v[200:203], v146, v146 op_sel_hi:[0,0,0]
	s_setprio 0
	s_barrier
	s_add_i32 s29, 0, 0x1c000
	v_add_u32_e32 v40, s29, v150
	v_mov_b32_e32 v132, v148
	ds_read_b128 v[136:139], v40
	ds_read_b128 v[140:143], v40 offset:1024
	ds_read_b128 v[152:155], v40 offset:2048
	ds_read_b128 v[156:159], v40 offset:3072
	s_add_i32 s24, s28, s21
	v_lshl_add_u64 v[40:41], s[38:39], 0, v[132:133]
	v_lshl_add_u64 v[40:41], v[40:41], 0, s[52:53]
	v_mov_b32_e32 v132, v149
	v_lshl_add_u64 v[40:41], s[38:39], 0, v[132:133]
	v_lshl_add_u64 v[40:41], v[40:41], 0, s[52:53]
	s_barrier
	s_waitcnt lgkmcnt(0)
	s_setprio 1
	s_waitcnt lgkmcnt(0)
	v_mfma_scale_f32_16x16x128_f8f6f4 v[60:63], v[136:143], v[16:23], v[204:207], v146, v146 op_sel_hi:[0,0,0]
	v_mfma_scale_f32_16x16x128_f8f6f4 v[56:59], v[152:159], v[16:23], v[160:163], v146, v146 op_sel_hi:[0,0,0]
	s_add_u32 s98, s38, s52
	s_addc_u32 s99, s39, s53
	s_mov_b32 m0, s24
	v_mfma_scale_f32_16x16x128_f8f6f4 v[52:55], v[136:143], v[24:31], v[164:167], v146, v146 op_sel_hi:[0,0,0]
	global_load_lds_dwordx4 v148, s[98:99]
	v_mfma_scale_f32_16x16x128_f8f6f4 v[48:51], v[152:159], v[24:31], v[168:171], v146, v146 op_sel_hi:[0,0,0]
	v_mfma_scale_f32_16x16x128_f8f6f4 v[44:47], v[136:143], v[32:39], v[172:175], v146, v146 op_sel_hi:[0,0,0]
	s_add_i32 m0, s24, 0x2000
	v_mfma_scale_f32_16x16x128_f8f6f4 v[40:43], v[152:159], v[32:39], v[176:179], v146, v146 op_sel_hi:[0,0,0]
	global_load_lds_dwordx4 v149, s[98:99]
	v_mfma_scale_f32_16x16x128_f8f6f4 v[36:39], v[136:143], v[64:71], v[180:183], v146, v146 op_sel_hi:[0,0,0]
	v_mfma_scale_f32_16x16x128_f8f6f4 v[32:35], v[152:159], v[64:71], v[184:187], v146, v146 op_sel_hi:[0,0,0]
	s_setprio 0
	v_mov_b32_e32 v132, v148
	s_barrier
	ds_read_b128 v[16:19], v151 offset:49152
	ds_read_b128 v[20:23], v151 offset:50176
	ds_read_b128 v[160:163], v151 offset:51200
	ds_read_b128 v[164:167], v151 offset:52224
	ds_read_b128 v[168:171], v151 offset:53248
	ds_read_b128 v[172:175], v151 offset:54272
	ds_read_b128 v[176:179], v151 offset:55296
	ds_read_b128 v[180:183], v151 offset:56320
	v_lshl_add_u64 v[24:25], s[40:41], 0, v[132:133]
	v_lshl_add_u64 v[24:25], v[24:25], 0, s[52:53]
	v_mov_b32_e32 v132, v149
	v_lshl_add_u64 v[24:25], s[40:41], 0, v[132:133]
	v_lshl_add_u64 v[24:25], v[24:25], 0, s[52:53]
	s_barrier
	s_waitcnt lgkmcnt(0)
	s_setprio 1
	s_waitcnt lgkmcnt(0)
	v_mfma_scale_f32_16x16x128_f8f6f4 v[92:95], v[0:7], v[16:23], v[92:95], v146, v146 op_sel_hi:[0,0,0]
	v_mfma_scale_f32_16x16x128_f8f6f4 v[88:91], v[8:15], v[16:23], v[88:91], v146, v146 op_sel_hi:[0,0,0]
	s_add_u32 s98, s40, s52
	s_addc_u32 s99, s41, s53
	s_mov_b32 m0, s10
	v_mfma_scale_f32_16x16x128_f8f6f4 v[84:87], v[0:7], v[160:167], v[84:87], v146, v146 op_sel_hi:[0,0,0]
	global_load_lds_dwordx4 v148, s[98:99]
	v_mfma_scale_f32_16x16x128_f8f6f4 v[80:83], v[8:15], v[160:167], v[80:83], v146, v146 op_sel_hi:[0,0,0]
	v_mfma_scale_f32_16x16x128_f8f6f4 v[76:79], v[0:7], v[168:175], v[76:79], v146, v146 op_sel_hi:[0,0,0]
	s_mov_b32 m0, s11
	v_mfma_scale_f32_16x16x128_f8f6f4 v[72:75], v[8:15], v[168:175], v[72:75], v146, v146 op_sel_hi:[0,0,0]
	global_load_lds_dwordx4 v149, s[98:99]
	v_mfma_scale_f32_16x16x128_f8f6f4 v[68:71], v[0:7], v[176:183], v[188:191], v146, v146 op_sel_hi:[0,0,0]
	v_mfma_scale_f32_16x16x128_f8f6f4 v[64:67], v[8:15], v[176:183], v[208:211], v146, v146 op_sel_hi:[0,0,0]
	s_setprio 0
	s_barrier
	s_add_u32 s24, s38, 0x40080
	s_addc_u32 s25, s39, 0
	v_mov_b32_e32 v0, v148
	s_add_i32 s28, s29, s21
	s_nop 0
	v_mov_b32_e32 v0, v149
	s_nop 0
	s_waitcnt vmcnt(4)
	s_barrier
	s_setprio 1
	v_mfma_scale_f32_16x16x128_f8f6f4 v[28:31], v[136:143], v[16:23], v[212:215], v146, v146 op_sel_hi:[0,0,0]
	v_mfma_scale_f32_16x16x128_f8f6f4 v[24:27], v[152:159], v[16:23], v[216:219], v146, v146 op_sel_hi:[0,0,0]
	s_mov_b32 m0, s28
	v_mfma_scale_f32_16x16x128_f8f6f4 v[20:23], v[136:143], v[160:167], v[220:223], v146, v146 op_sel_hi:[0,0,0]
	global_load_lds_dwordx4 v148, s[24:25]
	v_mfma_scale_f32_16x16x128_f8f6f4 v[16:19], v[152:159], v[160:167], v[224:227], v146, v146 op_sel_hi:[0,0,0]
	v_mfma_scale_f32_16x16x128_f8f6f4 v[12:15], v[136:143], v[168:175], v[228:231], v146, v146 op_sel_hi:[0,0,0]
	s_add_i32 m0, s28, 0x2000
	v_mfma_scale_f32_16x16x128_f8f6f4 v[8:11], v[152:159], v[168:175], v[232:235], v146, v146 op_sel_hi:[0,0,0]
	global_load_lds_dwordx4 v149, s[24:25]
	v_mfma_scale_f32_16x16x128_f8f6f4 v[4:7], v[136:143], v[176:183], v[236:239], v146, v146 op_sel_hi:[0,0,0]
	v_mfma_scale_f32_16x16x128_f8f6f4 v[0:3], v[152:159], v[176:183], v[240:243], v146, v146 op_sel_hi:[0,0,0]
	s_setprio 0
	s_add_i32 s22, s22, 2
	s_add_u32 s2, s2, 0x100
	s_addc_u32 s3, s3, 0
	s_add_u32 s7, s7, 0x100
	s_addc_u32 s20, s20, 0
	s_cmp_gt_u32 s22, 13
	s_barrier
	s_cbranch_scc0 .LBB0_1503
	s_branch .Lpeel_exit_2

.Lpeel_exit_2:
	s_ashr_i32 s2, s13, 4
	s_mul_hi_i32 s3, s2, 0xc000
	s_mul_i32 s2, s2, 0xc000
	s_add_u32 s7, s69, s2
	s_addc_u32 s20, s71, s3
	s_lshl_b32 s2, s15, 8
	s_ashr_i32 s3, s2, 31
	s_lshl_b64 s[24:25], s[2:3], 2
	s_add_u32 s7, s7, s24
	v_mbcnt_lo_u32_b32 v132, -1, 0
	v_mbcnt_hi_u32_b32 v132, -1, v132
	s_addc_u32 s15, s20, s25
	v_ashrrev_i32_e32 v136, 4, v132
	s_lshl_b32 s20, s23, 2
	s_add_u32 s24, s7, s20
	v_lshlrev_b32_e32 v128, 2, v136
	s_addc_u32 s25, s15, 0
	v_ashrrev_i32_e32 v129, 31, v128
	v_lshl_add_u64 v[130:131], v[128:129], 2, s[24:25]
	v_lshlrev_b32_e32 v128, 3, v136
	global_load_dwordx4 v[136:139], v[130:131], off
	global_load_dwordx4 v[152:155], v[130:131], off offset:64
	s_lshl_b32 s7, s13, 8
	s_add_i32 s24, s7, s16
	s_ashr_i32 s25, s24, 31
	s_lshl_b64 s[24:25], s[24:25], 11
	s_add_u32 s7, s61, s24
	s_addc_u32 s13, s65, s25
	s_add_u32 s2, s7, s2
	s_addc_u32 s3, s13, s3
	v_bfi_b32 v128, -16, v128, v132
	s_add_u32 s2, s2, s23
	v_ashrrev_i32_e32 v129, 31, v128
	s_addc_u32 s3, s3, 0
	v_lshlrev_b64 v[128:129], 11, v[128:129]
	v_lshl_add_u64 v[128:129], s[2:3], 0, v[128:129]
	v_and_b32_e32 v132, 16, v132
	v_lshl_add_u64 v[128:129], v[128:129], 0, v[132:133]
	s_mov_b32 s2, 0x10000
	s_mov_b32 s13, s36
	s_mov_b32 s15, s6
	s_mov_b64 s[34:35], s[58:59]
	s_waitcnt vmcnt(0)
	v_pk_mul_f32 v[140:141], v[138:139], s[54:55] op_sel_hi:[1,0]
	v_pk_mul_f32 v[138:139], v[136:137], s[54:55] op_sel_hi:[1,0]
	v_pk_mul_f32 v[136:137], v[152:153], s[54:55] op_sel_hi:[1,0]
	v_pk_mul_f32 v[152:153], v[124:125], v[138:139]
	v_mov_b32_e32 v124, v133
	v_cvt_pk_fp8_f32 v124, v152, v153
	v_pk_mul_f32 v[126:127], v[126:127], v[140:141]
	v_pk_mul_f32 v[112:113], v[112:113], v[136:137]
	v_pk_mul_f32 v[110:111], v[110:111], v[140:141]
	v_cvt_pk_fp8_f32 v124, v126, v127 op_sel:[0,0,1]
	v_mov_b32_e32 v127, v133
	v_cvt_pk_fp8_f32 v127, v112, v113
	v_pk_mul_f32 v[112:113], v[108:109], v[138:139]
	v_mov_b32_e32 v108, v133
	v_cvt_pk_fp8_f32 v108, v112, v113
	v_pk_mul_f32 v[96:97], v[96:97], v[136:137]
	v_pk_mul_f32 v[142:143], v[154:155], s[54:55] op_sel_hi:[1,0]
	v_pk_mul_f32 v[94:95], v[94:95], v[140:141]
	v_cvt_pk_fp8_f32 v108, v110, v111 op_sel:[0,0,1]
	v_mov_b32_e32 v111, v133
	v_cvt_pk_fp8_f32 v111, v96, v97
	v_pk_mul_f32 v[98:99], v[98:99], v[142:143]
	v_pk_mul_f32 v[80:81], v[80:81], v[136:137]
	v_pk_mul_f32 v[78:79], v[78:79], v[140:141]
	v_cvt_pk_fp8_f32 v111, v98, v99 op_sel:[0,0,1]
	v_pk_mul_f32 v[98:99], v[92:93], v[138:139]
	v_mov_b32_e32 v92, v133
	v_cvt_pk_fp8_f32 v92, v98, v99
	v_pk_mul_f32 v[120:121], v[120:121], v[136:137]
	v_mov_b32_e32 v125, v133
	v_pk_mul_f32 v[116:117], v[116:117], v[138:139]
	v_cvt_pk_fp8_f32 v92, v94, v95 op_sel:[0,0,1]
	v_mov_b32_e32 v95, v133
	v_cvt_pk_fp8_f32 v95, v80, v81
	v_pk_mul_f32 v[80:81], v[76:77], v[138:139]
	v_mov_b32_e32 v76, v133
	v_cvt_pk_fp8_f32 v76, v80, v81
	v_mov_b32_e32 v126, v133
	v_pk_mul_f32 v[104:105], v[104:105], v[136:137]
	v_mov_b32_e32 v109, v133
	v_pk_mul_f32 v[100:101], v[100:101], v[138:139]
	v_mov_b32_e32 v110, v133
	v_pk_mul_f32 v[88:89], v[88:89], v[136:137]
	v_mov_b32_e32 v93, v133
	v_pk_mul_f32 v[84:85], v[84:85], v[138:139]
	v_mov_b32_e32 v94, v133
	v_cvt_pk_fp8_f32 v76, v78, v79 op_sel:[0,0,1]
	v_pk_mul_f32 v[72:73], v[72:73], v[136:137]
	v_mov_b32_e32 v77, v133
	v_pk_mul_f32 v[68:69], v[68:69], v[138:139]
	v_mov_b32_e32 v78, v133
	v_pk_mul_f32 v[64:65], v[64:65], v[136:137]
	v_mov_b32_e32 v79, v133
	v_cvt_pk_fp8_f32 v125, v120, v121
	v_cvt_pk_fp8_f32 v126, v116, v117
	v_cvt_pk_fp8_f32 v109, v104, v105
	v_cvt_pk_fp8_f32 v110, v100, v101
	v_cvt_pk_fp8_f32 v93, v88, v89
	v_cvt_pk_fp8_f32 v94, v84, v85
	v_cvt_pk_fp8_f32 v77, v72, v73
	v_cvt_pk_fp8_f32 v78, v68, v69
	v_cvt_pk_fp8_f32 v79, v64, v65
	v_pk_mul_f32 v[122:123], v[122:123], v[142:143]
	v_pk_mul_f32 v[118:119], v[118:119], v[140:141]
	v_pk_mul_f32 v[114:115], v[114:115], v[142:143]
	v_pk_mul_f32 v[106:107], v[106:107], v[142:143]
	v_pk_mul_f32 v[102:103], v[102:103], v[140:141]
	v_pk_mul_f32 v[90:91], v[90:91], v[142:143]
	v_pk_mul_f32 v[86:87], v[86:87], v[140:141]
	v_pk_mul_f32 v[82:83], v[82:83], v[142:143]
	v_pk_mul_f32 v[74:75], v[74:75], v[142:143]
	v_pk_mul_f32 v[70:71], v[70:71], v[140:141]
	v_pk_mul_f32 v[66:67], v[66:67], v[142:143]
	v_cvt_pk_fp8_f32 v125, v122, v123 op_sel:[0,0,1]
	v_cvt_pk_fp8_f32 v126, v118, v119 op_sel:[0,0,1]
	v_cvt_pk_fp8_f32 v127, v114, v115 op_sel:[0,0,1]
	v_cvt_pk_fp8_f32 v109, v106, v107 op_sel:[0,0,1]
	v_cvt_pk_fp8_f32 v110, v102, v103 op_sel:[0,0,1]
	v_add_co_u32_e32 v96, vcc, s2, v128
	v_cvt_pk_fp8_f32 v93, v90, v91 op_sel:[0,0,1]
	v_cvt_pk_fp8_f32 v94, v86, v87 op_sel:[0,0,1]
	v_cvt_pk_fp8_f32 v95, v82, v83 op_sel:[0,0,1]
	v_cvt_pk_fp8_f32 v77, v74, v75 op_sel:[0,0,1]
	v_cvt_pk_fp8_f32 v78, v70, v71 op_sel:[0,0,1]
	v_cvt_pk_fp8_f32 v79, v66, v67 op_sel:[0,0,1]
	v_addc_co_u32_e32 v97, vcc, 0, v129, vcc
	s_mov_b32 s2, 0x40000
	v_add_co_u32_e32 v64, vcc, s2, v128
	s_mov_b32 s2, 0x50000
	s_nop 0
	v_addc_co_u32_e32 v65, vcc, 0, v129, vcc
	v_permlane32_swap_b32_e32 v124, v126
	v_permlane32_swap_b32_e32 v125, v127
	v_permlane32_swap_b32_e32 v108, v110
	v_permlane32_swap_b32_e32 v109, v111
	v_permlane32_swap_b32_e32 v92, v94
	v_permlane32_swap_b32_e32 v93, v95
	v_permlane32_swap_b32_e32 v76, v78
	v_permlane32_swap_b32_e32 v77, v79
	v_add_co_u32_e32 v66, vcc, s2, v128
	v_permlane16_swap_b32_e32 v124, v125
	v_permlane16_swap_b32_e32 v126, v127
	v_permlane16_swap_b32_e32 v108, v109
	v_permlane16_swap_b32_e32 v110, v111
	v_permlane16_swap_b32_e32 v92, v93
	v_permlane16_swap_b32_e32 v94, v95
	v_permlane16_swap_b32_e32 v76, v77
	v_permlane16_swap_b32_e32 v78, v79
	v_addc_co_u32_e32 v67, vcc, 0, v129, vcc
	global_store_dwordx4 v[128:129], v[124:127], off
	global_store_dwordx4 v[96:97], v[108:111], off
	global_store_dwordx4 v[64:65], v[92:95], off
	global_store_dwordx4 v[66:67], v[76:79], off
	global_load_dwordx4 v[68:71], v[130:131], off offset:512
	s_and_b64 vcc, exec, s[4:5]
	global_load_dwordx4 v[76:79], v[130:131], off offset:576
	s_mov_b64 s[2:3], s[48:49]
	s_waitcnt vmcnt(0)
	v_pk_mul_f32 v[72:73], v[70:71], s[54:55] op_sel_hi:[1,0]
	v_pk_mul_f32 v[70:71], v[68:69], s[54:55] op_sel_hi:[1,0]
	v_pk_mul_f32 v[68:69], v[76:77], s[54:55] op_sel_hi:[1,0]
	v_pk_mul_f32 v[76:77], v[60:61], v[70:71]
	v_mov_b32_e32 v60, v133
	v_cvt_pk_fp8_f32 v60, v76, v77
	v_pk_mul_f32 v[62:63], v[62:63], v[72:73]
	v_pk_mul_f32 v[48:49], v[48:49], v[68:69]
	v_pk_mul_f32 v[46:47], v[46:47], v[72:73]
	v_cvt_pk_fp8_f32 v60, v62, v63 op_sel:[0,0,1]
	v_mov_b32_e32 v63, v133
	v_cvt_pk_fp8_f32 v63, v48, v49
	v_pk_mul_f32 v[48:49], v[44:45], v[70:71]
	v_mov_b32_e32 v44, v133
	v_cvt_pk_fp8_f32 v44, v48, v49
	v_pk_mul_f32 v[32:33], v[32:33], v[68:69]
	v_pk_mul_f32 v[30:31], v[30:31], v[72:73]
	v_pk_mul_f32 v[16:17], v[16:17], v[68:69]
	v_cvt_pk_fp8_f32 v44, v46, v47 op_sel:[0,0,1]
	v_mov_b32_e32 v47, v133
	v_cvt_pk_fp8_f32 v47, v32, v33
	v_pk_mul_f32 v[32:33], v[28:29], v[70:71]
	v_mov_b32_e32 v28, v133
	v_cvt_pk_fp8_f32 v28, v32, v33
	v_pk_mul_f32 v[56:57], v[56:57], v[68:69]
	v_mov_b32_e32 v61, v133
	v_pk_mul_f32 v[52:53], v[52:53], v[70:71]
	v_cvt_pk_fp8_f32 v28, v30, v31 op_sel:[0,0,1]
	v_mov_b32_e32 v31, v133
	v_cvt_pk_fp8_f32 v31, v16, v17
	v_pk_mul_f32 v[16:17], v[12:13], v[70:71]
	v_mov_b32_e32 v12, v133
	v_cvt_pk_fp8_f32 v12, v16, v17
	v_mov_b32_e32 v62, v133
	v_pk_mul_f32 v[24:25], v[24:25], v[68:69]
	v_mov_b32_e32 v29, v133
	v_pk_mul_f32 v[20:21], v[20:21], v[70:71]
	v_mov_b32_e32 v30, v133
	v_pk_mul_f32 v[14:15], v[14:15], v[72:73]
	v_cvt_pk_fp8_f32 v61, v56, v57
	v_cvt_pk_fp8_f32 v62, v52, v53
	v_pk_mul_f32 v[40:41], v[40:41], v[68:69]
	v_mov_b32_e32 v45, v133
	v_pk_mul_f32 v[36:37], v[36:37], v[70:71]
	v_mov_b32_e32 v46, v133
	v_cvt_pk_fp8_f32 v29, v24, v25
	v_cvt_pk_fp8_f32 v30, v20, v21
	v_cvt_pk_fp8_f32 v12, v14, v15 op_sel:[0,0,1]
	v_pk_mul_f32 v[8:9], v[8:9], v[68:69]
	v_mov_b32_e32 v13, v133
	v_pk_mul_f32 v[4:5], v[4:5], v[70:71]
	v_mov_b32_e32 v14, v133
	v_pk_mul_f32 v[0:1], v[0:1], v[68:69]
	v_mov_b32_e32 v15, v133
	v_cvt_pk_fp8_f32 v45, v40, v41
	v_cvt_pk_fp8_f32 v46, v36, v37
	v_cvt_pk_fp8_f32 v13, v8, v9
	v_cvt_pk_fp8_f32 v14, v4, v5
	v_cvt_pk_fp8_f32 v15, v0, v1
	v_pk_mul_f32 v[74:75], v[78:79], s[54:55] op_sel_hi:[1,0]
	v_pk_mul_f32 v[54:55], v[54:55], v[72:73]
	v_pk_mul_f32 v[58:59], v[58:59], v[74:75]
	v_pk_mul_f32 v[50:51], v[50:51], v[74:75]
	v_pk_mul_f32 v[26:27], v[26:27], v[74:75]
	v_pk_mul_f32 v[22:23], v[22:23], v[72:73]
	v_pk_mul_f32 v[18:19], v[18:19], v[74:75]
	v_cvt_pk_fp8_f32 v61, v58, v59 op_sel:[0,0,1]
	v_cvt_pk_fp8_f32 v62, v54, v55 op_sel:[0,0,1]
	v_cvt_pk_fp8_f32 v63, v50, v51 op_sel:[0,0,1]
	v_pk_mul_f32 v[42:43], v[42:43], v[74:75]
	v_pk_mul_f32 v[38:39], v[38:39], v[72:73]
	v_pk_mul_f32 v[34:35], v[34:35], v[74:75]
	v_cvt_pk_fp8_f32 v29, v26, v27 op_sel:[0,0,1]
	v_cvt_pk_fp8_f32 v30, v22, v23 op_sel:[0,0,1]
	v_cvt_pk_fp8_f32 v31, v18, v19 op_sel:[0,0,1]
	v_pk_mul_f32 v[10:11], v[10:11], v[74:75]
	v_pk_mul_f32 v[6:7], v[6:7], v[72:73]
	v_pk_mul_f32 v[2:3], v[2:3], v[74:75]
	v_cvt_pk_fp8_f32 v45, v42, v43 op_sel:[0,0,1]
	v_cvt_pk_fp8_f32 v46, v38, v39 op_sel:[0,0,1]
	v_cvt_pk_fp8_f32 v47, v34, v35 op_sel:[0,0,1]
	v_cvt_pk_fp8_f32 v13, v10, v11 op_sel:[0,0,1]
	v_cvt_pk_fp8_f32 v14, v6, v7 op_sel:[0,0,1]
	v_cvt_pk_fp8_f32 v15, v2, v3 op_sel:[0,0,1]
	v_permlane32_swap_b32_e32 v60, v62
	v_permlane32_swap_b32_e32 v61, v63
	v_permlane32_swap_b32_e32 v28, v30
	v_permlane32_swap_b32_e32 v29, v31
	v_permlane16_swap_b32_e32 v60, v61
	v_permlane16_swap_b32_e32 v62, v63
	v_permlane32_swap_b32_e32 v44, v46
	v_permlane32_swap_b32_e32 v45, v47
	v_permlane16_swap_b32_e32 v28, v29
	v_permlane16_swap_b32_e32 v30, v31
	v_permlane32_swap_b32_e32 v12, v14
	v_permlane32_swap_b32_e32 v13, v15
	v_permlane16_swap_b32_e32 v44, v45
	v_permlane16_swap_b32_e32 v46, v47
	global_store_dwordx4 v[128:129], v[60:63], off offset:128
	global_store_dwordx4 v[96:97], v[44:47], off offset:128
	v_permlane16_swap_b32_e32 v12, v13
	v_permlane16_swap_b32_e32 v14, v15
	global_store_dwordx4 v[64:65], v[28:31], off offset:128
	global_store_dwordx4 v[66:67], v[12:15], off offset:128
	s_cbranch_vccz .LBB0_1496
	v_readlane_b32 s0, v252, 18
	s_waitcnt vmcnt(0)
	v_readlane_b32 s1, v252, 19
	s_andn2_b64 vcc, exec, s[0:1]
	s_cbranch_vccnz .LBB0_1227
	s_barrier
	s_branch .LBB0_1227

.Lpeel_4:
	ds_read_b128 v[140:143], v134
	ds_read_b128 v[144:147], v134 offset:1024
	ds_read_b128 v[148:151], v134 offset:2048
	ds_read_b128 v[152:155], v134 offset:3072
	s_add_u32 s18, s16, 0xfffd0080
	s_addc_u32 s19, s17, -1
	s_cmp_eq_u32 s54, 8
	s_cselect_b32 s21, s15, s19
	s_cselect_b32 s20, s14, s18
	s_cselect_b32 s19, s13, s53
	s_cselect_b32 s18, s12, s52
	v_mov_b32_e32 v128, v132
	ds_read_b128 v[156:159], v135
	ds_read_b128 v[160:163], v135 offset:1024
	ds_read_b128 v[164:167], v135 offset:2048
	ds_read_b128 v[168:171], v135 offset:3072
	ds_read_b128 v[172:175], v135 offset:4096
	ds_read_b128 v[176:179], v135 offset:5120
	ds_read_b128 v[180:183], v135 offset:6144
	ds_read_b128 v[184:187], v135 offset:7168
	s_nop 0
	v_mov_b32_e32 v128, v133
	s_nop 0
	s_waitcnt lgkmcnt(8)
	s_barrier
	s_waitcnt lgkmcnt(0)
	s_setprio 1
	s_waitcnt lgkmcnt(0)
	v_mfma_scale_f32_16x16x128_f8f6f4 v[124:127], v[140:147], v[156:163], 0, v136, v136 op_sel_hi:[0,0,0]
	v_mfma_scale_f32_16x16x128_f8f6f4 v[120:123], v[148:155], v[156:163], 0, v136, v136 op_sel_hi:[0,0,0]
	s_mov_b32 m0, s39
	v_mfma_scale_f32_16x16x128_f8f6f4 v[116:119], v[140:147], v[164:171], 0, v136, v136 op_sel_hi:[0,0,0]
	global_load_lds_dwordx4 v132, s[16:17]
	v_mfma_scale_f32_16x16x128_f8f6f4 v[112:115], v[148:155], v[164:171], 0, v136, v136 op_sel_hi:[0,0,0]
	v_mfma_scale_f32_16x16x128_f8f6f4 v[188:191], v[140:147], v[172:179], 0, v136, v136 op_sel_hi:[0,0,0]
	s_mov_b32 m0, s40
	v_mfma_scale_f32_16x16x128_f8f6f4 v[192:195], v[148:155], v[172:179], 0, v136, v136 op_sel_hi:[0,0,0]
	global_load_lds_dwordx4 v133, s[16:17]
	v_mfma_scale_f32_16x16x128_f8f6f4 v[196:199], v[140:147], v[180:187], 0, v136, v136 op_sel_hi:[0,0,0]
	v_mfma_scale_f32_16x16x128_f8f6f4 v[200:203], v[148:155], v[180:187], 0, v136, v136 op_sel_hi:[0,0,0]
	s_setprio 0
	s_barrier
	v_mov_b32_e32 v128, v132
	s_nop 2
	ds_read_b128 v[96:99], v137
	ds_read_b128 v[100:103], v137 offset:1024
	ds_read_b128 v[104:107], v137 offset:2048
	ds_read_b128 v[108:111], v137 offset:3072
	s_nop 0
	v_mov_b32_e32 v128, v133
	s_nop 0
	s_barrier
	s_waitcnt lgkmcnt(0)
	s_setprio 1
	s_waitcnt lgkmcnt(0)
	v_mfma_scale_f32_16x16x128_f8f6f4 v[204:207], v[96:103], v[156:163], 0, v136, v136 op_sel_hi:[0,0,0]
	v_mfma_scale_f32_16x16x128_f8f6f4 v[156:159], v[104:111], v[156:163], 0, v136, v136 op_sel_hi:[0,0,0]
	s_mov_b32 m0, s41
	v_mfma_scale_f32_16x16x128_f8f6f4 v[160:163], v[96:103], v[164:171], 0, v136, v136 op_sel_hi:[0,0,0]
	global_load_lds_dwordx4 v132, s[18:19]
	v_mfma_scale_f32_16x16x128_f8f6f4 v[164:167], v[104:111], v[164:171], 0, v136, v136 op_sel_hi:[0,0,0]
	v_mfma_scale_f32_16x16x128_f8f6f4 v[168:171], v[96:103], v[172:179], 0, v136, v136 op_sel_hi:[0,0,0]
	s_mov_b32 m0, s42
	v_mfma_scale_f32_16x16x128_f8f6f4 v[172:175], v[104:111], v[172:179], 0, v136, v136 op_sel_hi:[0,0,0]
	global_load_lds_dwordx4 v133, s[18:19]
	v_mfma_scale_f32_16x16x128_f8f6f4 v[176:179], v[96:103], v[180:187], 0, v136, v136 op_sel_hi:[0,0,0]
	v_mfma_scale_f32_16x16x128_f8f6f4 v[180:183], v[104:111], v[180:187], 0, v136, v136 op_sel_hi:[0,0,0]
	s_setprio 0
	v_mov_b32_e32 v128, v132
	s_barrier
	s_nop 2
	ds_read_b128 v[64:67], v135 offset:16384
	ds_read_b128 v[68:71], v135 offset:17408
	ds_read_b128 v[72:75], v135 offset:18432
	ds_read_b128 v[76:79], v135 offset:19456
	ds_read_b128 v[80:83], v135 offset:20480
	ds_read_b128 v[84:87], v135 offset:21504
	ds_read_b128 v[88:91], v135 offset:22528
	ds_read_b128 v[92:95], v135 offset:23552
	s_nop 0
	v_mov_b32_e32 v128, v133
	s_nop 0
	s_barrier
	s_waitcnt lgkmcnt(0)
	s_setprio 1
	s_waitcnt lgkmcnt(0)
	v_mfma_scale_f32_16x16x128_f8f6f4 v[60:63], v[140:147], v[64:71], 0, v136, v136 op_sel_hi:[0,0,0]
	v_mfma_scale_f32_16x16x128_f8f6f4 v[56:59], v[148:155], v[64:71], 0, v136, v136 op_sel_hi:[0,0,0]
	s_mov_b32 m0, s25
	v_mfma_scale_f32_16x16x128_f8f6f4 v[52:55], v[140:147], v[72:79], 0, v136, v136 op_sel_hi:[0,0,0]
	global_load_lds_dwordx4 v132, s[20:21]
	v_mfma_scale_f32_16x16x128_f8f6f4 v[48:51], v[148:155], v[72:79], 0, v136, v136 op_sel_hi:[0,0,0]
	v_mfma_scale_f32_16x16x128_f8f6f4 v[184:187], v[140:147], v[80:87], 0, v136, v136 op_sel_hi:[0,0,0]
	s_mov_b32 m0, s26
	v_mfma_scale_f32_16x16x128_f8f6f4 v[208:211], v[148:155], v[80:87], 0, v136, v136 op_sel_hi:[0,0,0]
	global_load_lds_dwordx4 v133, s[20:21]
	v_mfma_scale_f32_16x16x128_f8f6f4 v[212:215], v[140:147], v[88:95], 0, v136, v136 op_sel_hi:[0,0,0]
	v_mfma_scale_f32_16x16x128_f8f6f4 v[216:219], v[148:155], v[88:95], 0, v136, v136 op_sel_hi:[0,0,0]
	s_setprio 0
	s_barrier
	s_add_u32 s56, s18, 0x30000
	s_nop 3
	v_mov_b32_e32 v32, v132
	s_addc_u32 s57, s19, 0
	s_nop 0
	v_mov_b32_e32 v32, v133
	s_nop 0
	s_waitcnt vmcnt(4)
	s_barrier
	s_setprio 1
	v_mfma_scale_f32_16x16x128_f8f6f4 v[220:223], v[96:103], v[64:71], 0, v136, v136 op_sel_hi:[0,0,0]
	v_mfma_scale_f32_16x16x128_f8f6f4 v[224:227], v[104:111], v[64:71], 0, v136, v136 op_sel_hi:[0,0,0]
	s_mov_b32 m0, s43
	v_mfma_scale_f32_16x16x128_f8f6f4 v[228:231], v[96:103], v[72:79], 0, v136, v136 op_sel_hi:[0,0,0]
	global_load_lds_dwordx4 v132, s[56:57]
	v_mfma_scale_f32_16x16x128_f8f6f4 v[232:235], v[104:111], v[72:79], 0, v136, v136 op_sel_hi:[0,0,0]
	v_mfma_scale_f32_16x16x128_f8f6f4 v[236:239], v[96:103], v[80:87], 0, v136, v136 op_sel_hi:[0,0,0]
	s_mov_b32 m0, s44
	v_mfma_scale_f32_16x16x128_f8f6f4 v[240:243], v[104:111], v[80:87], 0, v136, v136 op_sel_hi:[0,0,0]
	global_load_lds_dwordx4 v133, s[56:57]
	v_mfma_scale_f32_16x16x128_f8f6f4 v[244:247], v[96:103], v[88:95], 0, v136, v136 op_sel_hi:[0,0,0]
	v_mfma_scale_f32_16x16x128_f8f6f4 v[248:251], v[104:111], v[88:95], 0, v136, v136 op_sel_hi:[0,0,0]
	s_setprio 0
	s_barrier
	s_nop 4
	ds_read_b128 v[0:3], v138
	ds_read_b128 v[4:7], v138 offset:1024
	ds_read_b128 v[8:11], v138 offset:2048
	ds_read_b128 v[12:15], v138 offset:3072
	s_add_u32 s56, s20, 0x30000
	v_mov_b32_e32 v64, v132
	ds_read_b128 v[16:19], v135 offset:32768
	ds_read_b128 v[20:23], v135 offset:33792
	ds_read_b128 v[24:27], v135 offset:34816
	ds_read_b128 v[28:31], v135 offset:35840
	ds_read_b128 v[32:35], v135 offset:36864
	ds_read_b128 v[36:39], v135 offset:37888
	ds_read_b128 v[40:43], v135 offset:38912
	ds_read_b128 v[44:47], v135 offset:39936
	s_addc_u32 s57, s21, 0
	s_nop 0
	v_mov_b32_e32 v64, v133
	s_nop 0
	s_waitcnt lgkmcnt(8)
	s_barrier
	s_waitcnt lgkmcnt(0)
	s_setprio 1
	s_waitcnt lgkmcnt(0)
	v_mfma_scale_f32_16x16x128_f8f6f4 v[124:127], v[0:7], v[16:23], v[124:127], v136, v136 op_sel_hi:[0,0,0]
	v_mfma_scale_f32_16x16x128_f8f6f4 v[120:123], v[8:15], v[16:23], v[120:123], v136, v136 op_sel_hi:[0,0,0]
	s_mov_b32 m0, s27
	v_mfma_scale_f32_16x16x128_f8f6f4 v[116:119], v[0:7], v[24:31], v[116:119], v136, v136 op_sel_hi:[0,0,0]
	global_load_lds_dwordx4 v132, s[56:57]
	v_mfma_scale_f32_16x16x128_f8f6f4 v[112:115], v[8:15], v[24:31], v[112:115], v136, v136 op_sel_hi:[0,0,0]
	v_mfma_scale_f32_16x16x128_f8f6f4 v[108:111], v[0:7], v[32:39], v[188:191], v136, v136 op_sel_hi:[0,0,0]
	s_mov_b32 m0, s28
	v_mfma_scale_f32_16x16x128_f8f6f4 v[104:107], v[8:15], v[32:39], v[192:195], v136, v136 op_sel_hi:[0,0,0]
	global_load_lds_dwordx4 v133, s[56:57]
	v_mfma_scale_f32_16x16x128_f8f6f4 v[100:103], v[0:7], v[40:47], v[196:199], v136, v136 op_sel_hi:[0,0,0]
	v_mfma_scale_f32_16x16x128_f8f6f4 v[96:99], v[8:15], v[40:47], v[200:203], v136, v136 op_sel_hi:[0,0,0]
	s_setprio 0
	s_barrier
	v_mov_b32_e32 v128, v132
	ds_read_b128 v[140:143], v139
	ds_read_b128 v[144:147], v139 offset:1024
	ds_read_b128 v[148:151], v139 offset:2048
	ds_read_b128 v[152:155], v139 offset:3072
	v_lshl_add_u64 v[64:65], s[18:19], 0, v[128:129]
	v_lshl_add_u64 v[64:65], v[64:65], 0, s[4:5]
	v_mov_b32_e32 v128, v133
	v_lshl_add_u64 v[64:65], s[18:19], 0, v[128:129]
	v_lshl_add_u64 v[64:65], v[64:65], 0, s[4:5]
	s_barrier
	s_waitcnt lgkmcnt(0)
	s_setprio 1
	s_waitcnt lgkmcnt(0)
	v_mfma_scale_f32_16x16x128_f8f6f4 v[92:95], v[140:147], v[16:23], v[204:207], v136, v136 op_sel_hi:[0,0,0]
	v_mfma_scale_f32_16x16x128_f8f6f4 v[88:91], v[148:155], v[16:23], v[156:159], v136, v136 op_sel_hi:[0,0,0]
	s_add_u32 s98, s18, s4
	s_addc_u32 s99, s19, s5
	s_mov_b32 m0, s46
	v_mfma_scale_f32_16x16x128_f8f6f4 v[84:87], v[140:147], v[24:31], v[160:163], v136, v136 op_sel_hi:[0,0,0]
	global_load_lds_dwordx4 v132, s[98:99]
	v_mfma_scale_f32_16x16x128_f8f6f4 v[80:83], v[148:155], v[24:31], v[164:167], v136, v136 op_sel_hi:[0,0,0]
	v_mfma_scale_f32_16x16x128_f8f6f4 v[76:79], v[140:147], v[32:39], v[168:171], v136, v136 op_sel_hi:[0,0,0]
	s_mov_b32 m0, s47
	v_mfma_scale_f32_16x16x128_f8f6f4 v[72:75], v[148:155], v[32:39], v[172:175], v136, v136 op_sel_hi:[0,0,0]
	global_load_lds_dwordx4 v133, s[98:99]
	v_mfma_scale_f32_16x16x128_f8f6f4 v[68:71], v[140:147], v[40:47], v[176:179], v136, v136 op_sel_hi:[0,0,0]
	v_mfma_scale_f32_16x16x128_f8f6f4 v[64:67], v[148:155], v[40:47], v[180:183], v136, v136 op_sel_hi:[0,0,0]
	s_setprio 0
	v_mov_b32_e32 v128, v132
	s_barrier
	ds_read_b128 v[16:19], v135 offset:49152
	ds_read_b128 v[20:23], v135 offset:50176
	ds_read_b128 v[156:159], v135 offset:51200
	ds_read_b128 v[160:163], v135 offset:52224
	ds_read_b128 v[164:167], v135 offset:53248
	ds_read_b128 v[168:171], v135 offset:54272
	ds_read_b128 v[172:175], v135 offset:55296
	ds_read_b128 v[176:179], v135 offset:56320
	v_lshl_add_u64 v[24:25], s[20:21], 0, v[128:129]
	v_lshl_add_u64 v[24:25], v[24:25], 0, s[4:5]
	v_mov_b32_e32 v128, v133
	v_lshl_add_u64 v[24:25], s[20:21], 0, v[128:129]
	v_lshl_add_u64 v[24:25], v[24:25], 0, s[4:5]
	s_barrier
	s_waitcnt lgkmcnt(0)
	s_setprio 1
	s_waitcnt lgkmcnt(0)
	v_mfma_scale_f32_16x16x128_f8f6f4 v[60:63], v[0:7], v[16:23], v[60:63], v136, v136 op_sel_hi:[0,0,0]
	v_mfma_scale_f32_16x16x128_f8f6f4 v[56:59], v[8:15], v[16:23], v[56:59], v136, v136 op_sel_hi:[0,0,0]
	s_add_u32 s98, s20, s4
	s_addc_u32 s99, s21, s5
	s_mov_b32 m0, s36
	v_mfma_scale_f32_16x16x128_f8f6f4 v[52:55], v[0:7], v[156:163], v[52:55], v136, v136 op_sel_hi:[0,0,0]
	global_load_lds_dwordx4 v132, s[98:99]
	v_mfma_scale_f32_16x16x128_f8f6f4 v[48:51], v[8:15], v[156:163], v[48:51], v136, v136 op_sel_hi:[0,0,0]
	v_mfma_scale_f32_16x16x128_f8f6f4 v[44:47], v[0:7], v[164:171], v[184:187], v136, v136 op_sel_hi:[0,0,0]
	s_mov_b32 m0, s37
	v_mfma_scale_f32_16x16x128_f8f6f4 v[40:43], v[8:15], v[164:171], v[208:211], v136, v136 op_sel_hi:[0,0,0]
	global_load_lds_dwordx4 v133, s[98:99]
	v_mfma_scale_f32_16x16x128_f8f6f4 v[36:39], v[0:7], v[172:179], v[212:215], v136, v136 op_sel_hi:[0,0,0]
	v_mfma_scale_f32_16x16x128_f8f6f4 v[32:35], v[8:15], v[172:179], v[216:219], v136, v136 op_sel_hi:[0,0,0]
	s_setprio 0
	s_barrier
	s_add_u32 s18, s18, 0x30080
	s_addc_u32 s19, s19, 0
	v_mov_b32_e32 v0, v132
	s_add_i32 s20, s45, s24
	s_nop 0
	v_mov_b32_e32 v0, v133
	s_nop 0
	s_waitcnt vmcnt(4)
	s_barrier
	s_setprio 1
	v_mfma_scale_f32_16x16x128_f8f6f4 v[28:31], v[140:147], v[16:23], v[220:223], v136, v136 op_sel_hi:[0,0,0]
	v_mfma_scale_f32_16x16x128_f8f6f4 v[24:27], v[148:155], v[16:23], v[224:227], v136, v136 op_sel_hi:[0,0,0]
	s_mov_b32 m0, s20
	v_mfma_scale_f32_16x16x128_f8f6f4 v[20:23], v[140:147], v[156:163], v[228:231], v136, v136 op_sel_hi:[0,0,0]
	global_load_lds_dwordx4 v132, s[18:19]
	v_mfma_scale_f32_16x16x128_f8f6f4 v[16:19], v[148:155], v[156:163], v[232:235], v136, v136 op_sel_hi:[0,0,0]
	v_mfma_scale_f32_16x16x128_f8f6f4 v[12:15], v[140:147], v[164:171], v[236:239], v136, v136 op_sel_hi:[0,0,0]
	s_add_i32 m0, s20, 0x2000
	v_mfma_scale_f32_16x16x128_f8f6f4 v[8:11], v[148:155], v[164:171], v[240:243], v136, v136 op_sel_hi:[0,0,0]
	global_load_lds_dwordx4 v133, s[18:19]
	v_mfma_scale_f32_16x16x128_f8f6f4 v[4:7], v[140:147], v[172:179], v[244:247], v136, v136 op_sel_hi:[0,0,0]
	v_mfma_scale_f32_16x16x128_f8f6f4 v[0:3], v[148:155], v[172:179], v[248:251], v136, v136 op_sel_hi:[0,0,0]
	s_setprio 0
	s_add_i32 s54, s54, 2
	s_add_u32 s16, s16, 0x100
	s_addc_u32 s17, s17, 0
	s_add_u32 s52, s52, 0x100
	s_addc_u32 s53, s53, 0
	s_cmp_gt_u32 s54, 9
	s_barrier
	s_cbranch_scc0 .LBB0_2382
	s_branch .Lpeel_exit_4

.Lpeel_exit_4:
	v_pk_mul_f32 v[140:141], v[124:125], s[8:9] op_sel_hi:[1,0]
	v_pk_mul_f32 v[120:121], v[120:121], s[8:9] op_sel_hi:[1,0]
	v_mov_b32_e32 v125, v129
	v_cvt_pk_fp8_f32 v125, v120, v121
	v_pk_mul_f32 v[120:121], v[126:127], s[8:9] op_sel_hi:[1,0]
	v_pk_mul_f32 v[116:117], v[116:117], s[8:9] op_sel_hi:[1,0]
	v_mov_b32_e32 v126, v129
	v_cvt_pk_fp8_f32 v126, v116, v117
	v_pk_mul_f32 v[112:113], v[112:113], s[8:9] op_sel_hi:[1,0]
	v_mov_b32_e32 v127, v129
	v_cvt_pk_fp8_f32 v127, v112, v113
	v_pk_mul_f32 v[112:113], v[118:119], s[8:9] op_sel_hi:[1,0]
	v_pk_mul_f32 v[104:105], v[104:105], s[8:9] op_sel_hi:[1,0]
	v_cvt_pk_fp8_f32 v126, v112, v113 op_sel:[0,0,1]
	v_pk_mul_f32 v[112:113], v[114:115], s[8:9] op_sel_hi:[1,0]
	v_pk_mul_f32 v[100:101], v[100:101], s[8:9] op_sel_hi:[1,0]
	v_cvt_pk_fp8_f32 v127, v112, v113 op_sel:[0,0,1]
	v_pk_mul_f32 v[112:113], v[108:109], s[8:9] op_sel_hi:[1,0]
	v_mov_b32_e32 v109, v129
	v_cvt_pk_fp8_f32 v109, v104, v105
	v_pk_mul_f32 v[104:105], v[110:111], s[8:9] op_sel_hi:[1,0]
	v_mov_b32_e32 v110, v129
	v_cvt_pk_fp8_f32 v110, v100, v101
	v_pk_mul_f32 v[100:101], v[92:93], s[8:9] op_sel_hi:[1,0]
	v_pk_mul_f32 v[88:89], v[88:89], s[8:9] op_sel_hi:[1,0]
	v_mov_b32_e32 v93, v129
	v_cvt_pk_fp8_f32 v93, v88, v89
	v_pk_mul_f32 v[88:89], v[94:95], s[8:9] op_sel_hi:[1,0]
	v_pk_mul_f32 v[84:85], v[84:85], s[8:9] op_sel_hi:[1,0]
	v_mov_b32_e32 v94, v129
	v_cvt_pk_fp8_f32 v94, v84, v85
	v_pk_mul_f32 v[80:81], v[80:81], s[8:9] op_sel_hi:[1,0]
	v_mov_b32_e32 v95, v129
	v_cvt_pk_fp8_f32 v95, v80, v81
	v_pk_mul_f32 v[80:81], v[86:87], s[8:9] op_sel_hi:[1,0]
	v_pk_mul_f32 v[72:73], v[72:73], s[8:9] op_sel_hi:[1,0]
	v_cvt_pk_fp8_f32 v94, v80, v81 op_sel:[0,0,1]
	v_pk_mul_f32 v[80:81], v[82:83], s[8:9] op_sel_hi:[1,0]
	v_pk_mul_f32 v[68:69], v[68:69], s[8:9] op_sel_hi:[1,0]
	v_cvt_pk_fp8_f32 v95, v80, v81 op_sel:[0,0,1]
	v_pk_mul_f32 v[80:81], v[76:77], s[8:9] op_sel_hi:[1,0]
	v_mov_b32_e32 v77, v129
	v_cvt_pk_fp8_f32 v77, v72, v73
	v_pk_mul_f32 v[72:73], v[78:79], s[8:9] op_sel_hi:[1,0]
	v_mov_b32_e32 v78, v129
	v_cvt_pk_fp8_f32 v78, v68, v69
	v_pk_mul_f32 v[64:65], v[64:65], s[8:9] op_sel_hi:[1,0]
	v_mov_b32_e32 v79, v129
	v_cvt_pk_fp8_f32 v79, v64, v65
	v_pk_mul_f32 v[64:65], v[70:71], s[8:9] op_sel_hi:[1,0]
	v_pk_mul_f32 v[56:57], v[56:57], s[8:9] op_sel_hi:[1,0]
	v_cvt_pk_fp8_f32 v78, v64, v65 op_sel:[0,0,1]
	v_pk_mul_f32 v[64:65], v[66:67], s[8:9] op_sel_hi:[1,0]
	v_pk_mul_f32 v[52:53], v[52:53], s[8:9] op_sel_hi:[1,0]
	v_cvt_pk_fp8_f32 v79, v64, v65 op_sel:[0,0,1]
	v_pk_mul_f32 v[64:65], v[60:61], s[8:9] op_sel_hi:[1,0]
	v_mov_b32_e32 v61, v129
	v_cvt_pk_fp8_f32 v61, v56, v57
	v_pk_mul_f32 v[56:57], v[62:63], s[8:9] op_sel_hi:[1,0]
	v_mov_b32_e32 v62, v129
	v_cvt_pk_fp8_f32 v62, v52, v53
	v_pk_mul_f32 v[48:49], v[48:49], s[8:9] op_sel_hi:[1,0]
	v_mov_b32_e32 v63, v129
	v_cvt_pk_fp8_f32 v63, v48, v49
	s_lshl_b32 s16, s50, 8
	v_pk_mul_f32 v[48:49], v[54:55], s[8:9] op_sel_hi:[1,0]
	s_add_i32 s16, s16, s34
	v_cvt_pk_fp8_f32 v62, v48, v49 op_sel:[0,0,1]
	v_pk_mul_f32 v[48:49], v[50:51], s[8:9] op_sel_hi:[1,0]
	s_lshl_b32 s18, s51, 8
	s_ashr_i32 s17, s16, 31
	v_cvt_pk_fp8_f32 v63, v48, v49 op_sel:[0,0,1]
	v_pk_mul_f32 v[48:49], v[44:45], s[8:9] op_sel_hi:[1,0]
	v_pk_mul_f32 v[40:41], v[40:41], s[8:9] op_sel_hi:[1,0]
	v_mov_b32_e32 v45, v129
	s_ashr_i32 s19, s18, 31
	s_lshl_b64 s[20:21], s[16:17], 11
	v_cvt_pk_fp8_f32 v45, v40, v41
	v_pk_mul_f32 v[40:41], v[46:47], s[8:9] op_sel_hi:[1,0]
	v_pk_mul_f32 v[36:37], v[36:37], s[8:9] op_sel_hi:[1,0]
	v_mov_b32_e32 v46, v129
	s_add_u32 s17, s31, s20
	v_cvt_pk_fp8_f32 v46, v36, v37
	v_pk_mul_f32 v[36:37], v[28:29], s[8:9] op_sel_hi:[1,0]
	v_pk_mul_f32 v[24:25], v[24:25], s[8:9] op_sel_hi:[1,0]
	v_mov_b32_e32 v29, v129
	s_addc_u32 s20, s33, s21
	v_cvt_pk_fp8_f32 v29, v24, v25
	v_pk_mul_f32 v[24:25], v[30:31], s[8:9] op_sel_hi:[1,0]
	v_pk_mul_f32 v[20:21], v[20:21], s[8:9] op_sel_hi:[1,0]
	v_mov_b32_e32 v30, v129
	s_add_u32 s17, s17, s18
	v_cvt_pk_fp8_f32 v30, v20, v21
	v_pk_mul_f32 v[16:17], v[16:17], s[8:9] op_sel_hi:[1,0]
	v_mov_b32_e32 v31, v129
	s_addc_u32 s21, s20, s19
	v_cvt_pk_fp8_f32 v31, v16, v17
	s_add_u32 s20, s17, s35
	s_addc_u32 s21, s21, 0
	s_addk_i32 s16, 0x80
	v_pk_mul_f32 v[16:17], v[22:23], s[8:9] op_sel_hi:[1,0]
	s_ashr_i32 s17, s16, 31
	v_cvt_pk_fp8_f32 v30, v16, v17 op_sel:[0,0,1]
	v_pk_mul_f32 v[16:17], v[18:19], s[8:9] op_sel_hi:[1,0]
	v_mov_b32_e32 v124, v129
	v_mov_b32_e32 v108, v129
	v_pk_mul_f32 v[96:97], v[96:97], s[8:9] op_sel_hi:[1,0]
	v_mov_b32_e32 v111, v129
	v_mov_b32_e32 v92, v129
	s_lshl_b64 s[16:17], s[16:17], 11
	v_mov_b32_e32 v60, v129
	v_mov_b32_e32 v44, v129
	v_mov_b32_e32 v28, v129
	v_cvt_pk_fp8_f32 v31, v16, v17 op_sel:[0,0,1]
	v_pk_mul_f32 v[16:17], v[12:13], s[8:9] op_sel_hi:[1,0]
	v_pk_mul_f32 v[8:9], v[8:9], s[8:9] op_sel_hi:[1,0]
	v_mov_b32_e32 v13, v129
	v_mbcnt_lo_u32_b32 v128, -1, 0
	v_mbcnt_hi_u32_b32 v128, -1, v128
	v_cvt_pk_fp8_f32 v124, v140, v141
	v_ashrrev_i32_e32 v130, 1, v128
	v_cvt_pk_fp8_f32 v108, v112, v113
	v_cvt_pk_fp8_f32 v111, v96, v97
	v_cvt_pk_fp8_f32 v92, v100, v101
	v_mov_b32_e32 v76, v129
	v_cvt_pk_fp8_f32 v60, v64, v65
	v_cvt_pk_fp8_f32 v44, v48, v49
	v_pk_mul_f32 v[32:33], v[32:33], s[8:9] op_sel_hi:[1,0]
	v_mov_b32_e32 v47, v129
	s_add_u32 s16, s31, s16
	v_cvt_pk_fp8_f32 v28, v36, v37
	v_mov_b32_e32 v12, v129
	v_cvt_pk_fp8_f32 v13, v8, v9
	v_pk_mul_f32 v[8:9], v[14:15], s[8:9] op_sel_hi:[1,0]
	v_pk_mul_f32 v[4:5], v[4:5], s[8:9] op_sel_hi:[1,0]
	v_mov_b32_e32 v14, v129
	v_bfi_b32 v130, -16, v130, v128
	v_cvt_pk_fp8_f32 v76, v80, v81
	v_cvt_pk_fp8_f32 v47, v32, v33
	s_addc_u32 s17, s33, s17
	v_cvt_pk_fp8_f32 v12, v16, v17
	v_cvt_pk_fp8_f32 v14, v4, v5
	v_pk_mul_f32 v[0:1], v[0:1], s[8:9] op_sel_hi:[1,0]
	v_mov_b32_e32 v15, v129
	v_ashrrev_i32_e32 v131, 31, v130
	v_pk_mul_f32 v[96:97], v[102:103], s[8:9] op_sel_hi:[1,0]
	s_add_u32 s16, s16, s18
	v_cvt_pk_fp8_f32 v15, v0, v1
	v_lshlrev_b64 v[130:131], 11, v[130:131]
	v_cvt_pk_fp8_f32 v110, v96, v97 op_sel:[0,0,1]
	v_pk_mul_f32 v[96:97], v[98:99], s[8:9] op_sel_hi:[1,0]
	v_pk_mul_f32 v[32:33], v[38:39], s[8:9] op_sel_hi:[1,0]
	s_addc_u32 s17, s17, s19
	v_and_b32_e32 v128, 16, v128
	v_cvt_pk_fp8_f32 v124, v120, v121 op_sel:[0,0,1]
	v_pk_mul_f32 v[120:121], v[122:123], s[8:9] op_sel_hi:[1,0]
	v_cvt_pk_fp8_f32 v108, v104, v105 op_sel:[0,0,1]
	v_pk_mul_f32 v[104:105], v[106:107], s[8:9] op_sel_hi:[1,0]
	v_cvt_pk_fp8_f32 v111, v96, v97 op_sel:[0,0,1]
	v_lshl_add_u64 v[96:97], s[20:21], 0, v[130:131]
	v_cvt_pk_fp8_f32 v92, v88, v89 op_sel:[0,0,1]
	v_pk_mul_f32 v[88:89], v[90:91], s[8:9] op_sel_hi:[1,0]
	v_cvt_pk_fp8_f32 v60, v56, v57 op_sel:[0,0,1]
	v_pk_mul_f32 v[56:57], v[58:59], s[8:9] op_sel_hi:[1,0]
	v_cvt_pk_fp8_f32 v44, v40, v41 op_sel:[0,0,1]
	v_pk_mul_f32 v[40:41], v[42:43], s[8:9] op_sel_hi:[1,0]
	v_cvt_pk_fp8_f32 v46, v32, v33 op_sel:[0,0,1]
	v_pk_mul_f32 v[32:33], v[34:35], s[8:9] op_sel_hi:[1,0]
	s_add_u32 s16, s16, s35
	v_cvt_pk_fp8_f32 v28, v24, v25 op_sel:[0,0,1]
	v_pk_mul_f32 v[24:25], v[26:27], s[8:9] op_sel_hi:[1,0]
	v_pk_mul_f32 v[0:1], v[6:7], s[8:9] op_sel_hi:[1,0]
	v_cvt_pk_fp8_f32 v125, v120, v121 op_sel:[0,0,1]
	v_cvt_pk_fp8_f32 v109, v104, v105 op_sel:[0,0,1]
	v_lshl_add_u64 v[96:97], v[96:97], 0, v[128:129]
	v_cvt_pk_fp8_f32 v93, v88, v89 op_sel:[0,0,1]
	v_cvt_pk_fp8_f32 v76, v72, v73 op_sel:[0,0,1]
	v_pk_mul_f32 v[72:73], v[74:75], s[8:9] op_sel_hi:[1,0]
	v_cvt_pk_fp8_f32 v61, v56, v57 op_sel:[0,0,1]
	v_cvt_pk_fp8_f32 v45, v40, v41 op_sel:[0,0,1]
	v_cvt_pk_fp8_f32 v47, v32, v33 op_sel:[0,0,1]
	s_addc_u32 s17, s17, 0
	v_cvt_pk_fp8_f32 v29, v24, v25 op_sel:[0,0,1]
	v_cvt_pk_fp8_f32 v12, v8, v9 op_sel:[0,0,1]
	v_pk_mul_f32 v[8:9], v[10:11], s[8:9] op_sel_hi:[1,0]
	v_cvt_pk_fp8_f32 v14, v0, v1 op_sel:[0,0,1]
	v_pk_mul_f32 v[0:1], v[2:3], s[8:9] op_sel_hi:[1,0]
	v_add_co_u32_e32 v98, vcc, s30, v96
	v_cvt_pk_fp8_f32 v77, v72, v73 op_sel:[0,0,1]
	v_lshl_add_u64 v[32:33], s[16:17], 0, v[130:131]
	v_cvt_pk_fp8_f32 v13, v8, v9 op_sel:[0,0,1]
	v_cvt_pk_fp8_f32 v15, v0, v1 op_sel:[0,0,1]
	v_addc_co_u32_e32 v99, vcc, 0, v97, vcc
	v_lshl_add_u64 v[32:33], v[32:33], 0, v[128:129]
	v_add_co_u32_e32 v34, vcc, s30, v32
	v_permlane32_swap_b32_e32 v124, v126
	v_permlane32_swap_b32_e32 v125, v127
	v_permlane32_swap_b32_e32 v108, v110
	v_permlane32_swap_b32_e32 v109, v111
	v_permlane32_swap_b32_e32 v92, v94
	v_permlane32_swap_b32_e32 v93, v95
	v_permlane32_swap_b32_e32 v60, v62
	v_permlane32_swap_b32_e32 v61, v63
	v_permlane32_swap_b32_e32 v44, v46
	v_permlane32_swap_b32_e32 v45, v47
	v_addc_co_u32_e32 v35, vcc, 0, v33, vcc
	v_permlane32_swap_b32_e32 v28, v30
	v_permlane32_swap_b32_e32 v29, v31
	v_permlane16_swap_b32_e32 v124, v125
	v_permlane16_swap_b32_e32 v126, v127
	v_permlane16_swap_b32_e32 v108, v109
	v_permlane16_swap_b32_e32 v110, v111
	v_permlane16_swap_b32_e32 v92, v93
	v_permlane16_swap_b32_e32 v94, v95
	v_permlane32_swap_b32_e32 v76, v78
	v_permlane32_swap_b32_e32 v77, v79
	v_permlane16_swap_b32_e32 v60, v61
	v_permlane16_swap_b32_e32 v62, v63
	v_permlane16_swap_b32_e32 v44, v45
	v_permlane16_swap_b32_e32 v46, v47
	v_permlane16_swap_b32_e32 v28, v29
	v_permlane16_swap_b32_e32 v30, v31
	v_permlane32_swap_b32_e32 v12, v14
	v_permlane32_swap_b32_e32 v13, v15
	s_and_b64 vcc, exec, s[10:11]
	s_mov_b32 s51, s49
	s_mov_b32 s50, s48
	s_mov_b64 s[18:19], s[12:13]
	s_mov_b64 s[16:17], s[14:15]
	global_store_dwordx4 v[96:97], v[124:127], off
	global_store_dwordx4 v[98:99], v[108:111], off
	v_permlane16_swap_b32_e32 v76, v77
	v_permlane16_swap_b32_e32 v78, v79
	global_store_dwordx4 v[96:97], v[92:95], off offset:128
	global_store_dwordx4 v[98:99], v[76:79], off offset:128
	global_store_dwordx4 v[32:33], v[60:63], off
	global_store_dwordx4 v[34:35], v[44:47], off
	v_permlane16_swap_b32_e32 v12, v13
	v_permlane16_swap_b32_e32 v14, v15
	global_store_dwordx4 v[32:33], v[28:31], off offset:128
	global_store_dwordx4 v[34:35], v[12:15], off offset:128
	s_cbranch_vccz .LBB0_2377
	s_waitcnt vmcnt(0)
	v_readlane_b32 s0, v252, 2
	s_cmpk_gt_u32 s0, 0xff
	s_cbranch_scc1 .LBB0_2386
	s_barrier

.LBB0_3993:
	v_mbcnt_lo_u32_b32 v2, -1, 0
	v_mbcnt_hi_u32_b32 v2, -1, v2
	s_lshl_b32 s22, s10, 8
	v_add_u32_e32 v0, s58, v2
	v_ashrrev_i32_e32 v0, 1, v0
	v_add_u32_e32 v0, s22, v0
	v_ashrrev_i32_e32 v1, 31, v0
	v_readlane_b32 s8, v253, 54
	v_lshlrev_b64 v[0:1], 6, v[0:1]
	v_readlane_b32 s9, v253, 55
	v_lshlrev_b32_e32 v2, 4, v2
	v_and_b32_e32 v170, 16, v2
	v_lshl_add_u64 v[0:1], s[8:9], 0, v[0:1]
	s_lshl_b32 s8, s23, 3
	s_ashr_i32 s9, s8, 31
	v_lshl_add_u64 v[0:1], s[8:9], 2, v[0:1]
	v_lshl_add_u64 v[0:1], v[0:1], 0, v[170:171]
	s_add_i32 m0, s3, 0x22000
	v_readlane_b32 s8, v252, 31
	global_load_lds_dwordx4 v[0:1], off
	v_mov_b32_e32 v123, 0
	v_readlane_b32 s9, v252, 32
	s_andn2_b64 vcc, exec, s[8:9]
	s_waitcnt vmcnt(0)
	s_cbranch_vccnz .LBB0_3996
	s_add_u32 s4, s4, 0x20080
	s_addc_u32 s5, s5, 0
	s_add_u32 s25, s6, 0x100
	v_mov_b32_e32 v0, 0
	s_addc_u32 s27, s7, 0
	s_mov_b32 s6, 0
.Lpeel_5:
	s_add_i32 s34, s6, 2
	s_add_u32 s8, s4, 0xfffe0080
	s_addc_u32 s7, s5, -1
	s_add_i32 s30, 0, 0x10000
	v_add_u32_e32 v140, s30, v200
	ds_read_b128 v[128:131], v140
	ds_read_b128 v[132:135], v140 offset:1024
	ds_read_b128 v[136:139], v140 offset:2048
	ds_read_b128 v[140:143], v140 offset:3072
	s_cmp_eq_u32 s12, s6
	s_cselect_b32 s6, s52, s8
	s_cselect_b32 s7, s53, s7
	s_cselect_b32 s9, s55, s27
	s_cselect_b32 s8, s54, s25
	v_mov_b32_e32 v168, v169
	ds_read_b128 v[144:147], v182
	ds_read_b128 v[148:151], v182 offset:1024
	ds_read_b128 v[152:155], v182 offset:2048
	ds_read_b128 v[156:159], v182 offset:3072
	ds_read_b128 v[160:163], v182 offset:4096
	ds_read_b128 v[164:167], v182 offset:5120
	ds_read_b128 v[184:187], v182 offset:6144
	ds_read_b128 v[188:191], v182 offset:7168
	s_nop 0
	v_mov_b32_e32 v168, v181
	s_nop 0
	s_waitcnt lgkmcnt(8)
	s_barrier
	s_waitcnt lgkmcnt(0)
	s_setprio 1
	s_waitcnt lgkmcnt(0)
	v_mfma_scale_f32_16x16x128_f8f6f4 v[120:123], v[128:135], v[144:151], 0, v183, v183 op_sel_hi:[0,0,0]
	v_mov_b32_e32 v170, v200
	v_mfma_scale_f32_16x16x128_f8f6f4 v[124:127], v[136:143], v[144:151], 0, v183, v183 op_sel_hi:[0,0,0]
	s_add_i32 m0, s3, 0xc000
	v_mfma_scale_f32_16x16x128_f8f6f4 v[200:203], v[136:143], v[160:167], 0, v183, v183 op_sel_hi:[0,0,0]
	global_load_lds_dwordx4 v169, s[4:5]
	v_mfma_scale_f32_16x16x128_f8f6f4 v[176:179], v[128:135], v[152:159], 0, v183, v183 op_sel_hi:[0,0,0]
	v_mfma_scale_f32_16x16x128_f8f6f4 v[192:195], v[136:143], v[152:159], 0, v183, v183 op_sel_hi:[0,0,0]
	s_add_i32 m0, s3, 0xe000
	v_mfma_scale_f32_16x16x128_f8f6f4 v[196:199], v[128:135], v[160:167], 0, v183, v183 op_sel_hi:[0,0,0]
	global_load_lds_dwordx4 v181, s[4:5]
	v_mfma_scale_f32_16x16x128_f8f6f4 v[204:207], v[128:135], v[184:191], 0, v183, v183 op_sel_hi:[0,0,0]
	v_mfma_scale_f32_16x16x128_f8f6f4 v[208:211], v[136:143], v[184:191], 0, v183, v183 op_sel_hi:[0,0,0]
	s_setprio 0
	s_barrier
	s_add_i32 s35, 0, 0x14000
	s_nop 1
	v_add_u32_e32 v92, s35, v170
	v_mov_b32_e32 v104, v180
	s_add_i32 s30, s30, s33
	ds_read_b128 v[72:75], v92
	ds_read_b128 v[76:79], v92 offset:1024
	ds_read_b128 v[88:91], v92 offset:2048
	ds_read_b128 v[92:95], v92 offset:3072
	s_mov_b32 m0, s30
	s_nop 0
	global_load_lds_dwordx4 v104, s[8:9]
	v_mov_b32_e32 v104, v212
	s_add_i32 m0, s30, 0x2000
	s_nop 0
	global_load_lds_dwordx4 v104, s[8:9]
	s_barrier
	s_waitcnt lgkmcnt(0)
	s_setprio 1
	s_waitcnt lgkmcnt(0)
	v_mfma_scale_f32_16x16x128_f8f6f4 v[116:119], v[144:151], v[72:79], 0, v183, v183 op_sel_hi:[0,0,0]
	v_mov_b32_e32 v168, v212
	v_mfma_scale_f32_16x16x128_f8f6f4 v[112:115], v[144:151], v[88:95], 0, v183, v183 op_sel_hi:[0,0,0]
	v_mfma_scale_f32_16x16x128_f8f6f4 v[212:215], v[152:159], v[72:79], 0, v183, v183 op_sel_hi:[0,0,0]
	v_mfma_scale_f32_16x16x128_f8f6f4 v[216:219], v[152:159], v[88:95], 0, v183, v183 op_sel_hi:[0,0,0]
	v_mfma_scale_f32_16x16x128_f8f6f4 v[220:223], v[160:167], v[72:79], 0, v183, v183 op_sel_hi:[0,0,0]
	v_mfma_scale_f32_16x16x128_f8f6f4 v[160:163], v[160:167], v[88:95], 0, v183, v183 op_sel_hi:[0,0,0]
	v_mfma_scale_f32_16x16x128_f8f6f4 v[164:167], v[184:191], v[72:79], 0, v183, v183 op_sel_hi:[0,0,0]
	v_mfma_scale_f32_16x16x128_f8f6f4 v[184:187], v[184:191], v[88:95], 0, v183, v183 op_sel_hi:[0,0,0]
	s_setprio 0
	v_mov_b32_e32 v144, v169
	s_barrier
	s_nop 2
	ds_read_b128 v[64:67], v182 offset:16384
	ds_read_b128 v[68:71], v182 offset:17408
	ds_read_b128 v[80:83], v182 offset:18432
	ds_read_b128 v[84:87], v182 offset:19456
	ds_read_b128 v[96:99], v182 offset:20480
	ds_read_b128 v[100:103], v182 offset:21504
	ds_read_b128 v[104:107], v182 offset:22528
	ds_read_b128 v[108:111], v182 offset:23552
	s_nop 0
	v_mov_b32_e32 v144, v181
	s_nop 0
	s_barrier
	s_waitcnt lgkmcnt(0)
	s_setprio 1
	s_waitcnt lgkmcnt(0)
	v_mfma_scale_f32_16x16x128_f8f6f4 v[224:227], v[128:135], v[64:71], 0, v183, v183 op_sel_hi:[0,0,0]
	v_mfma_scale_f32_16x16x128_f8f6f4 v[228:231], v[136:143], v[64:71], 0, v183, v183 op_sel_hi:[0,0,0]
	s_mov_b32 m0, s3
	v_mfma_scale_f32_16x16x128_f8f6f4 v[232:235], v[128:135], v[80:87], 0, v183, v183 op_sel_hi:[0,0,0]
	global_load_lds_dwordx4 v169, s[6:7]
	v_mfma_scale_f32_16x16x128_f8f6f4 v[236:239], v[136:143], v[80:87], 0, v183, v183 op_sel_hi:[0,0,0]
	v_mfma_scale_f32_16x16x128_f8f6f4 v[240:243], v[128:135], v[96:103], 0, v183, v183 op_sel_hi:[0,0,0]
	s_mov_b32 m0, s11
	v_mfma_scale_f32_16x16x128_f8f6f4 v[244:247], v[136:143], v[96:103], 0, v183, v183 op_sel_hi:[0,0,0]
	global_load_lds_dwordx4 v181, s[6:7]
	v_mfma_scale_f32_16x16x128_f8f6f4 v[248:251], v[128:135], v[104:111], 0, v183, v183 op_sel_hi:[0,0,0]
	v_mfma_scale_f32_16x16x128_f8f6f4 v[172:175], v[136:143], v[104:111], 0, v183, v183 op_sel_hi:[0,0,0]
	s_setprio 0
	s_barrier
	s_add_u32 s30, s8, s20
	s_addc_u32 s31, s9, s21
	s_nop 2
	v_mov_b32_e32 v8, v180
	s_add_i32 s35, s35, s33
	s_mov_b32 s100, s35
	s_nop 0
	v_mov_b32_e32 v8, v168
	s_add_i32 s101, s35, 0x2000
	s_nop 0
	s_waitcnt vmcnt(4)
	s_barrier
	s_setprio 1
	v_mfma_scale_f32_16x16x128_f8f6f4 v[52:55], v[64:71], v[72:79], 0, v183, v183 op_sel_hi:[0,0,0]
	v_mfma_scale_f32_16x16x128_f8f6f4 v[48:51], v[64:71], v[88:95], 0, v183, v183 op_sel_hi:[0,0,0]
	s_mov_b32 m0, s100
	v_mfma_scale_f32_16x16x128_f8f6f4 v[36:39], v[80:87], v[72:79], 0, v183, v183 op_sel_hi:[0,0,0]
	global_load_lds_dwordx4 v180, s[30:31]
	v_mfma_scale_f32_16x16x128_f8f6f4 v[32:35], v[80:87], v[88:95], 0, v183, v183 op_sel_hi:[0,0,0]
	v_mfma_scale_f32_16x16x128_f8f6f4 v[20:23], v[96:103], v[72:79], 0, v183, v183 op_sel_hi:[0,0,0]
	s_mov_b32 m0, s101
	v_mfma_scale_f32_16x16x128_f8f6f4 v[16:19], v[96:103], v[88:95], 0, v183, v183 op_sel_hi:[0,0,0]
	global_load_lds_dwordx4 v168, s[30:31]
	v_mfma_scale_f32_16x16x128_f8f6f4 v[4:7], v[104:111], v[72:79], 0, v183, v183 op_sel_hi:[0,0,0]
	v_mfma_scale_f32_16x16x128_f8f6f4 v[0:3], v[104:111], v[88:95], 0, v183, v183 op_sel_hi:[0,0,0]
	s_setprio 0
	s_add_i32 s35, 0, 0x18000
	v_add_u32_e32 v24, s35, v170
	s_barrier
	ds_read_b128 v[8:11], v24
	ds_read_b128 v[12:15], v24 offset:1024
	ds_read_b128 v[128:131], v24 offset:2048
	ds_read_b128 v[132:135], v24 offset:3072
	s_add_u32 s36, s6, 0x20000
	v_mov_b32_e32 v64, v169
	ds_read_b128 v[24:27], v182 offset:32768
	ds_read_b128 v[28:31], v182 offset:33792
	ds_read_b128 v[40:43], v182 offset:34816
	ds_read_b128 v[44:47], v182 offset:35840
	ds_read_b128 v[56:59], v182 offset:36864
	ds_read_b128 v[60:63], v182 offset:37888
	ds_read_b128 v[136:139], v182 offset:38912
	ds_read_b128 v[140:143], v182 offset:39936
	s_addc_u32 s37, s7, 0
	s_nop 0
	v_mov_b32_e32 v64, v181
	s_nop 0
	s_waitcnt lgkmcnt(8)
	s_barrier
	s_waitcnt lgkmcnt(0)
	s_setprio 1
	s_waitcnt lgkmcnt(0)
	v_mfma_scale_f32_16x16x128_f8f6f4 v[120:123], v[8:15], v[24:31], v[120:123], v183, v183 op_sel_hi:[0,0,0]
	v_mfma_scale_f32_16x16x128_f8f6f4 v[124:127], v[128:135], v[24:31], v[124:127], v183, v183 op_sel_hi:[0,0,0]
	s_mov_b32 m0, s14
	v_mfma_scale_f32_16x16x128_f8f6f4 v[108:111], v[8:15], v[40:47], v[176:179], v183, v183 op_sel_hi:[0,0,0]
	global_load_lds_dwordx4 v169, s[36:37]
	v_mfma_scale_f32_16x16x128_f8f6f4 v[104:107], v[128:135], v[40:47], v[192:195], v183, v183 op_sel_hi:[0,0,0]
	v_mfma_scale_f32_16x16x128_f8f6f4 v[92:95], v[8:15], v[56:63], v[196:199], v183, v183 op_sel_hi:[0,0,0]
	s_mov_b32 m0, s15
	v_mfma_scale_f32_16x16x128_f8f6f4 v[88:91], v[128:135], v[56:63], v[200:203], v183, v183 op_sel_hi:[0,0,0]
	global_load_lds_dwordx4 v181, s[36:37]
	v_mfma_scale_f32_16x16x128_f8f6f4 v[76:79], v[8:15], v[136:143], v[204:207], v183, v183 op_sel_hi:[0,0,0]
	s_nop 5
	v_mov_b32_e32 v200, v170
	v_mfma_scale_f32_16x16x128_f8f6f4 v[72:75], v[128:135], v[136:143], v[208:211], v183, v183 op_sel_hi:[0,0,0]
	s_setprio 0
	s_barrier
	s_add_i32 s36, 0, 0x1c000
	v_add_u32_e32 v64, s36, v200
	v_mov_b32_e32 v170, v180
	ds_read_b128 v[144:147], v64
	ds_read_b128 v[148:151], v64 offset:1024
	ds_read_b128 v[152:155], v64 offset:2048
	ds_read_b128 v[156:159], v64 offset:3072
	s_add_i32 s35, s35, s33
	v_lshl_add_u64 v[64:65], s[8:9], 0, v[170:171]
	v_lshl_add_u64 v[64:65], v[64:65], 0, s[62:63]
	v_mov_b32_e32 v170, v168
	v_lshl_add_u64 v[64:65], s[8:9], 0, v[170:171]
	v_lshl_add_u64 v[64:65], v[64:65], 0, s[62:63]
	s_barrier
	s_waitcnt lgkmcnt(0)
	s_setprio 1
	s_waitcnt lgkmcnt(0)
	v_mfma_scale_f32_16x16x128_f8f6f4 v[116:119], v[24:31], v[144:151], v[116:119], v183, v183 op_sel_hi:[0,0,0]
	v_mfma_scale_f32_16x16x128_f8f6f4 v[112:115], v[24:31], v[152:159], v[112:115], v183, v183 op_sel_hi:[0,0,0]
	s_add_u32 s98, s8, s62
	s_addc_u32 s99, s9, s63
	s_mov_b32 m0, s35
	v_mfma_scale_f32_16x16x128_f8f6f4 v[100:103], v[40:47], v[144:151], v[212:215], v183, v183 op_sel_hi:[0,0,0]
	global_load_lds_dwordx4 v180, s[98:99]
	v_mfma_scale_f32_16x16x128_f8f6f4 v[96:99], v[40:47], v[152:159], v[216:219], v183, v183 op_sel_hi:[0,0,0]
	s_nop 5
	v_mov_b32_e32 v212, v168
	v_mfma_scale_f32_16x16x128_f8f6f4 v[84:87], v[56:63], v[144:151], v[220:223], v183, v183 op_sel_hi:[0,0,0]
	s_add_i32 m0, s35, 0x2000
	v_mfma_scale_f32_16x16x128_f8f6f4 v[80:83], v[56:63], v[152:159], v[160:163], v183, v183 op_sel_hi:[0,0,0]
	global_load_lds_dwordx4 v168, s[98:99]
	v_mfma_scale_f32_16x16x128_f8f6f4 v[68:71], v[136:143], v[144:151], v[164:167], v183, v183 op_sel_hi:[0,0,0]
	v_mfma_scale_f32_16x16x128_f8f6f4 v[64:67], v[136:143], v[152:159], v[184:187], v183, v183 op_sel_hi:[0,0,0]
	s_setprio 0
	v_mov_b32_e32 v170, v169
	s_barrier
	ds_read_b128 v[136:139], v182 offset:49152
	ds_read_b128 v[140:143], v182 offset:50176
	ds_read_b128 v[160:163], v182 offset:51200
	ds_read_b128 v[164:167], v182 offset:52224
	ds_read_b128 v[184:187], v182 offset:53248
	ds_read_b128 v[188:191], v182 offset:54272
	ds_read_b128 v[192:195], v182 offset:55296
	ds_read_b128 v[196:199], v182 offset:56320
	v_lshl_add_u64 v[24:25], s[6:7], 0, v[170:171]
	v_lshl_add_u64 v[24:25], v[24:25], 0, s[62:63]
	v_mov_b32_e32 v170, v181
	v_lshl_add_u64 v[24:25], s[6:7], 0, v[170:171]
	v_lshl_add_u64 v[24:25], v[24:25], 0, s[62:63]
	s_barrier
	s_waitcnt lgkmcnt(0)
	s_setprio 1
	s_waitcnt lgkmcnt(0)
	v_mfma_scale_f32_16x16x128_f8f6f4 v[60:63], v[8:15], v[136:143], v[224:227], v183, v183 op_sel_hi:[0,0,0]
	v_mfma_scale_f32_16x16x128_f8f6f4 v[56:59], v[128:135], v[136:143], v[228:231], v183, v183 op_sel_hi:[0,0,0]
	s_add_u32 s98, s6, s62
	s_addc_u32 s99, s7, s63
	s_mov_b32 m0, s16
	v_mfma_scale_f32_16x16x128_f8f6f4 v[44:47], v[8:15], v[160:167], v[232:235], v183, v183 op_sel_hi:[0,0,0]
	global_load_lds_dwordx4 v169, s[98:99]
	v_mfma_scale_f32_16x16x128_f8f6f4 v[40:43], v[128:135], v[160:167], v[236:239], v183, v183 op_sel_hi:[0,0,0]
	v_mfma_scale_f32_16x16x128_f8f6f4 v[28:31], v[8:15], v[184:191], v[240:243], v183, v183 op_sel_hi:[0,0,0]
	s_mov_b32 m0, s17
	v_mfma_scale_f32_16x16x128_f8f6f4 v[24:27], v[128:135], v[184:191], v[244:247], v183, v183 op_sel_hi:[0,0,0]
	global_load_lds_dwordx4 v181, s[98:99]
	v_mfma_scale_f32_16x16x128_f8f6f4 v[12:15], v[8:15], v[192:199], v[248:251], v183, v183 op_sel_hi:[0,0,0]
	v_mfma_scale_f32_16x16x128_f8f6f4 v[8:11], v[128:135], v[192:199], v[172:175], v183, v183 op_sel_hi:[0,0,0]
	s_setprio 0
	s_barrier
	v_mov_b32_e32 v170, v180
	s_add_i32 s6, s36, s33
	v_lshl_add_u64 v[128:129], s[30:31], 0, v[170:171]
	v_lshl_add_u64 v[128:129], v[128:129], 0, s[62:63]
	s_mov_b32 s100, s6
	v_mov_b32_e32 v170, v168
	s_add_i32 s101, s6, 0x2000
	v_lshl_add_u64 v[128:129], s[30:31], 0, v[170:171]
	v_lshl_add_u64 v[128:129], v[128:129], 0, s[62:63]
	s_waitcnt vmcnt(4)
	s_barrier
	s_setprio 1
	v_mfma_scale_f32_16x16x128_f8f6f4 v[52:55], v[136:143], v[144:151], v[52:55], v183, v183 op_sel_hi:[0,0,0]
	v_mfma_scale_f32_16x16x128_f8f6f4 v[48:51], v[136:143], v[152:159], v[48:51], v183, v183 op_sel_hi:[0,0,0]
	s_add_u32 s98, s30, s62
	s_addc_u32 s99, s31, s63
	s_mov_b32 m0, s100
	v_mfma_scale_f32_16x16x128_f8f6f4 v[36:39], v[160:167], v[144:151], v[36:39], v183, v183 op_sel_hi:[0,0,0]
	global_load_lds_dwordx4 v180, s[98:99]
	v_mfma_scale_f32_16x16x128_f8f6f4 v[32:35], v[160:167], v[152:159], v[32:35], v183, v183 op_sel_hi:[0,0,0]
	v_mfma_scale_f32_16x16x128_f8f6f4 v[20:23], v[184:191], v[144:151], v[20:23], v183, v183 op_sel_hi:[0,0,0]
	s_mov_b32 m0, s101
	v_mfma_scale_f32_16x16x128_f8f6f4 v[16:19], v[184:191], v[152:159], v[16:19], v183, v183 op_sel_hi:[0,0,0]
	global_load_lds_dwordx4 v168, s[98:99]
	v_mfma_scale_f32_16x16x128_f8f6f4 v[4:7], v[192:199], v[144:151], v[4:7], v183, v183 op_sel_hi:[0,0,0]
	v_mfma_scale_f32_16x16x128_f8f6f4 v[0:3], v[192:199], v[152:159], v[0:3], v183, v183 op_sel_hi:[0,0,0]
	s_setprio 0
	s_add_u32 s4, s4, 0x100
	s_addc_u32 s5, s5, 0
	s_add_u32 s25, s25, 0x100
	s_addc_u32 s27, s27, 0
	s_cmp_ge_i32 s34, s13
	s_mov_b32 s6, s34
	s_barrier
	s_cbranch_scc0 .LBB0_3995
	s_branch .Lpeel_exit_5

.Lpeel_exit_5:
.LBB0_3996:
	v_mbcnt_lo_u32_b32 v129, -1, 0
	v_mbcnt_hi_u32_b32 v129, -1, v129
	s_nop 0
	v_add_u32_e32 v128, s58, v129
	v_cmp_gt_i32_e32 vcc, s41, v128
	s_and_saveexec_b64 s[4:5], vcc
	s_cbranch_execz .LBB0_3998
	v_lshl_add_u32 v130, v128, 5, 0
	v_add_u32_e32 v134, 0x22000, v130
	ds_read_b128 v[130:133], v134
	ds_read_b128 v[134:137], v134 offset:16
	v_lshl_add_u32 v128, v128, 2, 0
	v_add_u32_e32 v128, 0x21800, v128
	s_waitcnt lgkmcnt(0)
	v_mov_b32_e32 v138, v130
	v_mov_b32_e32 v139, v134
	v_mov_b32_e32 v134, v131
	v_pk_add_f32 v[130:131], v[138:139], v[134:135]
	v_mov_b32_e32 v134, v132
	v_mov_b32_e32 v135, v136
	v_mov_b32_e32 v136, v133
	v_pk_add_f32 v[132:133], v[134:135], v[136:137]
	s_nop 0
	v_pk_add_f32 v[130:131], v[130:131], v[132:133]
	s_nop 0
	v_add_f32_e32 v130, v130, v131
	v_mov_b32_e32 v131, 0x358637bd
	v_fmamk_f32 v130, v130, 0x3b000000, v131
	v_rsq_f32_e32 v130, v130
	s_nop 0
	v_mul_f32_e32 v130, 0x3c800000, v130
	ds_write_b32 v128, v130

.LBB0_4064:
	v_mbcnt_lo_u32_b32 v2, -1, 0
	v_mbcnt_hi_u32_b32 v2, -1, v2
	s_lshl_b32 s22, s10, 8
	v_add_u32_e32 v0, s58, v2
	v_ashrrev_i32_e32 v0, 1, v0
	v_add_u32_e32 v0, s22, v0
	v_ashrrev_i32_e32 v1, 31, v0
	v_readlane_b32 s8, v253, 54
	v_lshlrev_b64 v[0:1], 6, v[0:1]
	v_readlane_b32 s9, v253, 55
	v_lshlrev_b32_e32 v2, 4, v2
	v_and_b32_e32 v170, 16, v2
	v_lshl_add_u64 v[0:1], s[8:9], 0, v[0:1]
	s_lshl_b32 s8, s23, 3
	s_ashr_i32 s9, s8, 31
	v_lshl_add_u64 v[0:1], s[8:9], 2, v[0:1]
	v_lshl_add_u64 v[0:1], v[0:1], 0, v[170:171]
	s_add_i32 m0, s3, 0x22000
	v_readlane_b32 s8, v252, 31
	global_load_lds_dwordx4 v[0:1], off
	v_mov_b32_e32 v123, 0
	v_readlane_b32 s9, v252, 32
	s_andn2_b64 vcc, exec, s[8:9]
	s_waitcnt vmcnt(0)
	s_waitcnt vmcnt(0)
	s_cbranch_vccnz .LBB0_4067
	s_add_u32 s4, s4, 0x20080
	s_addc_u32 s5, s5, 0
	s_add_u32 s25, s6, 0x100
	v_mov_b32_e32 v0, 0
	s_addc_u32 s27, s7, 0
	s_mov_b32 s6, 0
.Lpeel_6:
	s_add_i32 s34, s6, 2
	s_add_u32 s8, s4, 0xfffe0080
	s_addc_u32 s7, s5, -1
	s_add_i32 s30, 0, 0x10000
	v_add_u32_e32 v140, s30, v181
	ds_read_b128 v[128:131], v140
	ds_read_b128 v[132:135], v140 offset:1024
	ds_read_b128 v[136:139], v140 offset:2048
	ds_read_b128 v[140:143], v140 offset:3072
	s_cmp_eq_u32 s12, s6
	s_cselect_b32 s6, s52, s8
	s_cselect_b32 s7, s53, s7
	s_cselect_b32 s9, s55, s27
	s_cselect_b32 s8, s54, s25
	v_mov_b32_e32 v168, v169
	ds_read_b128 v[144:147], v182
	ds_read_b128 v[148:151], v182 offset:1024
	ds_read_b128 v[152:155], v182 offset:2048
	ds_read_b128 v[156:159], v182 offset:3072
	ds_read_b128 v[160:163], v182 offset:4096
	ds_read_b128 v[164:167], v182 offset:5120
	ds_read_b128 v[184:187], v182 offset:6144
	ds_read_b128 v[188:191], v182 offset:7168
	s_add_i32 m0, s3, 0xc000
	s_nop 0
	global_load_lds_dwordx4 v168, s[4:5]
	v_mov_b32_e32 v168, v200
	s_add_i32 m0, s3, 0xe000
	s_nop 0
	global_load_lds_dwordx4 v168, s[4:5]
	s_waitcnt lgkmcnt(8)
	s_barrier
	s_waitcnt lgkmcnt(0)
	s_setprio 1
	s_waitcnt lgkmcnt(0)
	v_mfma_scale_f32_16x16x128_f8f6f4 v[120:123], v[128:135], v[144:151], 0, v183, v183 op_sel_hi:[0,0,0]
	v_mov_b32_e32 v170, v200
	v_mfma_scale_f32_16x16x128_f8f6f4 v[124:127], v[136:143], v[144:151], 0, v183, v183 op_sel_hi:[0,0,0]
	v_mfma_scale_f32_16x16x128_f8f6f4 v[200:203], v[128:135], v[160:167], 0, v183, v183 op_sel_hi:[0,0,0]
	v_mfma_scale_f32_16x16x128_f8f6f4 v[192:195], v[128:135], v[152:159], 0, v183, v183 op_sel_hi:[0,0,0]
	v_mfma_scale_f32_16x16x128_f8f6f4 v[196:199], v[136:143], v[152:159], 0, v183, v183 op_sel_hi:[0,0,0]
	v_mfma_scale_f32_16x16x128_f8f6f4 v[204:207], v[136:143], v[160:167], 0, v183, v183 op_sel_hi:[0,0,0]
	v_mfma_scale_f32_16x16x128_f8f6f4 v[208:211], v[128:135], v[184:191], 0, v183, v183 op_sel_hi:[0,0,0]
	v_mfma_scale_f32_16x16x128_f8f6f4 v[212:215], v[136:143], v[184:191], 0, v183, v183 op_sel_hi:[0,0,0]
	s_setprio 0
	s_barrier
	s_add_i32 s35, 0, 0x14000
	v_add_u32_e32 v92, s35, v181
	v_mov_b32_e32 v104, v216
	s_add_i32 s30, s30, s33
	s_nop 0
	ds_read_b128 v[72:75], v92
	ds_read_b128 v[76:79], v92 offset:1024
	ds_read_b128 v[88:91], v92 offset:2048
	ds_read_b128 v[92:95], v92 offset:3072
	s_mov_b32 m0, s30
	s_nop 0
	global_load_lds_dwordx4 v104, s[8:9]
	v_mov_b32_e32 v104, v180
	s_add_i32 m0, s30, 0x2000
	s_nop 0
	global_load_lds_dwordx4 v104, s[8:9]
	s_barrier
	s_waitcnt lgkmcnt(0)
	s_setprio 1
	s_waitcnt lgkmcnt(0)
	v_mfma_scale_f32_16x16x128_f8f6f4 v[116:119], v[72:79], v[144:151], 0, v183, v183 op_sel_hi:[0,0,0]
	v_mov_b32_e32 v168, v216
	v_mfma_scale_f32_16x16x128_f8f6f4 v[112:115], v[88:95], v[144:151], 0, v183, v183 op_sel_hi:[0,0,0]
	v_mfma_scale_f32_16x16x128_f8f6f4 v[216:219], v[72:79], v[152:159], 0, v183, v183 op_sel_hi:[0,0,0]
	v_mfma_scale_f32_16x16x128_f8f6f4 v[220:223], v[88:95], v[152:159], 0, v183, v183 op_sel_hi:[0,0,0]
	v_mfma_scale_f32_16x16x128_f8f6f4 v[224:227], v[72:79], v[160:167], 0, v183, v183 op_sel_hi:[0,0,0]
	v_mfma_scale_f32_16x16x128_f8f6f4 v[160:163], v[88:95], v[160:167], 0, v183, v183 op_sel_hi:[0,0,0]
	v_mfma_scale_f32_16x16x128_f8f6f4 v[164:167], v[72:79], v[184:191], 0, v183, v183 op_sel_hi:[0,0,0]
	v_mfma_scale_f32_16x16x128_f8f6f4 v[184:187], v[88:95], v[184:191], 0, v183, v183 op_sel_hi:[0,0,0]
	s_setprio 0
	v_mov_b32_e32 v144, v169
	s_barrier
	s_nop 2
	ds_read_b128 v[64:67], v182 offset:16384
	ds_read_b128 v[68:71], v182 offset:17408
	ds_read_b128 v[80:83], v182 offset:18432
	ds_read_b128 v[84:87], v182 offset:19456
	ds_read_b128 v[96:99], v182 offset:20480
	ds_read_b128 v[100:103], v182 offset:21504
	ds_read_b128 v[104:107], v182 offset:22528
	ds_read_b128 v[108:111], v182 offset:23552
	s_nop 0
	v_mov_b32_e32 v144, v170
	s_nop 0
	s_barrier
	s_waitcnt lgkmcnt(0)
	s_setprio 1
	s_waitcnt lgkmcnt(0)
	v_mfma_scale_f32_16x16x128_f8f6f4 v[228:231], v[128:135], v[64:71], 0, v183, v183 op_sel_hi:[0,0,0]
	v_mfma_scale_f32_16x16x128_f8f6f4 v[232:235], v[136:143], v[64:71], 0, v183, v183 op_sel_hi:[0,0,0]
	s_mov_b32 m0, s3
	v_mfma_scale_f32_16x16x128_f8f6f4 v[236:239], v[128:135], v[80:87], 0, v183, v183 op_sel_hi:[0,0,0]
	global_load_lds_dwordx4 v169, s[6:7]
	v_mfma_scale_f32_16x16x128_f8f6f4 v[240:243], v[136:143], v[80:87], 0, v183, v183 op_sel_hi:[0,0,0]
	v_mfma_scale_f32_16x16x128_f8f6f4 v[244:247], v[128:135], v[96:103], 0, v183, v183 op_sel_hi:[0,0,0]
	s_mov_b32 m0, s11
	v_mfma_scale_f32_16x16x128_f8f6f4 v[248:251], v[136:143], v[96:103], 0, v183, v183 op_sel_hi:[0,0,0]
	global_load_lds_dwordx4 v170, s[6:7]
	v_mfma_scale_f32_16x16x128_f8f6f4 v[172:175], v[128:135], v[104:111], 0, v183, v183 op_sel_hi:[0,0,0]
	v_mfma_scale_f32_16x16x128_f8f6f4 v[176:179], v[136:143], v[104:111], 0, v183, v183 op_sel_hi:[0,0,0]
	s_setprio 0
	s_barrier
	s_add_u32 s30, s8, s20
	s_addc_u32 s31, s9, s21
	s_nop 2
	v_mov_b32_e32 v8, v168
	s_add_i32 s35, s35, s33
	s_mov_b32 s100, s35
	s_nop 0
	v_mov_b32_e32 v8, v180
	s_add_i32 s101, s35, 0x2000
	s_nop 0
	s_waitcnt vmcnt(4)
	s_barrier
	s_setprio 1
	v_mfma_scale_f32_16x16x128_f8f6f4 v[52:55], v[72:79], v[64:71], 0, v183, v183 op_sel_hi:[0,0,0]
	v_mfma_scale_f32_16x16x128_f8f6f4 v[48:51], v[88:95], v[64:71], 0, v183, v183 op_sel_hi:[0,0,0]
	s_mov_b32 m0, s100
	v_mfma_scale_f32_16x16x128_f8f6f4 v[36:39], v[72:79], v[80:87], 0, v183, v183 op_sel_hi:[0,0,0]
	global_load_lds_dwordx4 v168, s[30:31]
	v_mfma_scale_f32_16x16x128_f8f6f4 v[32:35], v[88:95], v[80:87], 0, v183, v183 op_sel_hi:[0,0,0]
	v_mfma_scale_f32_16x16x128_f8f6f4 v[20:23], v[72:79], v[96:103], 0, v183, v183 op_sel_hi:[0,0,0]
	s_mov_b32 m0, s101
	v_mfma_scale_f32_16x16x128_f8f6f4 v[16:19], v[88:95], v[96:103], 0, v183, v183 op_sel_hi:[0,0,0]
	global_load_lds_dwordx4 v180, s[30:31]
	v_mfma_scale_f32_16x16x128_f8f6f4 v[4:7], v[72:79], v[104:111], 0, v183, v183 op_sel_hi:[0,0,0]
	v_mfma_scale_f32_16x16x128_f8f6f4 v[0:3], v[88:95], v[104:111], 0, v183, v183 op_sel_hi:[0,0,0]
	s_setprio 0
	s_add_i32 s35, 0, 0x18000
	v_add_u32_e32 v24, s35, v181
	s_barrier
	ds_read_b128 v[8:11], v24
	ds_read_b128 v[12:15], v24 offset:1024
	ds_read_b128 v[128:131], v24 offset:2048
	ds_read_b128 v[132:135], v24 offset:3072
	s_add_u32 s36, s6, 0x20000
	v_mov_b32_e32 v64, v169
	ds_read_b128 v[24:27], v182 offset:32768
	ds_read_b128 v[28:31], v182 offset:33792
	ds_read_b128 v[40:43], v182 offset:34816
	ds_read_b128 v[44:47], v182 offset:35840
	ds_read_b128 v[56:59], v182 offset:36864
	ds_read_b128 v[60:63], v182 offset:37888
	ds_read_b128 v[136:139], v182 offset:38912
	ds_read_b128 v[140:143], v182 offset:39936
	s_addc_u32 s37, s7, 0
	s_nop 0
	v_mov_b32_e32 v64, v170
	s_nop 0
	s_waitcnt lgkmcnt(8)
	s_barrier
	s_waitcnt lgkmcnt(0)
	s_setprio 1
	s_waitcnt lgkmcnt(0)
	v_mfma_scale_f32_16x16x128_f8f6f4 v[120:123], v[8:15], v[24:31], v[120:123], v183, v183 op_sel_hi:[0,0,0]
	v_mfma_scale_f32_16x16x128_f8f6f4 v[124:127], v[128:135], v[24:31], v[124:127], v183, v183 op_sel_hi:[0,0,0]
	s_mov_b32 m0, s14
	v_mfma_scale_f32_16x16x128_f8f6f4 v[108:111], v[8:15], v[40:47], v[192:195], v183, v183 op_sel_hi:[0,0,0]
	global_load_lds_dwordx4 v169, s[36:37]
	v_mfma_scale_f32_16x16x128_f8f6f4 v[104:107], v[128:135], v[40:47], v[196:199], v183, v183 op_sel_hi:[0,0,0]
	v_mfma_scale_f32_16x16x128_f8f6f4 v[92:95], v[8:15], v[56:63], v[200:203], v183, v183 op_sel_hi:[0,0,0]
	s_mov_b32 m0, s15
	v_mfma_scale_f32_16x16x128_f8f6f4 v[88:91], v[128:135], v[56:63], v[204:207], v183, v183 op_sel_hi:[0,0,0]
	global_load_lds_dwordx4 v170, s[36:37]
	s_nop 5
	v_mov_b32_e32 v200, v170
	v_mfma_scale_f32_16x16x128_f8f6f4 v[76:79], v[8:15], v[136:143], v[208:211], v183, v183 op_sel_hi:[0,0,0]
	v_mfma_scale_f32_16x16x128_f8f6f4 v[72:75], v[128:135], v[136:143], v[212:215], v183, v183 op_sel_hi:[0,0,0]
	s_setprio 0
	s_barrier
	s_add_i32 s36, 0, 0x1c000
	v_add_u32_e32 v64, s36, v181
	v_mov_b32_e32 v170, v168
	ds_read_b128 v[144:147], v64
	ds_read_b128 v[148:151], v64 offset:1024
	ds_read_b128 v[152:155], v64 offset:2048
	ds_read_b128 v[156:159], v64 offset:3072
	s_add_i32 s35, s35, s33
	v_lshl_add_u64 v[64:65], s[8:9], 0, v[170:171]
	v_lshl_add_u64 v[64:65], v[64:65], 0, s[62:63]
	v_mov_b32_e32 v170, v180
	v_lshl_add_u64 v[64:65], s[8:9], 0, v[170:171]
	v_lshl_add_u64 v[64:65], v[64:65], 0, s[62:63]
	s_barrier
	s_waitcnt lgkmcnt(0)
	s_setprio 1
	s_waitcnt lgkmcnt(0)
	v_mfma_scale_f32_16x16x128_f8f6f4 v[116:119], v[144:151], v[24:31], v[116:119], v183, v183 op_sel_hi:[0,0,0]
	v_mfma_scale_f32_16x16x128_f8f6f4 v[112:115], v[152:159], v[24:31], v[112:115], v183, v183 op_sel_hi:[0,0,0]
	s_add_u32 s98, s8, s62
	s_addc_u32 s99, s9, s63
	s_mov_b32 m0, s35
	v_mfma_scale_f32_16x16x128_f8f6f4 v[100:103], v[144:151], v[40:47], v[216:219], v183, v183 op_sel_hi:[0,0,0]
	global_load_lds_dwordx4 v168, s[98:99]
	v_mfma_scale_f32_16x16x128_f8f6f4 v[96:99], v[152:159], v[40:47], v[220:223], v183, v183 op_sel_hi:[0,0,0]
	s_nop 5
	v_mov_b32_e32 v216, v168
	v_mfma_scale_f32_16x16x128_f8f6f4 v[84:87], v[144:151], v[56:63], v[224:227], v183, v183 op_sel_hi:[0,0,0]
	s_add_i32 m0, s35, 0x2000
	v_mfma_scale_f32_16x16x128_f8f6f4 v[80:83], v[152:159], v[56:63], v[160:163], v183, v183 op_sel_hi:[0,0,0]
	global_load_lds_dwordx4 v180, s[98:99]
	v_mfma_scale_f32_16x16x128_f8f6f4 v[68:71], v[144:151], v[136:143], v[164:167], v183, v183 op_sel_hi:[0,0,0]
	v_mfma_scale_f32_16x16x128_f8f6f4 v[64:67], v[152:159], v[136:143], v[184:187], v183, v183 op_sel_hi:[0,0,0]
	s_setprio 0
	v_mov_b32_e32 v170, v169
	s_barrier
	ds_read_b128 v[136:139], v182 offset:49152
	ds_read_b128 v[140:143], v182 offset:50176
	ds_read_b128 v[160:163], v182 offset:51200
	ds_read_b128 v[164:167], v182 offset:52224
	ds_read_b128 v[184:187], v182 offset:53248
	ds_read_b128 v[188:191], v182 offset:54272
	ds_read_b128 v[192:195], v182 offset:55296
	ds_read_b128 v[196:199], v182 offset:56320
	v_lshl_add_u64 v[24:25], s[6:7], 0, v[170:171]
	v_lshl_add_u64 v[24:25], v[24:25], 0, s[62:63]
	v_mov_b32_e32 v170, v200
	v_lshl_add_u64 v[24:25], s[6:7], 0, v[170:171]
	v_lshl_add_u64 v[24:25], v[24:25], 0, s[62:63]
	s_barrier
	s_waitcnt lgkmcnt(0)
	s_setprio 1
	s_waitcnt lgkmcnt(0)
	v_mfma_scale_f32_16x16x128_f8f6f4 v[60:63], v[8:15], v[136:143], v[228:231], v183, v183 op_sel_hi:[0,0,0]
	v_mfma_scale_f32_16x16x128_f8f6f4 v[56:59], v[128:135], v[136:143], v[232:235], v183, v183 op_sel_hi:[0,0,0]
	s_add_u32 s98, s6, s62
	s_addc_u32 s99, s7, s63
	s_mov_b32 m0, s16
	v_mfma_scale_f32_16x16x128_f8f6f4 v[44:47], v[8:15], v[160:167], v[236:239], v183, v183 op_sel_hi:[0,0,0]
	global_load_lds_dwordx4 v169, s[98:99]
	v_mfma_scale_f32_16x16x128_f8f6f4 v[40:43], v[128:135], v[160:167], v[240:243], v183, v183 op_sel_hi:[0,0,0]
	v_mfma_scale_f32_16x16x128_f8f6f4 v[28:31], v[8:15], v[184:191], v[244:247], v183, v183 op_sel_hi:[0,0,0]
	s_mov_b32 m0, s17
	v_mfma_scale_f32_16x16x128_f8f6f4 v[24:27], v[128:135], v[184:191], v[248:251], v183, v183 op_sel_hi:[0,0,0]
	global_load_lds_dwordx4 v200, s[98:99]
	v_mfma_scale_f32_16x16x128_f8f6f4 v[12:15], v[8:15], v[192:199], v[172:175], v183, v183 op_sel_hi:[0,0,0]
	v_mfma_scale_f32_16x16x128_f8f6f4 v[8:11], v[128:135], v[192:199], v[176:179], v183, v183 op_sel_hi:[0,0,0]
	s_setprio 0
	s_barrier
	v_mov_b32_e32 v170, v168
	s_add_i32 s6, s36, s33
	v_lshl_add_u64 v[128:129], s[30:31], 0, v[170:171]
	v_lshl_add_u64 v[128:129], v[128:129], 0, s[62:63]
	s_mov_b32 s100, s6
	v_mov_b32_e32 v170, v180
	s_add_i32 s101, s6, 0x2000
	v_lshl_add_u64 v[128:129], s[30:31], 0, v[170:171]
	v_lshl_add_u64 v[128:129], v[128:129], 0, s[62:63]
	s_waitcnt vmcnt(4)
	s_barrier
	s_setprio 1
	v_mfma_scale_f32_16x16x128_f8f6f4 v[52:55], v[144:151], v[136:143], v[52:55], v183, v183 op_sel_hi:[0,0,0]
	v_mfma_scale_f32_16x16x128_f8f6f4 v[48:51], v[152:159], v[136:143], v[48:51], v183, v183 op_sel_hi:[0,0,0]
	s_add_u32 s98, s30, s62
	s_addc_u32 s99, s31, s63
	s_mov_b32 m0, s100
	v_mfma_scale_f32_16x16x128_f8f6f4 v[36:39], v[144:151], v[160:167], v[36:39], v183, v183 op_sel_hi:[0,0,0]
	global_load_lds_dwordx4 v168, s[98:99]
	v_mfma_scale_f32_16x16x128_f8f6f4 v[32:35], v[152:159], v[160:167], v[32:35], v183, v183 op_sel_hi:[0,0,0]
	v_mfma_scale_f32_16x16x128_f8f6f4 v[20:23], v[144:151], v[184:191], v[20:23], v183, v183 op_sel_hi:[0,0,0]
	s_mov_b32 m0, s101
	v_mfma_scale_f32_16x16x128_f8f6f4 v[16:19], v[152:159], v[184:191], v[16:19], v183, v183 op_sel_hi:[0,0,0]
	global_load_lds_dwordx4 v180, s[98:99]
	v_mfma_scale_f32_16x16x128_f8f6f4 v[4:7], v[144:151], v[192:199], v[4:7], v183, v183 op_sel_hi:[0,0,0]
	v_mfma_scale_f32_16x16x128_f8f6f4 v[0:3], v[152:159], v[192:199], v[0:3], v183, v183 op_sel_hi:[0,0,0]
	s_setprio 0
	s_add_u32 s4, s4, 0x100
	s_addc_u32 s5, s5, 0
	s_add_u32 s25, s25, 0x100
	s_addc_u32 s27, s27, 0
	s_cmp_ge_i32 s34, s13
	s_mov_b32 s6, s34
	s_barrier
	s_cbranch_scc0 .LBB0_4066
	s_branch .Lpeel_exit_6

.Lpeel_7:
	ds_read_b128 v[146:149], v141
	ds_read_b128 v[150:153], v141 offset:1024
	ds_read_b128 v[154:157], v141 offset:2048
	ds_read_b128 v[158:161], v141 offset:3072
	s_add_u32 s22, s20, 0xfffc0080
	s_addc_u32 s23, s21, -1
	s_cmp_eq_u32 s50, 12
	s_cselect_b32 s25, s15, s23
	s_cselect_b32 s24, s14, s22
	s_cselect_b32 s23, s17, s13
	s_cselect_b32 s22, s16, s11
	v_mov_b32_e32 v128, v138
	ds_read_b128 v[162:165], v142
	ds_read_b128 v[166:169], v142 offset:1024
	ds_read_b128 v[170:173], v142 offset:2048
	ds_read_b128 v[174:177], v142 offset:3072
	ds_read_b128 v[178:181], v142 offset:4096
	ds_read_b128 v[182:185], v142 offset:5120
	ds_read_b128 v[186:189], v142 offset:6144
	ds_read_b128 v[190:193], v142 offset:7168
	s_nop 0
	v_mov_b32_e32 v128, v139
	s_nop 0
	s_waitcnt lgkmcnt(8)
	s_barrier
	s_waitcnt lgkmcnt(0)
	s_setprio 1
	s_waitcnt lgkmcnt(0)
	v_mfma_scale_f32_16x16x128_f8f6f4 v[124:127], v[146:153], v[162:169], 0, v143, v143 op_sel_hi:[0,0,0]
	v_mfma_scale_f32_16x16x128_f8f6f4 v[120:123], v[154:161], v[162:169], 0, v143, v143 op_sel_hi:[0,0,0]
	s_add_i32 m0, s19, 0xc000
	v_mfma_scale_f32_16x16x128_f8f6f4 v[116:119], v[146:153], v[170:177], 0, v143, v143 op_sel_hi:[0,0,0]
	global_load_lds_dwordx4 v138, s[20:21]
	v_mfma_scale_f32_16x16x128_f8f6f4 v[112:115], v[154:161], v[170:177], 0, v143, v143 op_sel_hi:[0,0,0]
	v_mfma_scale_f32_16x16x128_f8f6f4 v[132:135], v[146:153], v[178:185], 0, v143, v143 op_sel_hi:[0,0,0]
	s_add_i32 m0, s19, 0xe000
	v_mfma_scale_f32_16x16x128_f8f6f4 v[194:197], v[154:161], v[178:185], 0, v143, v143 op_sel_hi:[0,0,0]
	global_load_lds_dwordx4 v139, s[20:21]
	v_mfma_scale_f32_16x16x128_f8f6f4 v[198:201], v[146:153], v[186:193], 0, v143, v143 op_sel_hi:[0,0,0]
	v_mfma_scale_f32_16x16x128_f8f6f4 v[202:205], v[154:161], v[186:193], 0, v143, v143 op_sel_hi:[0,0,0]
	s_setprio 0
	s_barrier
	v_mov_b32_e32 v128, v138
	s_add_i32 s51, s44, s28
	s_nop 2
	ds_read_b128 v[96:99], v144
	ds_read_b128 v[100:103], v144 offset:1024
	ds_read_b128 v[104:107], v144 offset:2048
	ds_read_b128 v[108:111], v144 offset:3072
	s_nop 0
	v_mov_b32_e32 v128, v139
	s_nop 0
	s_barrier
	s_waitcnt lgkmcnt(0)
	s_setprio 1
	s_waitcnt lgkmcnt(0)
	v_mfma_scale_f32_16x16x128_f8f6f4 v[206:209], v[96:103], v[162:169], 0, v143, v143 op_sel_hi:[0,0,0]
	v_mfma_scale_f32_16x16x128_f8f6f4 v[162:165], v[104:111], v[162:169], 0, v143, v143 op_sel_hi:[0,0,0]
	s_mov_b32 m0, s51
	v_mfma_scale_f32_16x16x128_f8f6f4 v[166:169], v[96:103], v[170:177], 0, v143, v143 op_sel_hi:[0,0,0]
	global_load_lds_dwordx4 v138, s[22:23]
	v_mfma_scale_f32_16x16x128_f8f6f4 v[170:173], v[104:111], v[170:177], 0, v143, v143 op_sel_hi:[0,0,0]
	v_mfma_scale_f32_16x16x128_f8f6f4 v[174:177], v[96:103], v[178:185], 0, v143, v143 op_sel_hi:[0,0,0]
	s_add_i32 m0, s51, 0x2000
	v_mfma_scale_f32_16x16x128_f8f6f4 v[178:181], v[104:111], v[178:185], 0, v143, v143 op_sel_hi:[0,0,0]
	global_load_lds_dwordx4 v139, s[22:23]
	v_mfma_scale_f32_16x16x128_f8f6f4 v[182:185], v[96:103], v[186:193], 0, v143, v143 op_sel_hi:[0,0,0]
	v_mfma_scale_f32_16x16x128_f8f6f4 v[186:189], v[104:111], v[186:193], 0, v143, v143 op_sel_hi:[0,0,0]
	s_setprio 0
	v_mov_b32_e32 v128, v138
	s_barrier
	s_nop 2
	ds_read_b128 v[32:35], v142 offset:16384
	ds_read_b128 v[36:39], v142 offset:17408
	ds_read_b128 v[40:43], v142 offset:18432
	ds_read_b128 v[44:47], v142 offset:19456
	ds_read_b128 v[48:51], v142 offset:20480
	ds_read_b128 v[52:55], v142 offset:21504
	ds_read_b128 v[56:59], v142 offset:22528
	ds_read_b128 v[60:63], v142 offset:23552
	s_nop 0
	v_mov_b32_e32 v128, v139
	s_nop 0
	s_barrier
	s_waitcnt lgkmcnt(0)
	s_setprio 1
	s_waitcnt lgkmcnt(0)
	v_mfma_scale_f32_16x16x128_f8f6f4 v[92:95], v[146:153], v[32:39], 0, v143, v143 op_sel_hi:[0,0,0]
	v_mfma_scale_f32_16x16x128_f8f6f4 v[88:91], v[154:161], v[32:39], 0, v143, v143 op_sel_hi:[0,0,0]
	s_mov_b32 m0, s19
	v_mfma_scale_f32_16x16x128_f8f6f4 v[84:87], v[146:153], v[40:47], 0, v143, v143 op_sel_hi:[0,0,0]
	global_load_lds_dwordx4 v138, s[24:25]
	v_mfma_scale_f32_16x16x128_f8f6f4 v[80:83], v[154:161], v[40:47], 0, v143, v143 op_sel_hi:[0,0,0]
	v_mfma_scale_f32_16x16x128_f8f6f4 v[76:79], v[146:153], v[48:55], 0, v143, v143 op_sel_hi:[0,0,0]
	s_mov_b32 m0, s29
	v_mfma_scale_f32_16x16x128_f8f6f4 v[72:75], v[154:161], v[48:55], 0, v143, v143 op_sel_hi:[0,0,0]
	global_load_lds_dwordx4 v139, s[24:25]
	v_mfma_scale_f32_16x16x128_f8f6f4 v[190:193], v[146:153], v[56:63], 0, v143, v143 op_sel_hi:[0,0,0]
	v_mfma_scale_f32_16x16x128_f8f6f4 v[210:213], v[154:161], v[56:63], 0, v143, v143 op_sel_hi:[0,0,0]
	s_setprio 0
	s_barrier
	s_add_u32 s52, s22, 0x40000
	s_addc_u32 s53, s23, 0
	s_nop 2
	v_mov_b32_e32 v64, v138
	s_add_i32 s51, s45, s28
	s_mov_b32 s100, s51
	s_nop 0
	v_mov_b32_e32 v64, v139
	s_add_i32 s101, s51, 0x2000
	s_nop 0
	s_waitcnt vmcnt(4)
	s_barrier
	s_setprio 1
	v_mfma_scale_f32_16x16x128_f8f6f4 v[214:217], v[96:103], v[32:39], 0, v143, v143 op_sel_hi:[0,0,0]
	v_mfma_scale_f32_16x16x128_f8f6f4 v[218:221], v[104:111], v[32:39], 0, v143, v143 op_sel_hi:[0,0,0]
	s_mov_b32 m0, s100
	v_mfma_scale_f32_16x16x128_f8f6f4 v[222:225], v[96:103], v[40:47], 0, v143, v143 op_sel_hi:[0,0,0]
	global_load_lds_dwordx4 v138, s[52:53]
	v_mfma_scale_f32_16x16x128_f8f6f4 v[226:229], v[104:111], v[40:47], 0, v143, v143 op_sel_hi:[0,0,0]
	v_mfma_scale_f32_16x16x128_f8f6f4 v[230:233], v[96:103], v[48:55], 0, v143, v143 op_sel_hi:[0,0,0]
	s_mov_b32 m0, s101
	v_mfma_scale_f32_16x16x128_f8f6f4 v[234:237], v[104:111], v[48:55], 0, v143, v143 op_sel_hi:[0,0,0]
	global_load_lds_dwordx4 v139, s[52:53]
	v_mfma_scale_f32_16x16x128_f8f6f4 v[238:241], v[96:103], v[56:63], 0, v143, v143 op_sel_hi:[0,0,0]
	v_mfma_scale_f32_16x16x128_f8f6f4 v[242:245], v[104:111], v[56:63], 0, v143, v143 op_sel_hi:[0,0,0]
	s_setprio 0
	s_add_i32 s51, 0, 0x18000
	s_nop 1
	v_add_u32_e32 v12, s51, v140
	s_barrier
	s_nop 0
	ds_read_b128 v[0:3], v12
	ds_read_b128 v[4:7], v12 offset:1024
	ds_read_b128 v[8:11], v12 offset:2048
	ds_read_b128 v[12:15], v12 offset:3072
	s_add_u32 s52, s24, 0x40000
	v_mov_b32_e32 v40, v138
	ds_read_b128 v[16:19], v142 offset:32768
	ds_read_b128 v[20:23], v142 offset:33792
	ds_read_b128 v[24:27], v142 offset:34816
	ds_read_b128 v[28:31], v142 offset:35840
	ds_read_b128 v[32:35], v142 offset:36864
	ds_read_b128 v[36:39], v142 offset:37888
	ds_read_b128 v[64:67], v142 offset:38912
	ds_read_b128 v[68:71], v142 offset:39936
	s_addc_u32 s53, s25, 0
	s_nop 0
	v_mov_b32_e32 v40, v139
	s_nop 0
	s_waitcnt lgkmcnt(8)
	s_barrier
	s_waitcnt lgkmcnt(0)
	s_setprio 1
	s_waitcnt lgkmcnt(0)
	v_mfma_scale_f32_16x16x128_f8f6f4 v[124:127], v[0:7], v[16:23], v[124:127], v143, v143 op_sel_hi:[0,0,0]
	v_mfma_scale_f32_16x16x128_f8f6f4 v[120:123], v[8:15], v[16:23], v[120:123], v143, v143 op_sel_hi:[0,0,0]
	s_mov_b32 m0, s30
	v_mfma_scale_f32_16x16x128_f8f6f4 v[116:119], v[0:7], v[24:31], v[116:119], v143, v143 op_sel_hi:[0,0,0]
	global_load_lds_dwordx4 v138, s[52:53]
	v_mfma_scale_f32_16x16x128_f8f6f4 v[112:115], v[8:15], v[24:31], v[112:115], v143, v143 op_sel_hi:[0,0,0]
	v_mfma_scale_f32_16x16x128_f8f6f4 v[108:111], v[0:7], v[32:39], v[132:135], v143, v143 op_sel_hi:[0,0,0]
	s_mov_b32 m0, s31
	v_mfma_scale_f32_16x16x128_f8f6f4 v[104:107], v[8:15], v[32:39], v[194:197], v143, v143 op_sel_hi:[0,0,0]
	global_load_lds_dwordx4 v139, s[52:53]
	v_mfma_scale_f32_16x16x128_f8f6f4 v[100:103], v[0:7], v[64:71], v[198:201], v143, v143 op_sel_hi:[0,0,0]
	v_mfma_scale_f32_16x16x128_f8f6f4 v[96:99], v[8:15], v[64:71], v[202:205], v143, v143 op_sel_hi:[0,0,0]
	s_setprio 0
	s_barrier
	s_add_i32 s52, 0, 0x1c000
	v_add_u32_e32 v40, s52, v140
	v_mov_b32_e32 v128, v138
	ds_read_b128 v[146:149], v40
	ds_read_b128 v[150:153], v40 offset:1024
	ds_read_b128 v[154:157], v40 offset:2048
	ds_read_b128 v[158:161], v40 offset:3072
	s_add_i32 s51, s51, s28
	v_lshl_add_u64 v[40:41], s[22:23], 0, v[128:129]
	v_lshl_add_u64 v[40:41], v[40:41], 0, s[6:7]
	v_mov_b32_e32 v128, v139
	v_lshl_add_u64 v[40:41], s[22:23], 0, v[128:129]
	v_lshl_add_u64 v[40:41], v[40:41], 0, s[6:7]
	s_barrier
	s_waitcnt lgkmcnt(0)
	s_setprio 1
	s_waitcnt lgkmcnt(0)
	v_mfma_scale_f32_16x16x128_f8f6f4 v[60:63], v[146:153], v[16:23], v[206:209], v143, v143 op_sel_hi:[0,0,0]
	v_mfma_scale_f32_16x16x128_f8f6f4 v[56:59], v[154:161], v[16:23], v[162:165], v143, v143 op_sel_hi:[0,0,0]
	s_add_u32 s98, s22, s6
	s_addc_u32 s99, s23, s7
	s_mov_b32 m0, s51
	v_mfma_scale_f32_16x16x128_f8f6f4 v[52:55], v[146:153], v[24:31], v[166:169], v143, v143 op_sel_hi:[0,0,0]
	global_load_lds_dwordx4 v138, s[98:99]
	v_mfma_scale_f32_16x16x128_f8f6f4 v[48:51], v[154:161], v[24:31], v[170:173], v143, v143 op_sel_hi:[0,0,0]
	v_mfma_scale_f32_16x16x128_f8f6f4 v[44:47], v[146:153], v[32:39], v[174:177], v143, v143 op_sel_hi:[0,0,0]
	s_add_i32 m0, s51, 0x2000
	v_mfma_scale_f32_16x16x128_f8f6f4 v[40:43], v[154:161], v[32:39], v[178:181], v143, v143 op_sel_hi:[0,0,0]
	global_load_lds_dwordx4 v139, s[98:99]
	v_mfma_scale_f32_16x16x128_f8f6f4 v[36:39], v[146:153], v[64:71], v[182:185], v143, v143 op_sel_hi:[0,0,0]
	v_mfma_scale_f32_16x16x128_f8f6f4 v[32:35], v[154:161], v[64:71], v[186:189], v143, v143 op_sel_hi:[0,0,0]
	s_setprio 0
	v_mov_b32_e32 v128, v138
	s_barrier
	ds_read_b128 v[16:19], v142 offset:49152
	ds_read_b128 v[20:23], v142 offset:50176
	ds_read_b128 v[162:165], v142 offset:51200
	ds_read_b128 v[166:169], v142 offset:52224
	ds_read_b128 v[170:173], v142 offset:53248
	ds_read_b128 v[174:177], v142 offset:54272
	ds_read_b128 v[178:181], v142 offset:55296
	ds_read_b128 v[182:185], v142 offset:56320
	v_lshl_add_u64 v[24:25], s[24:25], 0, v[128:129]
	v_lshl_add_u64 v[24:25], v[24:25], 0, s[6:7]
	v_mov_b32_e32 v128, v139
	v_lshl_add_u64 v[24:25], s[24:25], 0, v[128:129]
	v_lshl_add_u64 v[24:25], v[24:25], 0, s[6:7]
	s_barrier
	s_waitcnt lgkmcnt(0)
	s_setprio 1
	s_waitcnt lgkmcnt(0)
	v_mfma_scale_f32_16x16x128_f8f6f4 v[92:95], v[0:7], v[16:23], v[92:95], v143, v143 op_sel_hi:[0,0,0]
	v_mfma_scale_f32_16x16x128_f8f6f4 v[88:91], v[8:15], v[16:23], v[88:91], v143, v143 op_sel_hi:[0,0,0]
	s_add_u32 s98, s24, s6
	s_addc_u32 s99, s25, s7
	s_mov_b32 m0, s41
	v_mfma_scale_f32_16x16x128_f8f6f4 v[84:87], v[0:7], v[162:169], v[84:87], v143, v143 op_sel_hi:[0,0,0]
	global_load_lds_dwordx4 v138, s[98:99]
	v_mfma_scale_f32_16x16x128_f8f6f4 v[80:83], v[8:15], v[162:169], v[80:83], v143, v143 op_sel_hi:[0,0,0]
	v_mfma_scale_f32_16x16x128_f8f6f4 v[76:79], v[0:7], v[170:177], v[76:79], v143, v143 op_sel_hi:[0,0,0]
	s_mov_b32 m0, s42
	v_mfma_scale_f32_16x16x128_f8f6f4 v[72:75], v[8:15], v[170:177], v[72:75], v143, v143 op_sel_hi:[0,0,0]
	global_load_lds_dwordx4 v139, s[98:99]
	v_mfma_scale_f32_16x16x128_f8f6f4 v[68:71], v[0:7], v[178:185], v[190:193], v143, v143 op_sel_hi:[0,0,0]
	v_mfma_scale_f32_16x16x128_f8f6f4 v[64:67], v[8:15], v[178:185], v[210:213], v143, v143 op_sel_hi:[0,0,0]
	s_setprio 0
	s_barrier
	s_add_u32 s22, s22, 0x40080
	s_addc_u32 s23, s23, 0
	v_mov_b32_e32 v0, v138
	s_add_i32 s24, s52, s28
	s_nop 0
	v_mov_b32_e32 v0, v139
	s_nop 0
	s_waitcnt vmcnt(4)
	s_barrier
	s_setprio 1
	v_mfma_scale_f32_16x16x128_f8f6f4 v[28:31], v[146:153], v[16:23], v[214:217], v143, v143 op_sel_hi:[0,0,0]
	v_mfma_scale_f32_16x16x128_f8f6f4 v[24:27], v[154:161], v[16:23], v[218:221], v143, v143 op_sel_hi:[0,0,0]
	s_mov_b32 m0, s24
	v_mfma_scale_f32_16x16x128_f8f6f4 v[20:23], v[146:153], v[162:169], v[222:225], v143, v143 op_sel_hi:[0,0,0]
	global_load_lds_dwordx4 v138, s[22:23]
	v_mfma_scale_f32_16x16x128_f8f6f4 v[16:19], v[154:161], v[162:169], v[226:229], v143, v143 op_sel_hi:[0,0,0]
	v_mfma_scale_f32_16x16x128_f8f6f4 v[12:15], v[146:153], v[170:177], v[230:233], v143, v143 op_sel_hi:[0,0,0]
	s_add_i32 m0, s24, 0x2000
	v_mfma_scale_f32_16x16x128_f8f6f4 v[8:11], v[154:161], v[170:177], v[234:237], v143, v143 op_sel_hi:[0,0,0]
	global_load_lds_dwordx4 v139, s[22:23]
	v_mfma_scale_f32_16x16x128_f8f6f4 v[4:7], v[146:153], v[178:185], v[238:241], v143, v143 op_sel_hi:[0,0,0]
	v_mfma_scale_f32_16x16x128_f8f6f4 v[0:3], v[154:161], v[178:185], v[242:245], v143, v143 op_sel_hi:[0,0,0]
	s_setprio 0
	s_add_i32 s50, s50, 2
	s_add_u32 s20, s20, 0x100
	s_addc_u32 s21, s21, 0
	s_add_u32 s11, s11, 0x100
	s_addc_u32 s13, s13, 0
	s_cmp_gt_u32 s50, 13
	s_barrier
	s_cbranch_scc0 .LBB0_4932
	s_branch .Lpeel_exit_7

.Lpeel_exit_7:
	s_ashr_i32 s11, s18, 4
	s_mul_hi_i32 s13, s11, 0xc000
	s_mul_i32 s11, s11, 0xc000
	s_add_u32 s11, s37, s11
	s_addc_u32 s13, s38, s13
	s_lshl_b32 s20, s49, 8
	s_ashr_i32 s21, s20, 31
	s_lshl_b64 s[22:23], s[20:21], 2
	s_add_u32 s11, s11, s22
	v_mbcnt_lo_u32_b32 v134, -1, 0
	v_mbcnt_hi_u32_b32 v134, -1, v134
	s_addc_u32 s13, s13, s23
	v_ashrrev_i32_e32 v135, 4, v134
	s_add_u32 s22, s11, s46
	v_lshlrev_b32_e32 v132, 2, v135
	s_addc_u32 s23, s13, 0
	v_ashrrev_i32_e32 v133, 31, v132
	v_lshl_add_u64 v[132:133], v[132:133], 2, s[22:23]
	global_load_dwordx4 v[146:149], v[132:133], off
	global_load_dwordx4 v[150:153], v[132:133], off offset:64
	v_mov_b32_e32 v164, v129
	s_lshl_b32 s11, s18, 8
	v_mov_b32_e32 v165, v129
	s_add_i32 s22, s11, s39
	s_ashr_i32 s23, s22, 31
	s_lshl_b64 s[22:23], s[22:23], 11
	s_add_u32 s11, s35, s22
	s_addc_u32 s13, s36, s23
	v_mov_b32_e32 v162, v129
	v_lshlrev_b32_e32 v135, 3, v135
	s_add_u32 s11, s11, s20
	v_mov_b32_e32 v154, v129
	v_mov_b32_e32 v155, v129
	v_mov_b32_e32 v156, v129
	v_mov_b32_e32 v157, v129
	v_and_b32_e32 v128, 16, v134
	v_bfi_b32 v134, -16, v135, v134
	s_addc_u32 s13, s13, s21
	v_mov_b32_e32 v163, v129
	v_mov_b32_e32 v158, v129
	v_mov_b32_e32 v159, v129
	v_mov_b32_e32 v160, v129
	v_mov_b32_e32 v161, v129
	v_ashrrev_i32_e32 v135, 31, v134
	s_add_u32 s20, s11, s40
	v_lshlrev_b64 v[134:135], 11, v[134:135]
	s_addc_u32 s21, s13, 0
	v_lshl_add_u64 v[134:135], s[20:21], 0, v[134:135]
	v_lshl_add_u64 v[134:135], v[134:135], 0, v[128:129]
	v_add_co_u32_e32 v136, vcc, s34, v134
	s_mov_b32 s18, s12
	s_nop 0
	v_addc_co_u32_e32 v137, vcc, 0, v135, vcc
	s_mov_b32 s49, s10
	s_mov_b64 s[22:23], s[16:17]
	s_mov_b64 s[20:21], s[14:15]
	s_waitcnt vmcnt(0)
	v_pk_mul_f32 v[146:147], v[146:147], s[8:9] op_sel_hi:[1,0]
	v_pk_mul_f32 v[150:151], v[150:151], s[8:9] op_sel_hi:[1,0]
	v_pk_mul_f32 v[84:85], v[84:85], v[146:147]
	v_pk_mul_f32 v[80:81], v[80:81], v[150:151]
	v_cvt_pk_fp8_f32 v164, v84, v85
	v_cvt_pk_fp8_f32 v165, v80, v81
	v_pk_mul_f32 v[148:149], v[148:149], s[8:9] op_sel_hi:[1,0]
	v_pk_mul_f32 v[152:153], v[152:153], s[8:9] op_sel_hi:[1,0]
	v_pk_mul_f32 v[80:81], v[86:87], v[148:149]
	v_pk_mul_f32 v[72:73], v[72:73], v[150:151]
	v_cvt_pk_fp8_f32 v164, v80, v81 op_sel:[0,0,1]
	v_pk_mul_f32 v[80:81], v[82:83], v[152:153]
	v_pk_mul_f32 v[92:93], v[92:93], v[146:147]
	v_cvt_pk_fp8_f32 v165, v80, v81 op_sel:[0,0,1]
	v_pk_mul_f32 v[80:81], v[76:77], v[146:147]
	v_mov_b32_e32 v77, v129
	v_mov_b32_e32 v76, v129
	v_cvt_pk_fp8_f32 v77, v72, v73
	v_pk_mul_f32 v[72:73], v[78:79], v[148:149]
	v_pk_mul_f32 v[68:69], v[68:69], v[146:147]
	v_mov_b32_e32 v78, v129
	v_pk_mul_f32 v[124:125], v[124:125], v[146:147]
	v_pk_mul_f32 v[120:121], v[120:121], v[150:151]
	v_pk_mul_f32 v[116:117], v[116:117], v[146:147]
	v_pk_mul_f32 v[112:113], v[112:113], v[150:151]
	v_cvt_pk_fp8_f32 v162, v92, v93
	v_pk_mul_f32 v[88:89], v[88:89], v[150:151]
	v_cvt_pk_fp8_f32 v76, v80, v81
	v_cvt_pk_fp8_f32 v78, v68, v69
	v_pk_mul_f32 v[64:65], v[64:65], v[150:151]
	v_mov_b32_e32 v79, v129
	v_pk_mul_f32 v[108:109], v[108:109], v[146:147]
	v_pk_mul_f32 v[104:105], v[104:105], v[150:151]
	v_pk_mul_f32 v[100:101], v[100:101], v[146:147]
	v_pk_mul_f32 v[96:97], v[96:97], v[150:151]
	v_cvt_pk_fp8_f32 v154, v124, v125
	v_cvt_pk_fp8_f32 v155, v120, v121
	v_cvt_pk_fp8_f32 v156, v116, v117
	v_cvt_pk_fp8_f32 v157, v112, v113
	v_cvt_pk_fp8_f32 v163, v88, v89
	v_cvt_pk_fp8_f32 v79, v64, v65
	v_cvt_pk_fp8_f32 v158, v108, v109
	v_cvt_pk_fp8_f32 v159, v104, v105
	v_cvt_pk_fp8_f32 v160, v100, v101
	v_cvt_pk_fp8_f32 v161, v96, v97
	v_pk_mul_f32 v[88:89], v[94:95], v[148:149]
	v_pk_mul_f32 v[64:65], v[70:71], v[148:149]
	v_pk_mul_f32 v[126:127], v[126:127], v[148:149]
	v_pk_mul_f32 v[122:123], v[122:123], v[152:153]
	v_pk_mul_f32 v[118:119], v[118:119], v[148:149]
	v_pk_mul_f32 v[114:115], v[114:115], v[152:153]
	v_cvt_pk_fp8_f32 v162, v88, v89 op_sel:[0,0,1]
	v_pk_mul_f32 v[88:89], v[90:91], v[152:153]
	v_cvt_pk_fp8_f32 v76, v72, v73 op_sel:[0,0,1]
	v_pk_mul_f32 v[72:73], v[74:75], v[152:153]
	v_cvt_pk_fp8_f32 v78, v64, v65 op_sel:[0,0,1]
	v_pk_mul_f32 v[64:65], v[66:67], v[152:153]
	v_pk_mul_f32 v[110:111], v[110:111], v[148:149]
	v_pk_mul_f32 v[106:107], v[106:107], v[152:153]
	v_pk_mul_f32 v[102:103], v[102:103], v[148:149]
	v_pk_mul_f32 v[98:99], v[98:99], v[152:153]
	v_cvt_pk_fp8_f32 v154, v126, v127 op_sel:[0,0,1]
	v_cvt_pk_fp8_f32 v155, v122, v123 op_sel:[0,0,1]
	v_cvt_pk_fp8_f32 v156, v118, v119 op_sel:[0,0,1]
	v_cvt_pk_fp8_f32 v157, v114, v115 op_sel:[0,0,1]
	v_cvt_pk_fp8_f32 v163, v88, v89 op_sel:[0,0,1]
	v_cvt_pk_fp8_f32 v77, v72, v73 op_sel:[0,0,1]
	v_cvt_pk_fp8_f32 v79, v64, v65 op_sel:[0,0,1]
	v_cvt_pk_fp8_f32 v158, v110, v111 op_sel:[0,0,1]
	v_cvt_pk_fp8_f32 v159, v106, v107 op_sel:[0,0,1]
	v_cvt_pk_fp8_f32 v160, v102, v103 op_sel:[0,0,1]
	v_cvt_pk_fp8_f32 v161, v98, v99 op_sel:[0,0,1]
	v_add_co_u32_e32 v80, vcc, s47, v134
	v_permlane32_swap_b32_e32 v154, v156
	s_nop 0
	v_addc_co_u32_e32 v81, vcc, 0, v135, vcc
	v_permlane32_swap_b32_e32 v155, v157
	v_permlane32_swap_b32_e32 v162, v164
	v_permlane32_swap_b32_e32 v163, v165
	v_permlane32_swap_b32_e32 v76, v78
	v_permlane32_swap_b32_e32 v77, v79
	v_add_co_u32_e32 v82, vcc, s48, v134
	v_permlane32_swap_b32_e32 v158, v160
	v_permlane32_swap_b32_e32 v159, v161
	v_permlane16_swap_b32_e32 v154, v155
	v_permlane16_swap_b32_e32 v156, v157
	v_permlane16_swap_b32_e32 v162, v163
	v_permlane16_swap_b32_e32 v164, v165
	v_permlane16_swap_b32_e32 v76, v77
	v_permlane16_swap_b32_e32 v78, v79
	v_addc_co_u32_e32 v83, vcc, 0, v135, vcc
	v_permlane16_swap_b32_e32 v158, v159
	v_permlane16_swap_b32_e32 v160, v161
	global_store_dwordx4 v[134:135], v[154:157], off
	global_store_dwordx4 v[136:137], v[158:161], off
	global_store_dwordx4 v[80:81], v[162:165], off
	global_store_dwordx4 v[82:83], v[76:79], off
	global_load_dwordx4 v[64:67], v[132:133], off offset:512
	global_load_dwordx4 v[68:71], v[132:133], off offset:576
	v_mov_b32_e32 v75, v129
	v_mov_b32_e32 v72, v129
	v_mov_b32_e32 v73, v129
	v_mov_b32_e32 v74, v129
	s_and_b64 vcc, exec, s[4:5]
	s_waitcnt vmcnt(0)
	v_pk_mul_f32 v[64:65], v[64:65], s[8:9] op_sel_hi:[1,0]
	v_pk_mul_f32 v[68:69], v[68:69], s[8:9] op_sel_hi:[1,0]
	v_pk_mul_f32 v[70:71], v[70:71], s[8:9] op_sel_hi:[1,0]
	v_pk_mul_f32 v[48:49], v[48:49], v[68:69]
	v_pk_mul_f32 v[66:67], v[66:67], s[8:9] op_sel_hi:[1,0]
	v_cvt_pk_fp8_f32 v75, v48, v49
	v_pk_mul_f32 v[48:49], v[50:51], v[70:71]
	v_pk_mul_f32 v[40:41], v[40:41], v[68:69]
	v_pk_mul_f32 v[36:37], v[36:37], v[64:65]
	v_cvt_pk_fp8_f32 v75, v48, v49 op_sel:[0,0,1]
	v_pk_mul_f32 v[48:49], v[44:45], v[64:65]
	v_mov_b32_e32 v45, v129
	v_cvt_pk_fp8_f32 v45, v40, v41
	v_pk_mul_f32 v[40:41], v[46:47], v[66:67]
	v_mov_b32_e32 v46, v129
	v_cvt_pk_fp8_f32 v46, v36, v37
	v_pk_mul_f32 v[32:33], v[32:33], v[68:69]
	v_mov_b32_e32 v47, v129
	v_cvt_pk_fp8_f32 v47, v32, v33
	v_pk_mul_f32 v[32:33], v[38:39], v[66:67]
	v_pk_mul_f32 v[24:25], v[24:25], v[68:69]
	v_cvt_pk_fp8_f32 v46, v32, v33 op_sel:[0,0,1]
	v_pk_mul_f32 v[32:33], v[34:35], v[70:71]
	v_pk_mul_f32 v[20:21], v[20:21], v[64:65]
	v_cvt_pk_fp8_f32 v47, v32, v33 op_sel:[0,0,1]
	v_pk_mul_f32 v[32:33], v[28:29], v[64:65]
	v_mov_b32_e32 v29, v129
	v_cvt_pk_fp8_f32 v29, v24, v25
	v_pk_mul_f32 v[24:25], v[30:31], v[66:67]
	v_mov_b32_e32 v30, v129
	v_cvt_pk_fp8_f32 v30, v20, v21
	v_pk_mul_f32 v[16:17], v[16:17], v[68:69]
	v_mov_b32_e32 v31, v129
	v_cvt_pk_fp8_f32 v31, v16, v17
	v_pk_mul_f32 v[16:17], v[22:23], v[66:67]
	v_mov_b32_e32 v28, v129
	v_cvt_pk_fp8_f32 v30, v16, v17 op_sel:[0,0,1]
	v_pk_mul_f32 v[16:17], v[18:19], v[70:71]
	v_pk_mul_f32 v[8:9], v[8:9], v[68:69]
	v_cvt_pk_fp8_f32 v31, v16, v17 op_sel:[0,0,1]
	v_pk_mul_f32 v[16:17], v[12:13], v[64:65]
	v_mov_b32_e32 v13, v129
	v_pk_mul_f32 v[60:61], v[60:61], v[64:65]
	v_pk_mul_f32 v[56:57], v[56:57], v[68:69]
	v_pk_mul_f32 v[52:53], v[52:53], v[64:65]
	v_mov_b32_e32 v44, v129
	v_cvt_pk_fp8_f32 v28, v32, v33
	v_mov_b32_e32 v12, v129
	v_cvt_pk_fp8_f32 v13, v8, v9
	v_pk_mul_f32 v[8:9], v[14:15], v[66:67]
	v_pk_mul_f32 v[4:5], v[4:5], v[64:65]
	v_mov_b32_e32 v14, v129
	v_cvt_pk_fp8_f32 v72, v60, v61
	v_cvt_pk_fp8_f32 v73, v56, v57
	v_cvt_pk_fp8_f32 v74, v52, v53
	v_cvt_pk_fp8_f32 v44, v48, v49
	v_cvt_pk_fp8_f32 v12, v16, v17
	v_cvt_pk_fp8_f32 v14, v4, v5
	v_pk_mul_f32 v[0:1], v[0:1], v[68:69]
	v_mov_b32_e32 v15, v129
	v_cvt_pk_fp8_f32 v15, v0, v1
	v_pk_mul_f32 v[62:63], v[62:63], v[66:67]
	v_pk_mul_f32 v[58:59], v[58:59], v[70:71]
	v_pk_mul_f32 v[54:55], v[54:55], v[66:67]
	v_cvt_pk_fp8_f32 v28, v24, v25 op_sel:[0,0,1]
	v_pk_mul_f32 v[24:25], v[26:27], v[70:71]
	v_pk_mul_f32 v[0:1], v[6:7], v[66:67]
	v_cvt_pk_fp8_f32 v72, v62, v63 op_sel:[0,0,1]
	v_cvt_pk_fp8_f32 v73, v58, v59 op_sel:[0,0,1]
	v_cvt_pk_fp8_f32 v74, v54, v55 op_sel:[0,0,1]
	v_cvt_pk_fp8_f32 v44, v40, v41 op_sel:[0,0,1]
	v_pk_mul_f32 v[40:41], v[42:43], v[70:71]
	v_cvt_pk_fp8_f32 v29, v24, v25 op_sel:[0,0,1]
	v_cvt_pk_fp8_f32 v12, v8, v9 op_sel:[0,0,1]
	v_pk_mul_f32 v[8:9], v[10:11], v[70:71]
	v_cvt_pk_fp8_f32 v14, v0, v1 op_sel:[0,0,1]
	v_pk_mul_f32 v[0:1], v[2:3], v[70:71]
	v_cvt_pk_fp8_f32 v45, v40, v41 op_sel:[0,0,1]
	v_cvt_pk_fp8_f32 v13, v8, v9 op_sel:[0,0,1]
	v_cvt_pk_fp8_f32 v15, v0, v1 op_sel:[0,0,1]
	v_permlane32_swap_b32_e32 v72, v74
	v_permlane32_swap_b32_e32 v73, v75
	v_permlane32_swap_b32_e32 v28, v30
	v_permlane32_swap_b32_e32 v29, v31
	v_permlane16_swap_b32_e32 v72, v73
	v_permlane16_swap_b32_e32 v74, v75
	v_permlane32_swap_b32_e32 v44, v46
	v_permlane32_swap_b32_e32 v45, v47
	v_permlane16_swap_b32_e32 v28, v29
	v_permlane16_swap_b32_e32 v30, v31
	v_permlane32_swap_b32_e32 v12, v14
	v_permlane32_swap_b32_e32 v13, v15
	v_permlane16_swap_b32_e32 v44, v45
	v_permlane16_swap_b32_e32 v46, v47
	global_store_dwordx4 v[134:135], v[72:75], off offset:128
	global_store_dwordx4 v[136:137], v[44:47], off offset:128
	v_permlane16_swap_b32_e32 v12, v13
	v_permlane16_swap_b32_e32 v14, v15
	global_store_dwordx4 v[80:81], v[28:31], off offset:128
	global_store_dwordx4 v[82:83], v[12:15], off offset:128
	s_cbranch_vccz .LBB0_4925
	s_waitcnt vmcnt(0)
	v_readlane_b32 s0, v252, 2
	s_cmpk_gt_u32 s0, 0xff
	s_cbranch_scc1 .LBB0_4936
	s_barrier

.Lpeel_9:
	ds_read_b128 v[140:143], v134
	ds_read_b128 v[144:147], v134 offset:1024
	ds_read_b128 v[148:151], v134 offset:2048
	ds_read_b128 v[152:155], v134 offset:3072
	s_add_u32 s16, s14, 0xfffd0080
	s_addc_u32 s17, s15, -1
	s_cmp_eq_u32 s53, 8
	s_cselect_b32 s19, s13, s17
	s_cselect_b32 s18, s12, s16
	s_cselect_b32 s17, s11, s52
	s_cselect_b32 s16, s10, s51
	v_mov_b32_e32 v128, v132
	ds_read_b128 v[156:159], v135
	ds_read_b128 v[160:163], v135 offset:1024
	ds_read_b128 v[164:167], v135 offset:2048
	ds_read_b128 v[168:171], v135 offset:3072
	ds_read_b128 v[172:175], v135 offset:4096
	ds_read_b128 v[176:179], v135 offset:5120
	ds_read_b128 v[180:183], v135 offset:6144
	ds_read_b128 v[184:187], v135 offset:7168
	s_nop 0
	v_mov_b32_e32 v128, v133
	s_nop 0
	s_waitcnt lgkmcnt(8)
	s_barrier
	s_waitcnt lgkmcnt(0)
	s_setprio 1
	s_waitcnt lgkmcnt(0)
	v_mfma_scale_f32_16x16x128_f8f6f4 v[124:127], v[140:147], v[156:163], 0, v136, v136 op_sel_hi:[0,0,0]
	v_mfma_scale_f32_16x16x128_f8f6f4 v[120:123], v[148:155], v[156:163], 0, v136, v136 op_sel_hi:[0,0,0]
	s_mov_b32 m0, s38
	v_mfma_scale_f32_16x16x128_f8f6f4 v[116:119], v[140:147], v[164:171], 0, v136, v136 op_sel_hi:[0,0,0]
	global_load_lds_dwordx4 v132, s[14:15]
	v_mfma_scale_f32_16x16x128_f8f6f4 v[112:115], v[148:155], v[164:171], 0, v136, v136 op_sel_hi:[0,0,0]
	v_mfma_scale_f32_16x16x128_f8f6f4 v[188:191], v[140:147], v[172:179], 0, v136, v136 op_sel_hi:[0,0,0]
	s_mov_b32 m0, s39
	v_mfma_scale_f32_16x16x128_f8f6f4 v[192:195], v[148:155], v[172:179], 0, v136, v136 op_sel_hi:[0,0,0]
	global_load_lds_dwordx4 v133, s[14:15]
	v_mfma_scale_f32_16x16x128_f8f6f4 v[196:199], v[140:147], v[180:187], 0, v136, v136 op_sel_hi:[0,0,0]
	v_mfma_scale_f32_16x16x128_f8f6f4 v[200:203], v[148:155], v[180:187], 0, v136, v136 op_sel_hi:[0,0,0]
	s_setprio 0
	s_barrier
	v_mov_b32_e32 v128, v132
	s_nop 2
	ds_read_b128 v[96:99], v137
	ds_read_b128 v[100:103], v137 offset:1024
	ds_read_b128 v[104:107], v137 offset:2048
	ds_read_b128 v[108:111], v137 offset:3072
	s_nop 0
	v_mov_b32_e32 v128, v133
	s_nop 0
	s_barrier
	s_waitcnt lgkmcnt(0)
	s_setprio 1
	s_waitcnt lgkmcnt(0)
	v_mfma_scale_f32_16x16x128_f8f6f4 v[204:207], v[96:103], v[156:163], 0, v136, v136 op_sel_hi:[0,0,0]
	v_mfma_scale_f32_16x16x128_f8f6f4 v[156:159], v[104:111], v[156:163], 0, v136, v136 op_sel_hi:[0,0,0]
	s_mov_b32 m0, s40
	v_mfma_scale_f32_16x16x128_f8f6f4 v[160:163], v[96:103], v[164:171], 0, v136, v136 op_sel_hi:[0,0,0]
	global_load_lds_dwordx4 v132, s[16:17]
	v_mfma_scale_f32_16x16x128_f8f6f4 v[164:167], v[104:111], v[164:171], 0, v136, v136 op_sel_hi:[0,0,0]
	v_mfma_scale_f32_16x16x128_f8f6f4 v[168:171], v[96:103], v[172:179], 0, v136, v136 op_sel_hi:[0,0,0]
	s_mov_b32 m0, s41
	v_mfma_scale_f32_16x16x128_f8f6f4 v[172:175], v[104:111], v[172:179], 0, v136, v136 op_sel_hi:[0,0,0]
	global_load_lds_dwordx4 v133, s[16:17]
	v_mfma_scale_f32_16x16x128_f8f6f4 v[176:179], v[96:103], v[180:187], 0, v136, v136 op_sel_hi:[0,0,0]
	v_mfma_scale_f32_16x16x128_f8f6f4 v[180:183], v[104:111], v[180:187], 0, v136, v136 op_sel_hi:[0,0,0]
	s_setprio 0
	v_mov_b32_e32 v128, v132
	s_barrier
	s_nop 2
	ds_read_b128 v[64:67], v135 offset:16384
	ds_read_b128 v[68:71], v135 offset:17408
	ds_read_b128 v[72:75], v135 offset:18432
	ds_read_b128 v[76:79], v135 offset:19456
	ds_read_b128 v[80:83], v135 offset:20480
	ds_read_b128 v[84:87], v135 offset:21504
	ds_read_b128 v[88:91], v135 offset:22528
	ds_read_b128 v[92:95], v135 offset:23552
	s_nop 0
	v_mov_b32_e32 v128, v133
	s_nop 0
	s_barrier
	s_waitcnt lgkmcnt(0)
	s_setprio 1
	s_waitcnt lgkmcnt(0)
	v_mfma_scale_f32_16x16x128_f8f6f4 v[60:63], v[140:147], v[64:71], 0, v136, v136 op_sel_hi:[0,0,0]
	v_mfma_scale_f32_16x16x128_f8f6f4 v[56:59], v[148:155], v[64:71], 0, v136, v136 op_sel_hi:[0,0,0]
	s_mov_b32 m0, s24
	v_mfma_scale_f32_16x16x128_f8f6f4 v[52:55], v[140:147], v[72:79], 0, v136, v136 op_sel_hi:[0,0,0]
	global_load_lds_dwordx4 v132, s[18:19]
	v_mfma_scale_f32_16x16x128_f8f6f4 v[48:51], v[148:155], v[72:79], 0, v136, v136 op_sel_hi:[0,0,0]
	v_mfma_scale_f32_16x16x128_f8f6f4 v[184:187], v[140:147], v[80:87], 0, v136, v136 op_sel_hi:[0,0,0]
	s_mov_b32 m0, s25
	v_mfma_scale_f32_16x16x128_f8f6f4 v[208:211], v[148:155], v[80:87], 0, v136, v136 op_sel_hi:[0,0,0]
	global_load_lds_dwordx4 v133, s[18:19]
	v_mfma_scale_f32_16x16x128_f8f6f4 v[212:215], v[140:147], v[88:95], 0, v136, v136 op_sel_hi:[0,0,0]
	v_mfma_scale_f32_16x16x128_f8f6f4 v[216:219], v[148:155], v[88:95], 0, v136, v136 op_sel_hi:[0,0,0]
	s_setprio 0
	s_barrier
	s_add_u32 s54, s16, 0x30000
	s_nop 3
	v_mov_b32_e32 v32, v132
	s_addc_u32 s55, s17, 0
	s_nop 0
	v_mov_b32_e32 v32, v133
	s_nop 0
	s_waitcnt vmcnt(4)
	s_barrier
	s_setprio 1
	v_mfma_scale_f32_16x16x128_f8f6f4 v[220:223], v[96:103], v[64:71], 0, v136, v136 op_sel_hi:[0,0,0]
	v_mfma_scale_f32_16x16x128_f8f6f4 v[224:227], v[104:111], v[64:71], 0, v136, v136 op_sel_hi:[0,0,0]
	s_mov_b32 m0, s42
	v_mfma_scale_f32_16x16x128_f8f6f4 v[228:231], v[96:103], v[72:79], 0, v136, v136 op_sel_hi:[0,0,0]
	global_load_lds_dwordx4 v132, s[54:55]
	v_mfma_scale_f32_16x16x128_f8f6f4 v[232:235], v[104:111], v[72:79], 0, v136, v136 op_sel_hi:[0,0,0]
	v_mfma_scale_f32_16x16x128_f8f6f4 v[236:239], v[96:103], v[80:87], 0, v136, v136 op_sel_hi:[0,0,0]
	s_mov_b32 m0, s43
	v_mfma_scale_f32_16x16x128_f8f6f4 v[240:243], v[104:111], v[80:87], 0, v136, v136 op_sel_hi:[0,0,0]
	global_load_lds_dwordx4 v133, s[54:55]
	v_mfma_scale_f32_16x16x128_f8f6f4 v[244:247], v[96:103], v[88:95], 0, v136, v136 op_sel_hi:[0,0,0]
	v_mfma_scale_f32_16x16x128_f8f6f4 v[248:251], v[104:111], v[88:95], 0, v136, v136 op_sel_hi:[0,0,0]
	s_setprio 0
	s_barrier
	s_nop 4
	ds_read_b128 v[0:3], v138
	ds_read_b128 v[4:7], v138 offset:1024
	ds_read_b128 v[8:11], v138 offset:2048
	ds_read_b128 v[12:15], v138 offset:3072
	s_add_u32 s54, s18, 0x30000
	v_mov_b32_e32 v64, v132
	ds_read_b128 v[16:19], v135 offset:32768
	ds_read_b128 v[20:23], v135 offset:33792
	ds_read_b128 v[24:27], v135 offset:34816
	ds_read_b128 v[28:31], v135 offset:35840
	ds_read_b128 v[32:35], v135 offset:36864
	ds_read_b128 v[36:39], v135 offset:37888
	ds_read_b128 v[40:43], v135 offset:38912
	ds_read_b128 v[44:47], v135 offset:39936
	s_addc_u32 s55, s19, 0
	s_nop 0
	v_mov_b32_e32 v64, v133
	s_nop 0
	s_waitcnt lgkmcnt(8)
	s_barrier
	s_waitcnt lgkmcnt(0)
	s_setprio 1
	s_waitcnt lgkmcnt(0)
	v_mfma_scale_f32_16x16x128_f8f6f4 v[124:127], v[0:7], v[16:23], v[124:127], v136, v136 op_sel_hi:[0,0,0]
	v_mfma_scale_f32_16x16x128_f8f6f4 v[120:123], v[8:15], v[16:23], v[120:123], v136, v136 op_sel_hi:[0,0,0]
	s_mov_b32 m0, s26
	v_mfma_scale_f32_16x16x128_f8f6f4 v[116:119], v[0:7], v[24:31], v[116:119], v136, v136 op_sel_hi:[0,0,0]
	global_load_lds_dwordx4 v132, s[54:55]
	v_mfma_scale_f32_16x16x128_f8f6f4 v[112:115], v[8:15], v[24:31], v[112:115], v136, v136 op_sel_hi:[0,0,0]
	v_mfma_scale_f32_16x16x128_f8f6f4 v[108:111], v[0:7], v[32:39], v[188:191], v136, v136 op_sel_hi:[0,0,0]
	s_mov_b32 m0, s27
	v_mfma_scale_f32_16x16x128_f8f6f4 v[104:107], v[8:15], v[32:39], v[192:195], v136, v136 op_sel_hi:[0,0,0]
	global_load_lds_dwordx4 v133, s[54:55]
	v_mfma_scale_f32_16x16x128_f8f6f4 v[100:103], v[0:7], v[40:47], v[196:199], v136, v136 op_sel_hi:[0,0,0]
	v_mfma_scale_f32_16x16x128_f8f6f4 v[96:99], v[8:15], v[40:47], v[200:203], v136, v136 op_sel_hi:[0,0,0]
	s_setprio 0
	s_barrier
	v_mov_b32_e32 v128, v132
	ds_read_b128 v[140:143], v139
	ds_read_b128 v[144:147], v139 offset:1024
	ds_read_b128 v[148:151], v139 offset:2048
	ds_read_b128 v[152:155], v139 offset:3072
	v_lshl_add_u64 v[64:65], s[16:17], 0, v[128:129]
	v_lshl_add_u64 v[64:65], v[64:65], 0, s[4:5]
	v_mov_b32_e32 v128, v133
	v_lshl_add_u64 v[64:65], s[16:17], 0, v[128:129]
	v_lshl_add_u64 v[64:65], v[64:65], 0, s[4:5]
	s_barrier
	s_waitcnt lgkmcnt(0)
	s_setprio 1
	s_waitcnt lgkmcnt(0)
	v_mfma_scale_f32_16x16x128_f8f6f4 v[92:95], v[140:147], v[16:23], v[204:207], v136, v136 op_sel_hi:[0,0,0]
	v_mfma_scale_f32_16x16x128_f8f6f4 v[88:91], v[148:155], v[16:23], v[156:159], v136, v136 op_sel_hi:[0,0,0]
	s_add_u32 s98, s16, s4
	s_addc_u32 s99, s17, s5
	s_mov_b32 m0, s45
	v_mfma_scale_f32_16x16x128_f8f6f4 v[84:87], v[140:147], v[24:31], v[160:163], v136, v136 op_sel_hi:[0,0,0]
	global_load_lds_dwordx4 v132, s[98:99]
	v_mfma_scale_f32_16x16x128_f8f6f4 v[80:83], v[148:155], v[24:31], v[164:167], v136, v136 op_sel_hi:[0,0,0]
	v_mfma_scale_f32_16x16x128_f8f6f4 v[76:79], v[140:147], v[32:39], v[168:171], v136, v136 op_sel_hi:[0,0,0]
	s_mov_b32 m0, s46
	v_mfma_scale_f32_16x16x128_f8f6f4 v[72:75], v[148:155], v[32:39], v[172:175], v136, v136 op_sel_hi:[0,0,0]
	global_load_lds_dwordx4 v133, s[98:99]
	v_mfma_scale_f32_16x16x128_f8f6f4 v[68:71], v[140:147], v[40:47], v[176:179], v136, v136 op_sel_hi:[0,0,0]
	v_mfma_scale_f32_16x16x128_f8f6f4 v[64:67], v[148:155], v[40:47], v[180:183], v136, v136 op_sel_hi:[0,0,0]
	s_setprio 0
	v_mov_b32_e32 v128, v132
	s_barrier
	ds_read_b128 v[16:19], v135 offset:49152
	ds_read_b128 v[20:23], v135 offset:50176
	ds_read_b128 v[156:159], v135 offset:51200
	ds_read_b128 v[160:163], v135 offset:52224
	ds_read_b128 v[164:167], v135 offset:53248
	ds_read_b128 v[168:171], v135 offset:54272
	ds_read_b128 v[172:175], v135 offset:55296
	ds_read_b128 v[176:179], v135 offset:56320
	v_lshl_add_u64 v[24:25], s[18:19], 0, v[128:129]
	v_lshl_add_u64 v[24:25], v[24:25], 0, s[4:5]
	v_mov_b32_e32 v128, v133
	v_lshl_add_u64 v[24:25], s[18:19], 0, v[128:129]
	v_lshl_add_u64 v[24:25], v[24:25], 0, s[4:5]
	s_barrier
	s_waitcnt lgkmcnt(0)
	s_setprio 1
	s_waitcnt lgkmcnt(0)
	v_mfma_scale_f32_16x16x128_f8f6f4 v[60:63], v[0:7], v[16:23], v[60:63], v136, v136 op_sel_hi:[0,0,0]
	v_mfma_scale_f32_16x16x128_f8f6f4 v[56:59], v[8:15], v[16:23], v[56:59], v136, v136 op_sel_hi:[0,0,0]
	s_add_u32 s98, s18, s4
	s_addc_u32 s99, s19, s5
	s_mov_b32 m0, s35
	v_mfma_scale_f32_16x16x128_f8f6f4 v[52:55], v[0:7], v[156:163], v[52:55], v136, v136 op_sel_hi:[0,0,0]
	global_load_lds_dwordx4 v132, s[98:99]
	v_mfma_scale_f32_16x16x128_f8f6f4 v[48:51], v[8:15], v[156:163], v[48:51], v136, v136 op_sel_hi:[0,0,0]
	v_mfma_scale_f32_16x16x128_f8f6f4 v[44:47], v[0:7], v[164:171], v[184:187], v136, v136 op_sel_hi:[0,0,0]
	s_mov_b32 m0, s36
	v_mfma_scale_f32_16x16x128_f8f6f4 v[40:43], v[8:15], v[164:171], v[208:211], v136, v136 op_sel_hi:[0,0,0]
	global_load_lds_dwordx4 v133, s[98:99]
	v_mfma_scale_f32_16x16x128_f8f6f4 v[36:39], v[0:7], v[172:179], v[212:215], v136, v136 op_sel_hi:[0,0,0]
	v_mfma_scale_f32_16x16x128_f8f6f4 v[32:35], v[8:15], v[172:179], v[216:219], v136, v136 op_sel_hi:[0,0,0]
	s_setprio 0
	s_barrier
	s_add_u32 s16, s16, 0x30080
	s_addc_u32 s17, s17, 0
	v_mov_b32_e32 v0, v132
	s_add_i32 s18, s44, s23
	s_nop 0
	v_mov_b32_e32 v0, v133
	s_nop 0
	s_waitcnt vmcnt(4)
	s_barrier
	s_setprio 1
	v_mfma_scale_f32_16x16x128_f8f6f4 v[28:31], v[140:147], v[16:23], v[220:223], v136, v136 op_sel_hi:[0,0,0]
	v_mfma_scale_f32_16x16x128_f8f6f4 v[24:27], v[148:155], v[16:23], v[224:227], v136, v136 op_sel_hi:[0,0,0]
	s_mov_b32 m0, s18
	v_mfma_scale_f32_16x16x128_f8f6f4 v[20:23], v[140:147], v[156:163], v[228:231], v136, v136 op_sel_hi:[0,0,0]
	global_load_lds_dwordx4 v132, s[16:17]
	v_mfma_scale_f32_16x16x128_f8f6f4 v[16:19], v[148:155], v[156:163], v[232:235], v136, v136 op_sel_hi:[0,0,0]
	v_mfma_scale_f32_16x16x128_f8f6f4 v[12:15], v[140:147], v[164:171], v[236:239], v136, v136 op_sel_hi:[0,0,0]
	s_add_i32 m0, s18, 0x2000
	v_mfma_scale_f32_16x16x128_f8f6f4 v[8:11], v[148:155], v[164:171], v[240:243], v136, v136 op_sel_hi:[0,0,0]
	global_load_lds_dwordx4 v133, s[16:17]
	v_mfma_scale_f32_16x16x128_f8f6f4 v[4:7], v[140:147], v[172:179], v[244:247], v136, v136 op_sel_hi:[0,0,0]
	v_mfma_scale_f32_16x16x128_f8f6f4 v[0:3], v[148:155], v[172:179], v[248:251], v136, v136 op_sel_hi:[0,0,0]
	s_setprio 0
	s_add_i32 s53, s53, 2
	s_add_u32 s14, s14, 0x100
	s_addc_u32 s15, s15, 0
	s_add_u32 s51, s51, 0x100
	s_addc_u32 s52, s52, 0
	s_cmp_gt_u32 s53, 9
	s_barrier
	s_cbranch_scc0 .LBB0_5813
	s_branch .Lpeel_exit_9

.Lpeel_exit_9:
	v_pk_mul_f32 v[140:141], v[124:125], s[6:7] op_sel_hi:[1,0]
	v_pk_mul_f32 v[120:121], v[120:121], s[6:7] op_sel_hi:[1,0]
	v_mov_b32_e32 v125, v129
	v_cvt_pk_fp8_f32 v125, v120, v121
	v_pk_mul_f32 v[120:121], v[126:127], s[6:7] op_sel_hi:[1,0]
	v_pk_mul_f32 v[116:117], v[116:117], s[6:7] op_sel_hi:[1,0]
	v_mov_b32_e32 v126, v129
	v_cvt_pk_fp8_f32 v126, v116, v117
	v_pk_mul_f32 v[112:113], v[112:113], s[6:7] op_sel_hi:[1,0]
	v_mov_b32_e32 v127, v129
	v_cvt_pk_fp8_f32 v127, v112, v113
	v_pk_mul_f32 v[112:113], v[118:119], s[6:7] op_sel_hi:[1,0]
	v_pk_mul_f32 v[104:105], v[104:105], s[6:7] op_sel_hi:[1,0]
	v_cvt_pk_fp8_f32 v126, v112, v113 op_sel:[0,0,1]
	v_pk_mul_f32 v[112:113], v[114:115], s[6:7] op_sel_hi:[1,0]
	v_pk_mul_f32 v[100:101], v[100:101], s[6:7] op_sel_hi:[1,0]
	v_cvt_pk_fp8_f32 v127, v112, v113 op_sel:[0,0,1]
	v_pk_mul_f32 v[112:113], v[108:109], s[6:7] op_sel_hi:[1,0]
	v_mov_b32_e32 v109, v129
	v_cvt_pk_fp8_f32 v109, v104, v105
	v_pk_mul_f32 v[104:105], v[110:111], s[6:7] op_sel_hi:[1,0]
	v_mov_b32_e32 v110, v129
	v_cvt_pk_fp8_f32 v110, v100, v101
	v_pk_mul_f32 v[100:101], v[92:93], s[6:7] op_sel_hi:[1,0]
	v_pk_mul_f32 v[88:89], v[88:89], s[6:7] op_sel_hi:[1,0]
	v_mov_b32_e32 v93, v129
	v_cvt_pk_fp8_f32 v93, v88, v89
	v_pk_mul_f32 v[88:89], v[94:95], s[6:7] op_sel_hi:[1,0]
	v_pk_mul_f32 v[84:85], v[84:85], s[6:7] op_sel_hi:[1,0]
	v_mov_b32_e32 v94, v129
	v_cvt_pk_fp8_f32 v94, v84, v85
	v_pk_mul_f32 v[80:81], v[80:81], s[6:7] op_sel_hi:[1,0]
	v_mov_b32_e32 v95, v129
	v_cvt_pk_fp8_f32 v95, v80, v81
	v_pk_mul_f32 v[80:81], v[86:87], s[6:7] op_sel_hi:[1,0]
	v_pk_mul_f32 v[72:73], v[72:73], s[6:7] op_sel_hi:[1,0]
	v_cvt_pk_fp8_f32 v94, v80, v81 op_sel:[0,0,1]
	v_pk_mul_f32 v[80:81], v[82:83], s[6:7] op_sel_hi:[1,0]
	v_pk_mul_f32 v[68:69], v[68:69], s[6:7] op_sel_hi:[1,0]
	v_cvt_pk_fp8_f32 v95, v80, v81 op_sel:[0,0,1]
	v_pk_mul_f32 v[80:81], v[76:77], s[6:7] op_sel_hi:[1,0]
	v_mov_b32_e32 v77, v129
	v_cvt_pk_fp8_f32 v77, v72, v73
	v_pk_mul_f32 v[72:73], v[78:79], s[6:7] op_sel_hi:[1,0]
	v_mov_b32_e32 v78, v129
	v_cvt_pk_fp8_f32 v78, v68, v69
	v_pk_mul_f32 v[64:65], v[64:65], s[6:7] op_sel_hi:[1,0]
	v_mov_b32_e32 v79, v129
	v_cvt_pk_fp8_f32 v79, v64, v65
	v_pk_mul_f32 v[64:65], v[70:71], s[6:7] op_sel_hi:[1,0]
	v_pk_mul_f32 v[56:57], v[56:57], s[6:7] op_sel_hi:[1,0]
	v_cvt_pk_fp8_f32 v78, v64, v65 op_sel:[0,0,1]
	v_pk_mul_f32 v[64:65], v[66:67], s[6:7] op_sel_hi:[1,0]
	v_pk_mul_f32 v[52:53], v[52:53], s[6:7] op_sel_hi:[1,0]
	v_cvt_pk_fp8_f32 v79, v64, v65 op_sel:[0,0,1]
	v_pk_mul_f32 v[64:65], v[60:61], s[6:7] op_sel_hi:[1,0]
	v_mov_b32_e32 v61, v129
	v_cvt_pk_fp8_f32 v61, v56, v57
	v_pk_mul_f32 v[56:57], v[62:63], s[6:7] op_sel_hi:[1,0]
	v_mov_b32_e32 v62, v129
	v_cvt_pk_fp8_f32 v62, v52, v53
	v_pk_mul_f32 v[48:49], v[48:49], s[6:7] op_sel_hi:[1,0]
	v_mov_b32_e32 v63, v129
	v_cvt_pk_fp8_f32 v63, v48, v49
	s_lshl_b32 s14, s49, 8
	v_pk_mul_f32 v[48:49], v[54:55], s[6:7] op_sel_hi:[1,0]
	s_add_i32 s14, s14, s33
	v_cvt_pk_fp8_f32 v62, v48, v49 op_sel:[0,0,1]
	v_pk_mul_f32 v[48:49], v[50:51], s[6:7] op_sel_hi:[1,0]
	s_lshl_b32 s16, s50, 8
	s_ashr_i32 s15, s14, 31
	v_cvt_pk_fp8_f32 v63, v48, v49 op_sel:[0,0,1]
	v_pk_mul_f32 v[48:49], v[44:45], s[6:7] op_sel_hi:[1,0]
	v_pk_mul_f32 v[40:41], v[40:41], s[6:7] op_sel_hi:[1,0]
	v_mov_b32_e32 v45, v129
	s_ashr_i32 s17, s16, 31
	s_lshl_b64 s[18:19], s[14:15], 11
	v_cvt_pk_fp8_f32 v45, v40, v41
	v_pk_mul_f32 v[40:41], v[46:47], s[6:7] op_sel_hi:[1,0]
	v_pk_mul_f32 v[36:37], v[36:37], s[6:7] op_sel_hi:[1,0]
	v_mov_b32_e32 v46, v129
	s_add_u32 s15, s30, s18
	v_cvt_pk_fp8_f32 v46, v36, v37
	v_pk_mul_f32 v[36:37], v[28:29], s[6:7] op_sel_hi:[1,0]
	v_pk_mul_f32 v[24:25], v[24:25], s[6:7] op_sel_hi:[1,0]
	v_mov_b32_e32 v29, v129
	s_addc_u32 s18, s31, s19
	v_cvt_pk_fp8_f32 v29, v24, v25
	v_pk_mul_f32 v[24:25], v[30:31], s[6:7] op_sel_hi:[1,0]
	v_pk_mul_f32 v[20:21], v[20:21], s[6:7] op_sel_hi:[1,0]
	v_mov_b32_e32 v30, v129
	s_add_u32 s15, s15, s16
	v_cvt_pk_fp8_f32 v30, v20, v21
	v_pk_mul_f32 v[16:17], v[16:17], s[6:7] op_sel_hi:[1,0]
	v_mov_b32_e32 v31, v129
	s_addc_u32 s19, s18, s17
	v_cvt_pk_fp8_f32 v31, v16, v17
	s_add_u32 s18, s15, s34
	s_addc_u32 s19, s19, 0
	s_addk_i32 s14, 0x80
	v_pk_mul_f32 v[16:17], v[22:23], s[6:7] op_sel_hi:[1,0]
	s_ashr_i32 s15, s14, 31
	v_cvt_pk_fp8_f32 v30, v16, v17 op_sel:[0,0,1]
	v_pk_mul_f32 v[16:17], v[18:19], s[6:7] op_sel_hi:[1,0]
	v_mov_b32_e32 v124, v129
	v_mov_b32_e32 v108, v129
	v_pk_mul_f32 v[96:97], v[96:97], s[6:7] op_sel_hi:[1,0]
	v_mov_b32_e32 v111, v129
	v_mov_b32_e32 v92, v129
	s_lshl_b64 s[14:15], s[14:15], 11
	v_mov_b32_e32 v60, v129
	v_mov_b32_e32 v44, v129
	v_mov_b32_e32 v28, v129
	v_cvt_pk_fp8_f32 v31, v16, v17 op_sel:[0,0,1]
	v_pk_mul_f32 v[16:17], v[12:13], s[6:7] op_sel_hi:[1,0]
	v_pk_mul_f32 v[8:9], v[8:9], s[6:7] op_sel_hi:[1,0]
	v_mov_b32_e32 v13, v129
	v_mbcnt_lo_u32_b32 v128, -1, 0
	v_mbcnt_hi_u32_b32 v128, -1, v128
	v_cvt_pk_fp8_f32 v124, v140, v141
	v_ashrrev_i32_e32 v130, 1, v128
	v_cvt_pk_fp8_f32 v108, v112, v113
	v_cvt_pk_fp8_f32 v111, v96, v97
	v_cvt_pk_fp8_f32 v92, v100, v101
	v_mov_b32_e32 v76, v129
	v_cvt_pk_fp8_f32 v60, v64, v65
	v_cvt_pk_fp8_f32 v44, v48, v49
	v_pk_mul_f32 v[32:33], v[32:33], s[6:7] op_sel_hi:[1,0]
	v_mov_b32_e32 v47, v129
	s_add_u32 s14, s30, s14
	v_cvt_pk_fp8_f32 v28, v36, v37
	v_mov_b32_e32 v12, v129
	v_cvt_pk_fp8_f32 v13, v8, v9
	v_pk_mul_f32 v[8:9], v[14:15], s[6:7] op_sel_hi:[1,0]
	v_pk_mul_f32 v[4:5], v[4:5], s[6:7] op_sel_hi:[1,0]
	v_mov_b32_e32 v14, v129
	v_bfi_b32 v130, -16, v130, v128
	v_cvt_pk_fp8_f32 v76, v80, v81
	v_cvt_pk_fp8_f32 v47, v32, v33
	s_addc_u32 s15, s31, s15
	v_cvt_pk_fp8_f32 v12, v16, v17
	v_cvt_pk_fp8_f32 v14, v4, v5
	v_pk_mul_f32 v[0:1], v[0:1], s[6:7] op_sel_hi:[1,0]
	v_mov_b32_e32 v15, v129
	v_ashrrev_i32_e32 v131, 31, v130
	v_pk_mul_f32 v[96:97], v[102:103], s[6:7] op_sel_hi:[1,0]
	s_add_u32 s14, s14, s16
	v_cvt_pk_fp8_f32 v15, v0, v1
	v_lshlrev_b64 v[130:131], 11, v[130:131]
	v_cvt_pk_fp8_f32 v110, v96, v97 op_sel:[0,0,1]
	v_pk_mul_f32 v[96:97], v[98:99], s[6:7] op_sel_hi:[1,0]
	v_pk_mul_f32 v[32:33], v[38:39], s[6:7] op_sel_hi:[1,0]
	s_addc_u32 s15, s15, s17
	v_and_b32_e32 v128, 16, v128
	v_cvt_pk_fp8_f32 v124, v120, v121 op_sel:[0,0,1]
	v_pk_mul_f32 v[120:121], v[122:123], s[6:7] op_sel_hi:[1,0]
	v_cvt_pk_fp8_f32 v108, v104, v105 op_sel:[0,0,1]
	v_pk_mul_f32 v[104:105], v[106:107], s[6:7] op_sel_hi:[1,0]
	v_cvt_pk_fp8_f32 v111, v96, v97 op_sel:[0,0,1]
	v_lshl_add_u64 v[96:97], s[18:19], 0, v[130:131]
	v_cvt_pk_fp8_f32 v92, v88, v89 op_sel:[0,0,1]
	v_pk_mul_f32 v[88:89], v[90:91], s[6:7] op_sel_hi:[1,0]
	v_cvt_pk_fp8_f32 v60, v56, v57 op_sel:[0,0,1]
	v_pk_mul_f32 v[56:57], v[58:59], s[6:7] op_sel_hi:[1,0]
	v_cvt_pk_fp8_f32 v44, v40, v41 op_sel:[0,0,1]
	v_pk_mul_f32 v[40:41], v[42:43], s[6:7] op_sel_hi:[1,0]
	v_cvt_pk_fp8_f32 v46, v32, v33 op_sel:[0,0,1]
	v_pk_mul_f32 v[32:33], v[34:35], s[6:7] op_sel_hi:[1,0]
	s_add_u32 s14, s14, s34
	v_cvt_pk_fp8_f32 v28, v24, v25 op_sel:[0,0,1]
	v_pk_mul_f32 v[24:25], v[26:27], s[6:7] op_sel_hi:[1,0]
	v_pk_mul_f32 v[0:1], v[6:7], s[6:7] op_sel_hi:[1,0]
	v_cvt_pk_fp8_f32 v125, v120, v121 op_sel:[0,0,1]
	v_cvt_pk_fp8_f32 v109, v104, v105 op_sel:[0,0,1]
	v_lshl_add_u64 v[96:97], v[96:97], 0, v[128:129]
	v_cvt_pk_fp8_f32 v93, v88, v89 op_sel:[0,0,1]
	v_cvt_pk_fp8_f32 v76, v72, v73 op_sel:[0,0,1]
	v_pk_mul_f32 v[72:73], v[74:75], s[6:7] op_sel_hi:[1,0]
	v_cvt_pk_fp8_f32 v61, v56, v57 op_sel:[0,0,1]
	v_cvt_pk_fp8_f32 v45, v40, v41 op_sel:[0,0,1]
	v_cvt_pk_fp8_f32 v47, v32, v33 op_sel:[0,0,1]
	s_addc_u32 s15, s15, 0
	v_cvt_pk_fp8_f32 v29, v24, v25 op_sel:[0,0,1]
	v_cvt_pk_fp8_f32 v12, v8, v9 op_sel:[0,0,1]
	v_pk_mul_f32 v[8:9], v[10:11], s[6:7] op_sel_hi:[1,0]
	v_cvt_pk_fp8_f32 v14, v0, v1 op_sel:[0,0,1]
	v_pk_mul_f32 v[0:1], v[2:3], s[6:7] op_sel_hi:[1,0]
	v_add_co_u32_e32 v98, vcc, s29, v96
	v_cvt_pk_fp8_f32 v77, v72, v73 op_sel:[0,0,1]
	v_lshl_add_u64 v[32:33], s[14:15], 0, v[130:131]
	v_cvt_pk_fp8_f32 v13, v8, v9 op_sel:[0,0,1]
	v_cvt_pk_fp8_f32 v15, v0, v1 op_sel:[0,0,1]
	v_addc_co_u32_e32 v99, vcc, 0, v97, vcc
	v_lshl_add_u64 v[32:33], v[32:33], 0, v[128:129]
	v_add_co_u32_e32 v34, vcc, s29, v32
	v_permlane32_swap_b32_e32 v124, v126
	v_permlane32_swap_b32_e32 v125, v127
	v_permlane32_swap_b32_e32 v108, v110
	v_permlane32_swap_b32_e32 v109, v111
	v_permlane32_swap_b32_e32 v92, v94
	v_permlane32_swap_b32_e32 v93, v95
	v_permlane32_swap_b32_e32 v60, v62
	v_permlane32_swap_b32_e32 v61, v63
	v_permlane32_swap_b32_e32 v44, v46
	v_permlane32_swap_b32_e32 v45, v47
	v_addc_co_u32_e32 v35, vcc, 0, v33, vcc
	v_permlane32_swap_b32_e32 v28, v30
	v_permlane32_swap_b32_e32 v29, v31
	v_permlane16_swap_b32_e32 v124, v125
	v_permlane16_swap_b32_e32 v126, v127
	v_permlane16_swap_b32_e32 v108, v109
	v_permlane16_swap_b32_e32 v110, v111
	v_permlane16_swap_b32_e32 v92, v93
	v_permlane16_swap_b32_e32 v94, v95
	v_permlane32_swap_b32_e32 v76, v78
	v_permlane32_swap_b32_e32 v77, v79
	v_permlane16_swap_b32_e32 v60, v61
	v_permlane16_swap_b32_e32 v62, v63
	v_permlane16_swap_b32_e32 v44, v45
	v_permlane16_swap_b32_e32 v46, v47
	v_permlane16_swap_b32_e32 v28, v29
	v_permlane16_swap_b32_e32 v30, v31
	v_permlane32_swap_b32_e32 v12, v14
	v_permlane32_swap_b32_e32 v13, v15
	s_and_b64 vcc, exec, s[8:9]
	s_mov_b32 s50, s48
	s_mov_b32 s49, s47
	s_mov_b64 s[16:17], s[10:11]
	s_mov_b64 s[14:15], s[12:13]
	global_store_dwordx4 v[96:97], v[124:127], off
	global_store_dwordx4 v[98:99], v[108:111], off
	v_permlane16_swap_b32_e32 v76, v77
	v_permlane16_swap_b32_e32 v78, v79
	global_store_dwordx4 v[96:97], v[92:95], off offset:128
	global_store_dwordx4 v[98:99], v[76:79], off offset:128
	global_store_dwordx4 v[32:33], v[60:63], off
	global_store_dwordx4 v[34:35], v[44:47], off
	v_permlane16_swap_b32_e32 v12, v13
	v_permlane16_swap_b32_e32 v14, v15
	global_store_dwordx4 v[32:33], v[28:31], off offset:128
	global_store_dwordx4 v[34:35], v[12:15], off offset:128
	s_cbranch_vccz .LBB0_5808
	s_waitcnt vmcnt(0)
	v_readlane_b32 s0, v252, 2
	s_cmpk_gt_u32 s0, 0xff
	s_cbranch_scc1 .LBB0_5817
	s_barrier
